# router phase LN1: gamma/beta vectors loaded once per 64-token block into spare registers (128 serialized per-row loads removed)
# speedup vs baseline: 1.0160x; 1.0026x over previous
; #define GAS __attribute__((address_space(1)))
; #define FLANE lane_id()
; __device__ __forceinline__ void p6_router(Frame& F) {
;     ...
;     for (int blk = F.vcu; blk < T / 64; blk += F.G) {
;         const int t0 = blk * 64;
;         {
;             v2u raw[8][8]; const int ln_ = FLANE;
; #pragma unroll
;             for (int rr = 0; rr < 8; ++rr) { const GAS v2u* xr = (const GAS v2u*)(z1 + (size_t)(t0 + F.wave * 8 + rr) * D) + ln_;
; #pragma unroll
;                 for (int j = 0; j < 8; ++j) raw[rr][j] = xr[64 * j]; }
;     ...
;                 for (int j = 0; j < 8; ++j) { const f32x4 g = *((const GAS f32x4*)F.ln1_g + FLANE + 64 * j), b = *((const GAS f32x4*)F.ln1_b + FLANE + 64 * j);
.LBB0_1481:
	v_mbcnt_lo_u32_b32 v190, -1, 0
	v_mbcnt_hi_u32_b32 v190, -1, v190
	v_lshlrev_b32_e32 v190, 4, v190
	v_add_u32_e32 v191, 0x1000, v190
	global_load_dwordx4 v[196:199], v190, s[12:13]
	global_load_dwordx4 v[228:231], v190, s[14:15]
	global_load_dwordx4 v[200:203], v190, s[12:13] offset:1024
	global_load_dwordx4 v[232:235], v190, s[14:15] offset:1024
	global_load_dwordx4 v[204:207], v190, s[12:13] offset:2048
	global_load_dwordx4 v[236:239], v190, s[14:15] offset:2048
	global_load_dwordx4 v[208:211], v190, s[12:13] offset:3072
	global_load_dwordx4 v[240:243], v190, s[14:15] offset:3072
	global_load_dwordx4 v[212:215], v191, s[12:13]
	global_load_dwordx4 v[244:247], v191, s[14:15]
	global_load_dwordx4 v[216:219], v191, s[12:13] offset:1024
	global_load_dwordx4 v[248:251], v191, s[14:15] offset:1024
	global_load_dwordx4 v[220:223], v191, s[12:13] offset:2048
	global_load_dwordx4 v[182:185], v191, s[14:15] offset:2048
	global_load_dwordx4 v[224:227], v191, s[12:13] offset:3072
	global_load_dwordx4 v[186:189], v191, s[14:15] offset:3072
	s_lshl_b32 s42, s84, 6
	s_add_i32 s6, s42, s65
	s_ashr_i32 s7, s6, 31
	s_lshl_b64 s[4:5], s[6:7], 12
	v_mbcnt_lo_u32_b32 v0, -1, 0
	v_mbcnt_hi_u32_b32 v0, -1, v0
	s_add_u32 s4, s16, s4
	v_ashrrev_i32_e32 v1, 31, v0
	s_addc_u32 s5, s17, s5
	v_lshlrev_b64 v[8:9], 3, v[0:1]
	v_lshl_add_u64 v[10:11], s[4:5], 0, v[8:9]
	global_load_dwordx2 v[6:7], v[10:11], off
	global_load_dwordx2 v[128:129], v[10:11], off offset:512
	global_load_dwordx2 v[126:127], v[10:11], off offset:1024
	global_load_dwordx2 v[124:125], v[10:11], off offset:1536
	global_load_dwordx2 v[4:5], v[10:11], off offset:2048
	global_load_dwordx2 v[0:1], v[10:11], off offset:2560
	global_load_dwordx2 v[2:3], v[10:11], off offset:3072
	global_load_dwordx2 v[136:137], v[10:11], off offset:3584
	v_cmp_lt_i32_e32 vcc, v160, v159
	s_or_b32 s4, s6, 1
	s_ashr_i32 s5, s4, 31
	v_cndmask_b32_e32 v32, v158, v160, vcc
	v_cmp_lt_i32_e32 vcc, v161, v159
	v_lshlrev_b32_e32 v170, 2, v32
	s_lshl_b64 s[4:5], s[4:5], 12
	v_cndmask_b32_e32 v32, v158, v161, vcc
	v_cmp_lt_i32_e32 vcc, v162, v159
	v_lshlrev_b32_e32 v171, 2, v32
	s_add_u32 s4, s16, s4
	v_cndmask_b32_e32 v32, v158, v162, vcc
	v_cmp_lt_i32_e32 vcc, v163, v159
	v_lshlrev_b32_e32 v172, 2, v32
	s_addc_u32 s5, s17, s5
	v_cndmask_b32_e32 v32, v158, v163, vcc
	v_cmp_lt_i32_e32 vcc, v164, v159
	v_lshlrev_b32_e32 v173, 2, v32
	v_lshl_add_u64 v[10:11], s[4:5], 0, v[8:9]
	v_cndmask_b32_e32 v32, v158, v164, vcc
	v_cmp_lt_i32_e32 vcc, v165, v159
	v_lshlrev_b32_e32 v174, 2, v32
	s_or_b32 s4, s6, 2
	v_cndmask_b32_e32 v32, v158, v165, vcc
	v_lshlrev_b32_e32 v175, 2, v32
	s_ashr_i32 s5, s4, 31
	s_lshl_b64 s[4:5], s[4:5], 12
	s_add_u32 s4, s16, s4
	s_addc_u32 s5, s17, s5
	global_load_dwordx2 v[120:121], v[10:11], off
	global_load_dwordx2 v[122:123], v[10:11], off offset:512
	global_load_dwordx2 v[118:119], v[10:11], off offset:1024
	global_load_dwordx2 v[116:117], v[10:11], off offset:1536
	global_load_dwordx2 v[114:115], v[10:11], off offset:2048
	global_load_dwordx2 v[112:113], v[10:11], off offset:2560
	global_load_dwordx2 v[110:111], v[10:11], off offset:3072
	global_load_dwordx2 v[108:109], v[10:11], off offset:3584
	v_lshl_add_u64 v[10:11], s[4:5], 0, v[8:9]
	s_or_b32 s4, s6, 3
	s_ashr_i32 s5, s4, 31
	s_lshl_b64 s[4:5], s[4:5], 12
	s_add_u32 s4, s16, s4
	s_addc_u32 s5, s17, s5
	global_load_dwordx2 v[104:105], v[10:11], off
	global_load_dwordx2 v[106:107], v[10:11], off offset:512
	global_load_dwordx2 v[102:103], v[10:11], off offset:1024
	global_load_dwordx2 v[100:101], v[10:11], off offset:1536
	global_load_dwordx2 v[98:99], v[10:11], off offset:2048
	global_load_dwordx2 v[96:97], v[10:11], off offset:2560
	global_load_dwordx2 v[94:95], v[10:11], off offset:3072
	global_load_dwordx2 v[92:93], v[10:11], off offset:3584
	v_lshl_add_u64 v[10:11], s[4:5], 0, v[8:9]
	s_or_b32 s4, s6, 4
	s_ashr_i32 s5, s4, 31
	s_lshl_b64 s[4:5], s[4:5], 12
	s_add_u32 s4, s16, s4
	s_addc_u32 s5, s17, s5
	global_load_dwordx2 v[88:89], v[10:11], off
	global_load_dwordx2 v[90:91], v[10:11], off offset:512
	global_load_dwordx2 v[86:87], v[10:11], off offset:1024
	global_load_dwordx2 v[84:85], v[10:11], off offset:1536
	global_load_dwordx2 v[82:83], v[10:11], off offset:2048
	global_load_dwordx2 v[80:81], v[10:11], off offset:2560
	global_load_dwordx2 v[78:79], v[10:11], off offset:3072
	global_load_dwordx2 v[76:77], v[10:11], off offset:3584
	v_lshl_add_u64 v[10:11], s[4:5], 0, v[8:9]
	s_or_b32 s4, s6, 5
	s_ashr_i32 s5, s4, 31
	s_lshl_b64 s[4:5], s[4:5], 12
	s_add_u32 s4, s16, s4
	s_addc_u32 s5, s17, s5
	global_load_dwordx2 v[72:73], v[10:11], off
	global_load_dwordx2 v[74:75], v[10:11], off offset:512
	global_load_dwordx2 v[70:71], v[10:11], off offset:1024
	global_load_dwordx2 v[68:69], v[10:11], off offset:1536
	global_load_dwordx2 v[66:67], v[10:11], off offset:2048
	global_load_dwordx2 v[64:65], v[10:11], off offset:2560
	global_load_dwordx2 v[62:63], v[10:11], off offset:3072
	global_load_dwordx2 v[60:61], v[10:11], off offset:3584
	v_lshl_add_u64 v[10:11], s[4:5], 0, v[8:9]
	s_or_b32 s4, s6, 6
	s_ashr_i32 s5, s4, 31
	s_lshl_b64 s[4:5], s[4:5], 12
	s_add_u32 s4, s16, s4
	s_addc_u32 s5, s17, s5
	global_load_dwordx2 v[56:57], v[10:11], off
	global_load_dwordx2 v[58:59], v[10:11], off offset:512
	global_load_dwordx2 v[54:55], v[10:11], off offset:1024
	global_load_dwordx2 v[52:53], v[10:11], off offset:1536
	global_load_dwordx2 v[50:51], v[10:11], off offset:2048
	global_load_dwordx2 v[48:49], v[10:11], off offset:2560
	global_load_dwordx2 v[46:47], v[10:11], off offset:3072
	global_load_dwordx2 v[44:45], v[10:11], off offset:3584
	v_lshl_add_u64 v[10:11], s[4:5], 0, v[8:9]
	s_or_b32 s4, s6, 7
	s_ashr_i32 s5, s4, 31
	s_lshl_b64 s[4:5], s[4:5], 12
	s_add_u32 s4, s16, s4
	s_addc_u32 s5, s17, s5
	v_lshl_add_u64 v[8:9], s[4:5], 0, v[8:9]
	global_load_dwordx2 v[40:41], v[10:11], off
	global_load_dwordx2 v[42:43], v[10:11], off offset:512
	global_load_dwordx2 v[38:39], v[10:11], off offset:1024
	global_load_dwordx2 v[36:37], v[10:11], off offset:1536
	global_load_dwordx2 v[30:31], v[10:11], off offset:2048
	global_load_dwordx2 v[28:29], v[10:11], off offset:2560
	global_load_dwordx2 v[26:27], v[10:11], off offset:3072
	global_load_dwordx2 v[24:25], v[10:11], off offset:3584
	global_load_dwordx2 v[20:21], v[8:9], off
	global_load_dwordx2 v[22:23], v[8:9], off offset:512
	global_load_dwordx2 v[18:19], v[8:9], off offset:1024
	global_load_dwordx2 v[16:17], v[8:9], off offset:1536
	global_load_dwordx2 v[14:15], v[8:9], off offset:2048
	global_load_dwordx2 v[12:13], v[8:9], off offset:2560
	global_load_dwordx2 v[10:11], v[8:9], off offset:3072
	s_nop 0
	global_load_dwordx2 v[8:9], v[8:9], off offset:3584
	s_waitcnt vmcnt(62)
; __device__ __forceinline__ void p6_router(Frame& F) {
;     ...
;             for (int rr = 0; rr < 8; ++rr) { const int row = F.wave * 8 + rr, m = t0 + row;
;                 f32x4 v[8]; float s = 0.f;
; #pragma unroll
;                 for (int j = 0; j < 8; ++j) { const v2u w = raw[rr][j]; v[j] = (f32x4){bf_lo(w.x), bf_hi(w.x), bf_lo(w.y), bf_hi(w.y)}; s += (v[j][0] + v[j][1]) + (v[j][2] + v[j][3]); }
;                 const float mean = wave_sum(s) * (1.f / D); float s2 = 0.f;
; #pragma unroll
;                 for (int j = 0; j < 8; ++j) { v[j] = v[j] - mean; s2 += (v[j][0] * v[j][0] + v[j][1] * v[j][1]) + (v[j][2] * v[j][2] + v[j][3] * v[j][3]); }
;                 const float rstd = 1.f / sqrtf(wave_sum(s2) * (1.f / D) + LN_EPS);
	v_lshlrev_b32_e32 v144, 16, v6
	v_lshlrev_b32_e32 v145, 16, v128
	v_and_b32_e32 v149, 0xffff0000, v128
	v_and_b32_e32 v148, 0xffff0000, v6
	v_lshlrev_b32_e32 v151, 16, v129
	v_lshlrev_b32_e32 v150, 16, v7
	v_and_b32_e32 v157, 0xffff0000, v129
	v_and_b32_e32 v156, 0xffff0000, v7
	v_pk_add_f32 v[6:7], v[144:145], v[148:149]
	v_pk_add_f32 v[128:129], v[150:151], v[156:157]
	s_waitcnt vmcnt(61)
	v_lshlrev_b32_e32 v143, 16, v127
	v_pk_add_f32 v[6:7], v[6:7], v[128:129]
	v_lshlrev_b32_e32 v142, 16, v126
	v_and_b32_e32 v153, 0xffff0000, v127
	v_and_b32_e32 v152, 0xffff0000, v126
	v_add_f32_e32 v6, 0, v6
	v_pk_add_f32 v[126:127], v[142:143], v[152:153]
	v_add_f32_e32 v6, v6, v7
	s_waitcnt vmcnt(60)
	v_lshlrev_b32_e32 v138, 16, v124
	v_and_b32_e32 v139, 0xffff0000, v124
	v_lshlrev_b32_e32 v140, 16, v125
	v_and_b32_e32 v141, 0xffff0000, v125
	s_waitcnt vmcnt(59)
	v_lshlrev_b32_e32 v7, 16, v4
	v_and_b32_e32 v135, 0xffff0000, v4
	v_lshlrev_b32_e32 v133, 16, v5
	v_and_b32_e32 v131, 0xffff0000, v5
	v_pk_add_f32 v[4:5], v[126:127], v[126:127] op_sel:[0,1] op_sel_hi:[1,0]
	v_add_f32_e32 v132, v138, v139
	v_add_f32_e32 v130, v140, v141
	v_mov_b32_e32 v5, v135
	v_pk_add_f32 v[4:5], v[6:7], v[4:5]
	v_pk_add_f32 v[124:125], v[132:133], v[130:131]
	s_waitcnt vmcnt(58)
	v_and_b32_e32 v155, 0xffff0000, v1
	v_pk_add_f32 v[146:147], v[4:5], v[124:125]
	v_lshlrev_b32_e32 v5, 16, v1
	v_lshlrev_b32_e32 v4, 16, v0
	v_and_b32_e32 v154, 0xffff0000, v0
	v_pk_add_f32 v[176:177], v[4:5], v[154:155]
	s_waitcnt vmcnt(57)
	v_lshlrev_b32_e32 v0, 16, v2
	v_and_b32_e32 v1, 0xffff0000, v2
	v_lshlrev_b32_e32 v2, 16, v3
	v_and_b32_e32 v3, 0xffff0000, v3
	s_waitcnt vmcnt(56)
	v_lshlrev_b32_e32 v128, 16, v136
	v_and_b32_e32 v129, 0xffff0000, v136
	v_lshlrev_b32_e32 v127, 16, v137
	v_and_b32_e32 v125, 0xffff0000, v137
	v_pk_add_f32 v[136:137], v[146:147], v[146:147] op_sel:[0,1] op_sel_hi:[1,0]
	v_pk_add_f32 v[146:147], v[176:177], v[176:177] op_sel:[0,1] op_sel_hi:[1,0]
	v_add_f32_e32 v126, v0, v1
	v_add_f32_e32 v124, v2, v3
	v_mov_b32_e32 v137, v128
	v_mov_b32_e32 v147, v129
	v_pk_add_f32 v[136:137], v[136:137], v[146:147]
	v_pk_add_f32 v[146:147], v[126:127], v[124:125]
	s_nop 0
	v_pk_add_f32 v[136:137], v[136:137], v[146:147]
	s_nop 0
	v_add_f32_e32 v6, v136, v137
	s_waitcnt lgkmcnt(0)
	s_nop 1
	v_add_f32_dpp v6, v6, v6 quad_perm:[1,0,3,2] row_mask:0xf bank_mask:0xf
	s_waitcnt lgkmcnt(0)
	s_nop 1
	v_add_f32_dpp v6, v6, v6 quad_perm:[2,3,0,1] row_mask:0xf bank_mask:0xf
	s_waitcnt lgkmcnt(0)
	s_nop 1
	v_add_f32_dpp v6, v6, v6 row_half_mirror row_mask:0xf bank_mask:0xf
	s_waitcnt lgkmcnt(0)
	s_nop 1
	v_add_f32_dpp v6, v6, v6 row_mirror row_mask:0xf bank_mask:0xf
	s_waitcnt lgkmcnt(0)
	v_mov_b32_e32 v32, v6
	s_nop 1
	v_permlane16_swap_b32_e32 v6, v32
	v_add_f32_e32 v6, v6, v32
	s_waitcnt lgkmcnt(0)
	v_mov_b32_e32 v32, v6
	s_nop 1
	v_permlane32_swap_b32_e32 v6, v32
	v_add_f32_e32 v126, v6, v32
	v_fmac_f32_e32 v148, 0xba000000, v126
	v_fmac_f32_e32 v149, 0xba000000, v126
	v_fmac_f32_e32 v156, 0xba000000, v126
	v_fmac_f32_e32 v144, 0xba000000, v126
	v_fmac_f32_e32 v157, 0xba000000, v126
	v_fmac_f32_e32 v145, 0xba000000, v126
	v_mov_b32_e32 v147, v149
	v_mov_b32_e32 v137, v148
	v_pk_mul_f32 v[148:149], v[148:149], v[148:149]
	v_fmac_f32_e32 v150, 0xba000000, v126
	v_fmac_f32_e32 v151, 0xba000000, v126
	v_mov_b32_e32 v146, v145
	v_pk_fma_f32 v[176:177], v[144:145], v[144:145], v[148:149]
	v_mov_b32_e32 v149, v157
	v_mov_b32_e32 v145, v156
	v_pk_mul_f32 v[156:157], v[156:157], v[156:157]
	v_mov_b32_e32 v136, v144
	v_mov_b32_e32 v148, v151
	v_mov_b32_e32 v144, v150
	v_pk_fma_f32 v[150:151], v[150:151], v[150:151], v[156:157]
	v_fmac_f32_e32 v152, 0xba000000, v126
	v_pk_add_f32 v[150:151], v[176:177], v[150:151]
	v_fmac_f32_e32 v153, 0xba000000, v126
	v_fmac_f32_e32 v143, 0xba000000, v126
	v_pk_add_f32 v[156:157], v[150:151], v[150:151] op_sel_hi:[0,1]
	v_fmac_f32_e32 v142, 0xba000000, v126
	v_mov_b32_e32 v150, v143
	v_mov_b32_e32 v151, v153
	v_mov_b32_e32 v143, v152
	v_pk_mul_f32 v[176:177], v[150:151], v[150:151]
	v_pk_mul_f32 v[152:153], v[142:143], v[142:143]
	v_fmac_f32_e32 v138, 0xba000000, v126
	v_pk_mov_b32 v[178:179], v[152:153], v[176:177] op_sel:[1,0]
	v_mov_b32_e32 v153, v177
	v_fmac_f32_e32 v139, 0xba000000, v126
	v_fmac_f32_e32 v140, 0xba000000, v126
	v_mul_f32_e32 v6, v138, v138
	v_pk_add_f32 v[152:153], v[178:179], v[152:153]
	v_fmac_f32_e32 v141, 0xba000000, v126
	v_pk_fma_f32 v[176:177], v[138:139], v[138:139], v[6:7] op_sel_hi:[1,1,0]
	v_mul_f32_e32 v6, v140, v140
	v_pk_add_f32 v[152:153], v[152:153], v[152:153] op_sel_hi:[0,1]
	v_pk_fma_f32 v[178:179], v[140:141], v[140:141], v[6:7] op_sel_hi:[1,1,0]
	v_fmac_f32_e32 v131, 0xba000000, v126
	v_fmac_f32_e32 v133, 0xba000000, v126
	v_fmac_f32_e32 v135, 0xba000000, v126
	v_fmac_f32_e32 v7, 0xba000000, v126
	v_mul_f32_e32 v176, v7, v7
	v_mul_f32_e32 v178, v135, v135
	v_mul_f32_e32 v152, v133, v133
	v_mul_f32_e32 v156, v131, v131
	v_pk_add_f32 v[176:177], v[176:177], v[178:179]
	v_pk_add_f32 v[152:153], v[152:153], v[156:157]
	v_fmac_f32_e32 v154, 0xba000000, v126
	v_pk_add_f32 v[152:153], v[176:177], v[152:153]
	v_fmac_f32_e32 v155, 0xba000000, v126
	v_fmac_f32_e32 v5, 0xba000000, v126
	v_pk_add_f32 v[156:157], v[152:153], v[152:153] op_sel_hi:[0,1]
	v_fmac_f32_e32 v4, 0xba000000, v126
	v_mov_b32_e32 v152, v5
	v_mov_b32_e32 v153, v155
	v_mov_b32_e32 v5, v154
	v_pk_mul_f32 v[176:177], v[152:153], v[152:153]
	v_pk_mul_f32 v[154:155], v[4:5], v[4:5]
	v_fmac_f32_e32 v0, 0xba000000, v126
	v_pk_mov_b32 v[178:179], v[154:155], v[176:177] op_sel:[1,0]
	v_mov_b32_e32 v155, v177
	v_fmac_f32_e32 v1, 0xba000000, v126
	v_fmac_f32_e32 v2, 0xba000000, v126
	v_mul_f32_e32 v6, v0, v0
	v_pk_add_f32 v[154:155], v[178:179], v[154:155]
	v_fmac_f32_e32 v3, 0xba000000, v126
	v_pk_fma_f32 v[176:177], v[0:1], v[0:1], v[6:7] op_sel_hi:[1,1,0]
	v_mul_f32_e32 v6, v2, v2
	v_pk_add_f32 v[154:155], v[154:155], v[154:155] op_sel_hi:[0,1]
	v_pk_fma_f32 v[178:179], v[2:3], v[2:3], v[6:7] op_sel_hi:[1,1,0]
	v_fmac_f32_e32 v125, 0xba000000, v126
	v_fmac_f32_e32 v127, 0xba000000, v126
	v_fmac_f32_e32 v129, 0xba000000, v126
	v_fmac_f32_e32 v128, 0xba000000, v126
	v_mul_f32_e32 v176, v128, v128
	v_mul_f32_e32 v178, v129, v129
	v_mul_f32_e32 v154, v127, v127
	v_mul_f32_e32 v156, v125, v125
	v_pk_add_f32 v[176:177], v[176:177], v[178:179]
	v_pk_add_f32 v[154:155], v[154:155], v[156:157]
	s_nop 0
	v_pk_add_f32 v[154:155], v[176:177], v[154:155]
	s_nop 0
	v_add_f32_e32 v6, v154, v155
	v_mbcnt_lo_u32_b32 v154, -1, 0
	v_mbcnt_hi_u32_b32 v154, -1, v154
	v_ashrrev_i32_e32 v155, 31, v154
	v_lshl_add_u64 v[154:155], v[154:155], 4, s[12:13]
	v_mbcnt_lo_u32_b32 v176, -1, 0
	v_mbcnt_hi_u32_b32 v176, -1, v176
	s_waitcnt lgkmcnt(0)
; #define GAS __attribute__((address_space(1)))
; #define FLANE lane_id()
; __device__ __forceinline__ void p6_router(Frame& F) {
;     ...
;                 const float rstd = 1.f / sqrtf(wave_sum(s2) * (1.f / D) + LN_EPS);
;                 float am = 0.f;
; #pragma unroll
;                 for (int j = 0; j < 8; ++j) { const f32x4 g = *((const GAS f32x4*)F.ln1_g + FLANE + 64 * j), b = *((const GAS f32x4*)F.ln1_b + FLANE + 64 * j);
;                     v[j] = v[j] * rstd * g + b; am = fmaxf(am, fmaxf(fmaxf(fabsf(v[j][0]), fabsf(v[j][1])), fmaxf(fabsf(v[j][2]), fabsf(v[j][3])))); }
	s_nop 1
	v_add_f32_dpp v6, v6, v6 quad_perm:[1,0,3,2] row_mask:0xf bank_mask:0xf
	v_ashrrev_i32_e32 v177, 31, v176
	v_lshl_add_u64 v[176:177], v[176:177], 4, s[14:15]
	s_waitcnt lgkmcnt(0)
	s_nop 1
	v_add_f32_dpp v6, v6, v6 quad_perm:[2,3,0,1] row_mask:0xf bank_mask:0xf
	s_waitcnt lgkmcnt(0)
	s_nop 1
	v_add_f32_dpp v6, v6, v6 row_half_mirror row_mask:0xf bank_mask:0xf
	s_waitcnt lgkmcnt(0)
	s_nop 1
	v_add_f32_dpp v6, v6, v6 row_mirror row_mask:0xf bank_mask:0xf
	s_waitcnt lgkmcnt(0)
	v_mov_b32_e32 v32, v6
	s_nop 1
	v_permlane16_swap_b32_e32 v6, v32
	v_add_f32_e32 v6, v6, v32
	s_waitcnt lgkmcnt(0)
	v_mov_b32_e32 v32, v6
	s_nop 1
	v_permlane32_swap_b32_e32 v6, v32
	v_add_f32_e32 v6, v6, v32
	v_fmamk_f32 v6, v6, 0x3a000000, v166
	v_cmp_gt_f32_e32 vcc, s22, v6
	v_mul_f32_e32 v32, 0x4f800000, v6
	s_nop 0
	v_cndmask_b32_e32 v6, v6, v32, vcc
	v_sqrt_f32_e32 v32, v6
	s_nop 0
	v_add_u32_e32 v124, -1, v32
	v_fma_f32 v130, -v124, v32, v6
	v_cmp_ge_f32_e64 s[4:5], 0, v130
	v_add_u32_e32 v130, 1, v32
	s_nop 0
	v_cndmask_b32_e64 v124, v32, v124, s[4:5]
	v_fma_f32 v32, -v130, v32, v6
	v_cmp_lt_f32_e64 s[4:5], 0, v32
	s_nop 1
	v_cndmask_b32_e64 v32, v124, v130, s[4:5]
	v_mul_f32_e32 v124, 0x37800000, v32
	v_cndmask_b32_e32 v32, v32, v124, vcc
	v_cmp_class_f32_e32 vcc, v6, v167
	s_nop 1
	v_cndmask_b32_e32 v6, v32, v6, vcc
	v_div_scale_f32 v32, s[4:5], v6, v6, 1.0
	v_rcp_f32_e32 v124, v32
	s_nop 0
	v_fma_f32 v130, -v32, v124, 1.0
	v_fmac_f32_e32 v124, v130, v124
	v_div_scale_f32 v130, vcc, 1.0, v6, 1.0
	v_mul_f32_e32 v132, v130, v124
	v_fma_f32 v134, -v32, v132, v130
	v_fmac_f32_e32 v132, v134, v124
	v_fma_f32 v32, -v32, v132, v130
	v_div_fmas_f32 v32, v32, v124, v132
	v_div_fixup_f32 v32, v32, v6, 1.0
	v_pk_mul_f32 v[180:181], v[136:137], v[32:33] op_sel_hi:[1,0]
	v_pk_mul_f32 v[136:137], v[144:145], v[32:33] op_sel_hi:[1,0]
	v_mov_b32_e32 v134, v7
	v_pk_mul_f32 v[4:5], v[4:5], v[32:33] op_sel_hi:[1,0]
	v_pk_mul_f32 v[2:3], v[2:3], v[32:33] op_sel_hi:[1,0]
	v_pk_mul_f32 v[0:1], v[0:1], v[32:33] op_sel_hi:[1,0]
	v_pk_mul_f32 v[128:129], v[128:129], v[32:33] op_sel_hi:[1,0]
	s_waitcnt vmcnt(0)
	v_pk_fma_f32 v[144:145], v[196:197], v[180:181], v[228:229]
	v_mbcnt_lo_u32_b32 v154, -1, 0
	v_mbcnt_hi_u32_b32 v154, -1, v154
	v_pk_fma_f32 v[136:137], v[198:199], v[136:137], v[230:231]
	v_ashrrev_i32_e32 v155, 31, v154
	v_lshl_add_u64 v[154:155], v[154:155], 4, s[12:13]
	v_mbcnt_lo_u32_b32 v176, -1, 0
	v_mbcnt_hi_u32_b32 v176, -1, v176
	v_pk_mul_f32 v[180:181], v[146:147], v[32:33] op_sel_hi:[1,0]
	v_ashrrev_i32_e32 v177, 31, v176
	v_lshl_add_u64 v[176:177], v[176:177], 4, s[14:15]
	v_pk_mul_f32 v[146:147], v[148:149], v[32:33] op_sel_hi:[1,0]
	v_max_f32_e64 v6, |v136|, |v137|
	v_max3_f32 v6, |v144|, |v145|, v6
	s_waitcnt vmcnt(0)
	v_pk_fma_f32 v[148:149], v[200:201], v[180:181], v[232:233]
	v_mbcnt_lo_u32_b32 v154, -1, 0
	v_mbcnt_hi_u32_b32 v154, -1, v154
	v_pk_fma_f32 v[146:147], v[202:203], v[146:147], v[234:235]
	v_ashrrev_i32_e32 v155, 31, v154
	v_lshl_add_u64 v[154:155], v[154:155], 4, s[12:13]
	v_mbcnt_lo_u32_b32 v176, -1, 0
	v_mbcnt_hi_u32_b32 v176, -1, v176
	v_pk_mul_f32 v[180:181], v[142:143], v[32:33] op_sel_hi:[1,0]
	v_ashrrev_i32_e32 v177, 31, v176
	v_lshl_add_u64 v[176:177], v[176:177], 4, s[14:15]
	v_pk_mul_f32 v[142:143], v[150:151], v[32:33] op_sel_hi:[1,0]
	v_max_f32_e64 v124, |v146|, |v147|
	v_max3_f32 v124, |v148|, |v149|, v124
	v_max3_f32 v6, v6, 0, v124
	s_waitcnt vmcnt(0)
	v_pk_fma_f32 v[150:151], v[204:205], v[180:181], v[236:237]
	v_mbcnt_lo_u32_b32 v154, -1, 0
	v_mbcnt_hi_u32_b32 v154, -1, v154
	v_pk_fma_f32 v[142:143], v[206:207], v[142:143], v[238:239]
	v_ashrrev_i32_e32 v155, 31, v154
	v_lshl_add_u64 v[154:155], v[154:155], 4, s[12:13]
	v_mbcnt_lo_u32_b32 v176, -1, 0
	v_mbcnt_hi_u32_b32 v176, -1, v176
	v_pk_mul_f32 v[180:181], v[138:139], v[32:33] op_sel_hi:[1,0]
	v_ashrrev_i32_e32 v177, 31, v176
	v_lshl_add_u64 v[176:177], v[176:177], 4, s[14:15]
	v_pk_mul_f32 v[138:139], v[140:141], v[32:33] op_sel_hi:[1,0]
	v_max_f32_e64 v124, |v142|, |v143|
	v_max3_f32 v124, |v150|, |v151|, v124
	s_waitcnt vmcnt(0)
	v_pk_fma_f32 v[140:141], v[208:209], v[180:181], v[240:241]
	v_mbcnt_lo_u32_b32 v154, -1, 0
	v_mbcnt_hi_u32_b32 v154, -1, v154
	v_pk_fma_f32 v[138:139], v[210:211], v[138:139], v[242:243]
	v_ashrrev_i32_e32 v155, 31, v154
	v_lshl_add_u64 v[154:155], v[154:155], 4, s[12:13]
	v_add_co_u32_e32 v154, vcc, s23, v154
	v_max_f32_e64 v130, |v138|, |v139|
	s_nop 0
	v_addc_co_u32_e32 v155, vcc, 0, v155, vcc
	v_mbcnt_lo_u32_b32 v176, -1, 0
	v_mbcnt_hi_u32_b32 v176, -1, v176
	v_max3_f32 v130, |v140|, |v141|, v130
	v_ashrrev_i32_e32 v177, 31, v176
	v_lshl_add_u64 v[176:177], v[176:177], 4, s[14:15]
	v_add_co_u32_e32 v176, vcc, s23, v176
	v_max3_f32 v124, v6, v124, v130
	s_nop 0
	v_addc_co_u32_e32 v177, vcc, 0, v177, vcc
	v_mov_b32_e32 v130, v133
	v_pk_mul_f32 v[130:131], v[130:131], v[32:33] op_sel_hi:[1,0]
	v_pk_mul_f32 v[6:7], v[134:135], v[32:33] op_sel_hi:[1,0]
	s_waitcnt vmcnt(0)
	v_pk_fma_f32 v[130:131], v[214:215], v[130:131], v[246:247]
	v_pk_fma_f32 v[132:133], v[212:213], v[6:7], v[244:245]
	v_max_f32_e64 v6, |v130|, |v131|
	v_max3_f32 v180, |v132|, |v133|, v6
	v_mbcnt_lo_u32_b32 v6, -1, 0
	v_mbcnt_hi_u32_b32 v6, -1, v6
	s_nop 0
	v_ashrrev_i32_e32 v7, 31, v6
	v_lshl_add_u64 v[6:7], v[6:7], 4, s[12:13]
	v_add_co_u32_e32 v6, vcc, s23, v6
	s_nop 1
	v_addc_co_u32_e32 v7, vcc, 0, v7, vcc
	v_mbcnt_lo_u32_b32 v6, -1, 0
	v_mbcnt_hi_u32_b32 v6, -1, v6
	s_nop 0
	v_ashrrev_i32_e32 v7, 31, v6
	v_lshl_add_u64 v[6:7], v[6:7], 4, s[14:15]
	v_add_co_u32_e32 v6, vcc, s23, v6
	s_nop 1
	v_addc_co_u32_e32 v7, vcc, 0, v7, vcc
	v_pk_mul_f32 v[6:7], v[152:153], v[32:33] op_sel_hi:[1,0]
	s_waitcnt vmcnt(0)
; #define FLANE lane_id()
; __device__ __forceinline__ void p6_router(Frame& F) {
;     ...
;                     v[j] = v[j] * rstd * g + b; am = fmaxf(am, fmaxf(fmaxf(fabsf(v[j][0]), fabsf(v[j][1])), fmaxf(fabsf(v[j][2]), fabsf(v[j][3])))); }
; #pragma unroll
;                 for (int o = 1; o < 64; o <<= 1) am = fmaxf(am, __shfl_xor(am, o));
;                 const float sc = am > 0.f ? am * (1.f / 127.f) : 1.f, inv = 1.f / sc;
; #pragma unroll
;                 for (int j = 0; j < 8; ++j) { const int q0 = (int)__builtin_rintf(v[j][0] * inv), q1 = (int)__builtin_rintf(v[j][1] * inv), q2 = (int)__builtin_rintf(v[j][2] * inv), q3 = (int)__builtin_rintf(v[j][3] * inv);
;                     h1q[(size_t)m * (D / 4) + FLANE + 64 * j] = (unsigned)(q0 & 0xff) | ((unsigned)(q1 & 0xff) << 8) | ((unsigned)(q2 & 0xff) << 16) | ((unsigned)(q3 & 0xff) << 24); }
	v_pk_fma_f32 v[152:153], v[216:217], v[4:5], v[248:249]
	v_pk_fma_f32 v[134:135], v[218:219], v[6:7], v[250:251]
	s_nop 0
	v_max_f32_e64 v4, |v134|, |v135|
	v_max3_f32 v4, |v152|, |v153|, v4
	v_max3_f32 v180, v124, v180, v4
	v_mbcnt_lo_u32_b32 v4, -1, 0
	v_mbcnt_hi_u32_b32 v4, -1, v4
	v_mov_b32_e32 v124, v127
	v_ashrrev_i32_e32 v5, 31, v4
	v_lshl_add_u64 v[4:5], v[4:5], 4, s[12:13]
	v_add_co_u32_e32 v4, vcc, s23, v4
	v_pk_mul_f32 v[124:125], v[124:125], v[32:33] op_sel_hi:[1,0]
	s_nop 0
	v_addc_co_u32_e32 v5, vcc, 0, v5, vcc
	v_mbcnt_lo_u32_b32 v154, -1, 0
	v_mbcnt_hi_u32_b32 v154, -1, v154
	s_nop 0
	v_ashrrev_i32_e32 v155, 31, v154
	v_lshl_add_u64 v[154:155], v[154:155], 4, s[14:15]
	v_add_co_u32_e32 v154, vcc, s23, v154
	s_nop 1
	v_addc_co_u32_e32 v155, vcc, 0, v155, vcc
	s_waitcnt vmcnt(0)
	v_pk_fma_f32 v[154:155], v[2:3], v[222:223], v[184:185]
	v_pk_fma_f32 v[156:157], v[0:1], v[220:221], v[182:183]
	v_max_f32_e64 v0, |v154|, |v155|
	v_max3_f32 v176, |v156|, |v157|, v0
	v_mbcnt_lo_u32_b32 v0, -1, 0
	v_mbcnt_hi_u32_b32 v0, -1, v0
	s_nop 0
	v_ashrrev_i32_e32 v1, 31, v0
	v_lshl_add_u64 v[0:1], v[0:1], 4, s[12:13]
	v_add_co_u32_e32 v0, vcc, s23, v0
	s_nop 1
	v_addc_co_u32_e32 v1, vcc, 0, v1, vcc
	v_mbcnt_lo_u32_b32 v4, -1, 0
	v_mbcnt_hi_u32_b32 v4, -1, v4
	s_nop 0
	v_ashrrev_i32_e32 v5, 31, v4
	v_lshl_add_u64 v[4:5], v[4:5], 4, s[14:15]
	v_add_co_u32_e32 v4, vcc, s23, v4
	s_nop 1
	v_addc_co_u32_e32 v5, vcc, 0, v5, vcc
	s_waitcnt vmcnt(0)
	v_pk_fma_f32 v[2:3], v[124:125], v[226:227], v[188:189]
	v_pk_fma_f32 v[4:5], v[128:129], v[224:225], v[186:187]
	v_max_f32_e64 v0, |v2|, |v3|
	v_max3_f32 v0, |v4|, |v5|, v0
	v_max3_f32 v0, v180, v176, v0
	s_waitcnt lgkmcnt(0)
	s_nop 1
	v_max_f32_dpp v0, v0, v0 quad_perm:[1,0,3,2] row_mask:0xf bank_mask:0xf
	s_waitcnt lgkmcnt(0)
	s_nop 1
	v_max_f32_dpp v0, v0, v0 quad_perm:[2,3,0,1] row_mask:0xf bank_mask:0xf
	s_waitcnt lgkmcnt(0)
	s_nop 1
	v_max_f32_dpp v0, v0, v0 row_half_mirror row_mask:0xf bank_mask:0xf
	s_waitcnt lgkmcnt(0)
	s_nop 1
	v_max_f32_dpp v0, v0, v0 row_mirror row_mask:0xf bank_mask:0xf
	s_waitcnt lgkmcnt(0)
	v_mov_b32_e32 v1, v0
	s_nop 1
	v_permlane16_swap_b32_e32 v0, v1
	v_max_f32_e32 v0, v0, v1
	s_waitcnt lgkmcnt(0)
	v_mov_b32_e32 v1, v0
	s_nop 1
	v_permlane32_swap_b32_e32 v0, v1
	v_max_f32_e32 v0, v0, v1
	v_cmp_lt_f32_e32 vcc, 0, v0
	v_mul_f32_e32 v0, 0x3c010204, v0
	s_nop 0
	v_cndmask_b32_e32 v0, 1.0, v0, vcc
	v_div_scale_f32 v1, s[4:5], v0, v0, 1.0
	v_rcp_f32_e32 v6, v1
	s_lshl_b64 s[4:5], s[6:7], 11
	s_add_u32 s4, s3, s4
	s_addc_u32 s5, s24, s5
	v_fma_f32 v7, -v1, v6, 1.0
	v_fmac_f32_e32 v6, v7, v6
	v_div_scale_f32 v7, vcc, 1.0, v0, 1.0
	v_mul_f32_e32 v124, v7, v6
	v_fma_f32 v125, -v1, v124, v7
	v_fmac_f32_e32 v124, v125, v6
	v_fma_f32 v1, -v1, v124, v7
	v_div_fmas_f32 v1, v1, v6, v124
	v_div_fixup_f32 v1, v1, v0, 1.0
	v_mul_f32_e32 v7, v145, v1
	v_mul_f32_e32 v6, v144, v1
	v_rndne_f32_e32 v7, v7
	v_mul_f32_e32 v124, v136, v1
	v_mul_f32_e32 v125, v137, v1
	v_rndne_f32_e32 v6, v6
	v_cvt_i32_f32_e32 v7, v7
	v_rndne_f32_e32 v124, v124
	v_rndne_f32_e32 v125, v125
	v_cvt_i32_f32_e32 v6, v6
	v_cvt_i32_f32_sdwa v124, v124 dst_sel:WORD_1 dst_unused:UNUSED_PAD src0_sel:DWORD
	v_cvt_i32_f32_e32 v125, v125
	v_lshlrev_b32_e32 v7, 8, v7
	v_and_b32_e32 v7, 0xff00, v7
	v_and_b32_e32 v124, 0xff0000, v124
	v_perm_b32 v6, v125, v6, s1
	v_or3_b32 v124, v6, v7, v124
	v_mbcnt_lo_u32_b32 v6, -1, 0
	v_mbcnt_hi_u32_b32 v6, -1, v6
	v_mul_f32_e32 v125, v147, v1
	v_ashrrev_i32_e32 v7, 31, v6
	v_lshl_add_u64 v[6:7], v[6:7], 2, s[4:5]
	global_store_dword v[6:7], v124, off
	v_mul_f32_e32 v7, v149, v1
	v_mul_f32_e32 v6, v148, v1
	v_rndne_f32_e32 v7, v7
	v_mul_f32_e32 v124, v146, v1
	v_rndne_f32_e32 v6, v6
	v_cvt_i32_f32_e32 v7, v7
	v_rndne_f32_e32 v124, v124
	v_rndne_f32_e32 v125, v125
	v_cvt_i32_f32_e32 v6, v6
	v_cvt_i32_f32_sdwa v124, v124 dst_sel:WORD_1 dst_unused:UNUSED_PAD src0_sel:DWORD
	v_cvt_i32_f32_e32 v125, v125
	v_lshlrev_b32_e32 v7, 8, v7
	v_and_b32_e32 v7, 0xff00, v7
	v_and_b32_e32 v124, 0xff0000, v124
	v_perm_b32 v6, v125, v6, s1
	v_or3_b32 v124, v6, v7, v124
	v_mbcnt_lo_u32_b32 v6, -1, 0
	v_mbcnt_hi_u32_b32 v6, -1, v6
	v_mul_f32_e32 v125, v143, v1
	v_ashrrev_i32_e32 v7, 31, v6
	v_lshl_add_u64 v[6:7], v[6:7], 2, s[4:5]
	global_store_dword v[6:7], v124, off offset:256
	v_mul_f32_e32 v7, v151, v1
	v_mul_f32_e32 v6, v150, v1
	v_rndne_f32_e32 v7, v7
	v_mul_f32_e32 v124, v142, v1
	v_rndne_f32_e32 v6, v6
	v_cvt_i32_f32_e32 v7, v7
	v_rndne_f32_e32 v124, v124
	v_rndne_f32_e32 v125, v125
	v_cvt_i32_f32_e32 v6, v6
	v_cvt_i32_f32_sdwa v124, v124 dst_sel:WORD_1 dst_unused:UNUSED_PAD src0_sel:DWORD
	v_cvt_i32_f32_e32 v125, v125
	v_lshlrev_b32_e32 v7, 8, v7
	v_and_b32_e32 v7, 0xff00, v7
	v_and_b32_e32 v124, 0xff0000, v124
	v_perm_b32 v6, v125, v6, s1
	v_or3_b32 v124, v6, v7, v124
	v_mbcnt_lo_u32_b32 v6, -1, 0
	v_mbcnt_hi_u32_b32 v6, -1, v6
	v_mul_f32_e32 v125, v139, v1
	v_ashrrev_i32_e32 v7, 31, v6
	v_lshl_add_u64 v[6:7], v[6:7], 2, s[4:5]
	global_store_dword v[6:7], v124, off offset:512
	v_mul_f32_e32 v7, v141, v1
	v_mul_f32_e32 v6, v140, v1
	v_rndne_f32_e32 v7, v7
	v_mul_f32_e32 v124, v138, v1
	v_rndne_f32_e32 v6, v6
	v_cvt_i32_f32_e32 v7, v7
	v_rndne_f32_e32 v124, v124
	v_rndne_f32_e32 v125, v125
	v_cvt_i32_f32_e32 v6, v6
	v_cvt_i32_f32_sdwa v124, v124 dst_sel:WORD_1 dst_unused:UNUSED_PAD src0_sel:DWORD
	v_cvt_i32_f32_e32 v125, v125
	v_lshlrev_b32_e32 v7, 8, v7
	v_and_b32_e32 v7, 0xff00, v7
	v_and_b32_e32 v124, 0xff0000, v124
	v_perm_b32 v6, v125, v6, s1
	v_or3_b32 v124, v6, v7, v124
	v_mbcnt_lo_u32_b32 v6, -1, 0
	v_mbcnt_hi_u32_b32 v6, -1, v6
	v_mul_f32_e32 v125, v131, v1
	v_ashrrev_i32_e32 v7, 31, v6
; #define FLANE lane_id()
; __device__ __forceinline__ void p6_router(Frame& F) {
;     ...
;             for (int rr = 0; rr < 8; ++rr) { const int row = F.wave * 8 + rr, m = t0 + row;
;                 f32x4 v[8]; float s = 0.f;
; #pragma unroll
;                 for (int j = 0; j < 8; ++j) { const v2u w = raw[rr][j]; v[j] = (f32x4){bf_lo(w.x), bf_hi(w.x), bf_lo(w.y), bf_hi(w.y)}; s += (v[j][0] + v[j][1]) + (v[j][2] + v[j][3]); }
;                 const float mean = wave_sum(s) * (1.f / D); float s2 = 0.f;
;     ...
;                 for (int j = 0; j < 8; ++j) { const int q0 = (int)__builtin_rintf(v[j][0] * inv), q1 = (int)__builtin_rintf(v[j][1] * inv), q2 = (int)__builtin_rintf(v[j][2] * inv), q3 = (int)__builtin_rintf(v[j][3] * inv);
;                     h1q[(size_t)m * (D / 4) + FLANE + 64 * j] = (unsigned)(q0 & 0xff) | ((unsigned)(q1 & 0xff) << 8) | ((unsigned)(q2 & 0xff) << 16) | ((unsigned)(q3 & 0xff) << 24); }
;                 if (FLANE == 0) { st1[2 * m] = mean; st1[2 * m + 1] = rstd; stl[2 * row] = mean; stl[2 * row + 1] = rstd; sxg[m] = sc; sxl[row] = sc; }
	v_lshl_add_u64 v[6:7], v[6:7], 2, s[4:5]
	global_store_dword v[6:7], v124, off offset:768
	v_mul_f32_e32 v7, v133, v1
	v_mul_f32_e32 v6, v132, v1
	v_rndne_f32_e32 v7, v7
	v_mul_f32_e32 v124, v130, v1
	v_rndne_f32_e32 v6, v6
	v_cvt_i32_f32_e32 v7, v7
	v_rndne_f32_e32 v124, v124
	v_rndne_f32_e32 v125, v125
	v_cvt_i32_f32_e32 v6, v6
	v_cvt_i32_f32_sdwa v124, v124 dst_sel:WORD_1 dst_unused:UNUSED_PAD src0_sel:DWORD
	v_cvt_i32_f32_e32 v125, v125
	v_lshlrev_b32_e32 v7, 8, v7
	v_and_b32_e32 v7, 0xff00, v7
	v_and_b32_e32 v124, 0xff0000, v124
	v_perm_b32 v6, v125, v6, s1
	v_or3_b32 v124, v6, v7, v124
	v_mbcnt_lo_u32_b32 v6, -1, 0
	v_mbcnt_hi_u32_b32 v6, -1, v6
	v_mul_f32_e32 v125, v135, v1
	v_ashrrev_i32_e32 v7, 31, v6
	v_lshl_add_u64 v[6:7], v[6:7], 2, s[4:5]
	global_store_dword v[6:7], v124, off offset:1024
	v_mul_f32_e32 v7, v153, v1
	v_mul_f32_e32 v6, v152, v1
	v_rndne_f32_e32 v7, v7
	v_mul_f32_e32 v124, v134, v1
	v_rndne_f32_e32 v6, v6
	v_cvt_i32_f32_e32 v7, v7
	v_rndne_f32_e32 v124, v124
	v_rndne_f32_e32 v125, v125
	v_cvt_i32_f32_e32 v6, v6
	v_cvt_i32_f32_sdwa v124, v124 dst_sel:WORD_1 dst_unused:UNUSED_PAD src0_sel:DWORD
	v_cvt_i32_f32_e32 v125, v125
	v_lshlrev_b32_e32 v7, 8, v7
	v_and_b32_e32 v7, 0xff00, v7
	v_and_b32_e32 v124, 0xff0000, v124
	v_perm_b32 v6, v125, v6, s1
	v_or3_b32 v124, v6, v7, v124
	v_mbcnt_lo_u32_b32 v6, -1, 0
	v_mbcnt_hi_u32_b32 v6, -1, v6
	v_mul_f32_e32 v125, v155, v1
	v_ashrrev_i32_e32 v7, 31, v6
	v_lshl_add_u64 v[6:7], v[6:7], 2, s[4:5]
	global_store_dword v[6:7], v124, off offset:1280
	v_mul_f32_e32 v7, v157, v1
	v_mul_f32_e32 v6, v156, v1
	v_rndne_f32_e32 v7, v7
	v_mul_f32_e32 v124, v154, v1
	v_rndne_f32_e32 v6, v6
	v_cvt_i32_f32_e32 v7, v7
	v_rndne_f32_e32 v124, v124
	v_rndne_f32_e32 v125, v125
	v_mul_f32_e32 v5, v5, v1
	v_cvt_i32_f32_e32 v6, v6
	v_cvt_i32_f32_sdwa v124, v124 dst_sel:WORD_1 dst_unused:UNUSED_PAD src0_sel:DWORD
	v_cvt_i32_f32_e32 v125, v125
	v_mul_f32_e32 v4, v4, v1
	v_rndne_f32_e32 v5, v5
	v_mul_f32_e32 v2, v2, v1
	v_mul_f32_e32 v1, v3, v1
	v_rndne_f32_e32 v4, v4
	v_cvt_i32_f32_e32 v5, v5
	v_rndne_f32_e32 v2, v2
	v_rndne_f32_e32 v1, v1
	v_cvt_i32_f32_e32 v4, v4
	v_cvt_i32_f32_sdwa v2, v2 dst_sel:WORD_1 dst_unused:UNUSED_PAD src0_sel:DWORD
	v_cvt_i32_f32_e32 v1, v1
	v_lshlrev_b32_e32 v7, 8, v7
	v_and_b32_e32 v7, 0xff00, v7
	v_and_b32_e32 v124, 0xff0000, v124
	v_perm_b32 v6, v125, v6, s1
	v_or3_b32 v124, v6, v7, v124
	v_mbcnt_lo_u32_b32 v6, -1, 0
	v_mbcnt_hi_u32_b32 v6, -1, v6
	v_lshlrev_b32_e32 v3, 8, v5
	v_ashrrev_i32_e32 v7, 31, v6
	v_lshl_add_u64 v[6:7], v[6:7], 2, s[4:5]
	v_and_b32_e32 v3, 0xff00, v3
	v_and_b32_e32 v2, 0xff0000, v2
	v_perm_b32 v1, v1, v4, s1
	global_store_dword v[6:7], v124, off offset:1536
	v_or3_b32 v1, v1, v3, v2
	v_mbcnt_lo_u32_b32 v2, -1, 0
	v_mbcnt_hi_u32_b32 v2, -1, v2
	s_nop 0
	v_ashrrev_i32_e32 v3, 31, v2
	v_lshl_add_u64 v[2:3], v[2:3], 2, s[4:5]
	global_store_dword v[2:3], v1, off offset:1792
	v_mbcnt_lo_u32_b32 v1, -1, 0
	v_mbcnt_hi_u32_b32 v1, -1, v1
	s_nop 0
	v_cmp_eq_u32_e32 vcc, 0, v1
	s_and_saveexec_b64 s[4:5], vcc
	s_cbranch_execz .LBB0_1483
	s_lshl_b32 s8, s6, 1
	s_ashr_i32 s9, s8, 31
	s_lshl_b64 s[8:9], s[8:9], 2
	s_add_u32 s8, s27, s8
	s_addc_u32 s9, s64, s9
	s_add_i32 s0, s88, 0
	s_add_i32 s0, s0, 0x18c00
	s_lshl_b64 s[6:7], s[6:7], 2
	v_mul_f32_e32 v2, 0x3a000000, v126
	v_mov_b32_e32 v3, v32
	v_mov_b32_e32 v1, s0
	s_add_u32 s6, s25, s6
	v_readlane_b32 s0, v255, 20
	ds_write_b64 v1, v[2:3]
	s_addc_u32 s7, s26, s7
	v_mov_b32_e32 v1, s0
	global_store_dwordx2 v33, v[2:3], s[8:9]
	global_store_dword v33, v0, s[6:7]
	ds_write_b32 v1, v0
.LBB0_1483:
	s_or_b64 exec, exec, s[4:5]
	v_lshlrev_b32_e32 v125, 16, v122
	v_lshlrev_b32_e32 v124, 16, v120
	v_and_b32_e32 v137, 0xffff0000, v122
	v_and_b32_e32 v136, 0xffff0000, v120
	v_lshlrev_b32_e32 v139, 16, v123
	v_lshlrev_b32_e32 v138, 16, v121
	v_and_b32_e32 v141, 0xffff0000, v123
	v_and_b32_e32 v140, 0xffff0000, v121
	v_pk_add_f32 v[0:1], v[124:125], v[136:137]
	v_pk_add_f32 v[2:3], v[138:139], v[140:141]
	v_lshlrev_b32_e32 v123, 16, v119
	v_pk_add_f32 v[0:1], v[0:1], v[2:3]
	v_lshlrev_b32_e32 v122, 16, v118
	v_add_f32_e32 v0, 0, v0
	v_and_b32_e32 v143, 0xffff0000, v119
	v_and_b32_e32 v142, 0xffff0000, v118
	v_add_f32_e32 v6, v0, v1
	v_pk_add_f32 v[0:1], v[122:123], v[142:143]
	v_lshlrev_b32_e32 v126, 16, v116
	v_and_b32_e32 v127, 0xffff0000, v116
	v_lshlrev_b32_e32 v128, 16, v117
	v_and_b32_e32 v129, 0xffff0000, v117
	v_and_b32_e32 v135, 0xffff0000, v114
	v_pk_add_f32 v[0:1], v[0:1], v[0:1] op_sel:[0,1] op_sel_hi:[1,0]
	v_add_f32_e32 v132, v126, v127
	v_add_f32_e32 v130, v128, v129
	v_lshlrev_b32_e32 v7, 16, v114
	v_lshlrev_b32_e32 v133, 16, v115
	v_and_b32_e32 v131, 0xffff0000, v115
	v_mov_b32_e32 v1, v135
	v_pk_add_f32 v[0:1], v[6:7], v[0:1]
	v_pk_add_f32 v[2:3], v[132:133], v[130:131]
	v_lshlrev_b32_e32 v5, 16, v113
	v_lshlrev_b32_e32 v4, 16, v112
	v_and_b32_e32 v145, 0xffff0000, v113
	v_and_b32_e32 v144, 0xffff0000, v112
	v_pk_add_f32 v[116:117], v[0:1], v[2:3]
	v_pk_add_f32 v[118:119], v[4:5], v[144:145]
	v_lshlrev_b32_e32 v0, 16, v110
	v_and_b32_e32 v1, 0xffff0000, v110
	v_lshlrev_b32_e32 v2, 16, v111
	v_and_b32_e32 v3, 0xffff0000, v111
	v_lshlrev_b32_e32 v114, 16, v108
	v_and_b32_e32 v115, 0xffff0000, v108
	v_lshlrev_b32_e32 v113, 16, v109
	v_and_b32_e32 v111, 0xffff0000, v109
	v_pk_add_f32 v[108:109], v[116:117], v[116:117] op_sel:[0,1] op_sel_hi:[1,0]
	v_pk_add_f32 v[116:117], v[118:119], v[118:119] op_sel:[0,1] op_sel_hi:[1,0]
	v_add_f32_e32 v112, v0, v1
	v_add_f32_e32 v110, v2, v3
	v_mov_b32_e32 v109, v114
	v_mov_b32_e32 v117, v115
	v_pk_add_f32 v[108:109], v[108:109], v[116:117]
	v_pk_add_f32 v[116:117], v[112:113], v[110:111]
	v_readlane_b32 s0, v255, 16
	v_pk_add_f32 v[108:109], v[108:109], v[116:117]
	s_nop 0
	v_add_f32_e32 v6, v108, v109
	s_waitcnt lgkmcnt(0)
; __device__ __forceinline__ void p6_router(Frame& F) {
;     ...
;                 const float mean = wave_sum(s) * (1.f / D); float s2 = 0.f;
; #pragma unroll
;                 for (int j = 0; j < 8; ++j) { v[j] = v[j] - mean; s2 += (v[j][0] * v[j][0] + v[j][1] * v[j][1]) + (v[j][2] * v[j][2] + v[j][3] * v[j][3]); }
;                 const float rstd = 1.f / sqrtf(wave_sum(s2) * (1.f / D) + LN_EPS);
	s_nop 1
	v_add_f32_dpp v6, v6, v6 quad_perm:[1,0,3,2] row_mask:0xf bank_mask:0xf
	s_waitcnt lgkmcnt(0)
	s_nop 1
	v_add_f32_dpp v6, v6, v6 quad_perm:[2,3,0,1] row_mask:0xf bank_mask:0xf
	s_waitcnt lgkmcnt(0)
	s_nop 1
	v_add_f32_dpp v6, v6, v6 row_half_mirror row_mask:0xf bank_mask:0xf
	s_waitcnt lgkmcnt(0)
	s_nop 1
	v_add_f32_dpp v6, v6, v6 row_mirror row_mask:0xf bank_mask:0xf
	s_waitcnt lgkmcnt(0)
	v_mov_b32_e32 v32, v6
	s_nop 1
	v_permlane16_swap_b32_e32 v6, v32
	v_add_f32_e32 v6, v6, v32
	s_waitcnt lgkmcnt(0)
	v_mov_b32_e32 v32, v6
	s_nop 1
	v_permlane32_swap_b32_e32 v6, v32
	v_add_f32_e32 v112, v6, v32
	v_fmac_f32_e32 v140, 0xba000000, v112
	v_fmac_f32_e32 v136, 0xba000000, v112
	v_fmac_f32_e32 v141, 0xba000000, v112
	v_fmac_f32_e32 v137, 0xba000000, v112
	v_fmac_f32_e32 v138, 0xba000000, v112
	v_fmac_f32_e32 v124, 0xba000000, v112
	v_fmac_f32_e32 v139, 0xba000000, v112
	v_fmac_f32_e32 v125, 0xba000000, v112
	v_mov_b32_e32 v119, v137
	v_mov_b32_e32 v109, v136
	v_pk_mul_f32 v[116:117], v[136:137], v[136:137]
	v_pk_mul_f32 v[136:137], v[140:141], v[140:141]
	v_mov_b32_e32 v118, v125
	v_mov_b32_e32 v108, v124
	v_pk_fma_f32 v[124:125], v[124:125], v[124:125], v[116:117]
	v_pk_fma_f32 v[136:137], v[138:139], v[138:139], v[136:137]
	v_fmac_f32_e32 v142, 0xba000000, v112
	v_pk_add_f32 v[124:125], v[124:125], v[136:137]
	v_fmac_f32_e32 v143, 0xba000000, v112
	v_fmac_f32_e32 v123, 0xba000000, v112
	v_pk_add_f32 v[136:137], v[124:125], v[124:125] op_sel_hi:[0,1]
	v_fmac_f32_e32 v122, 0xba000000, v112
	v_mov_b32_e32 v124, v123
	v_mov_b32_e32 v125, v143
	v_mov_b32_e32 v123, v142
	v_mov_b32_e32 v120, v139
	v_mov_b32_e32 v121, v141
	v_mov_b32_e32 v116, v138
	v_mov_b32_e32 v117, v140
	v_pk_mul_f32 v[138:139], v[124:125], v[124:125]
	v_pk_mul_f32 v[140:141], v[122:123], v[122:123]
	v_fmac_f32_e32 v126, 0xba000000, v112
	v_pk_mov_b32 v[142:143], v[140:141], v[138:139] op_sel:[1,0]
	v_mov_b32_e32 v141, v139
	v_fmac_f32_e32 v127, 0xba000000, v112
	v_fmac_f32_e32 v128, 0xba000000, v112
	v_mul_f32_e32 v6, v126, v126
	v_pk_add_f32 v[138:139], v[142:143], v[140:141]
	v_fmac_f32_e32 v129, 0xba000000, v112
	v_pk_fma_f32 v[140:141], v[126:127], v[126:127], v[6:7] op_sel_hi:[1,1,0]
	v_mul_f32_e32 v6, v128, v128
	v_pk_add_f32 v[138:139], v[138:139], v[138:139] op_sel_hi:[0,1]
	v_pk_fma_f32 v[142:143], v[128:129], v[128:129], v[6:7] op_sel_hi:[1,1,0]
	v_fmac_f32_e32 v131, 0xba000000, v112
	v_fmac_f32_e32 v133, 0xba000000, v112
	v_fmac_f32_e32 v135, 0xba000000, v112
	v_fmac_f32_e32 v7, 0xba000000, v112
	v_mul_f32_e32 v140, v7, v7
	v_mul_f32_e32 v142, v135, v135
	v_mul_f32_e32 v138, v133, v133
	v_mul_f32_e32 v136, v131, v131
	v_pk_add_f32 v[140:141], v[140:141], v[142:143]
	v_pk_add_f32 v[136:137], v[138:139], v[136:137]
	v_fmac_f32_e32 v144, 0xba000000, v112
	v_pk_add_f32 v[136:137], v[140:141], v[136:137]
	v_fmac_f32_e32 v145, 0xba000000, v112
	v_fmac_f32_e32 v5, 0xba000000, v112
	v_pk_add_f32 v[138:139], v[136:137], v[136:137] op_sel_hi:[0,1]
	v_fmac_f32_e32 v4, 0xba000000, v112
	v_mov_b32_e32 v136, v5
	v_mov_b32_e32 v137, v145
	v_mov_b32_e32 v5, v144
	v_pk_mul_f32 v[140:141], v[136:137], v[136:137]
	v_pk_mul_f32 v[142:143], v[4:5], v[4:5]
	v_fmac_f32_e32 v0, 0xba000000, v112
	v_pk_mov_b32 v[144:145], v[142:143], v[140:141] op_sel:[1,0]
	v_mov_b32_e32 v143, v141
	v_fmac_f32_e32 v1, 0xba000000, v112
	v_fmac_f32_e32 v2, 0xba000000, v112
	v_mul_f32_e32 v6, v0, v0
	v_pk_add_f32 v[140:141], v[144:145], v[142:143]
	v_fmac_f32_e32 v3, 0xba000000, v112
	v_pk_fma_f32 v[142:143], v[0:1], v[0:1], v[6:7] op_sel_hi:[1,1,0]
	v_mul_f32_e32 v6, v2, v2
	v_pk_add_f32 v[140:141], v[140:141], v[140:141] op_sel_hi:[0,1]
	v_pk_fma_f32 v[144:145], v[2:3], v[2:3], v[6:7] op_sel_hi:[1,1,0]
	v_fmac_f32_e32 v111, 0xba000000, v112
	v_fmac_f32_e32 v113, 0xba000000, v112
	v_fmac_f32_e32 v115, 0xba000000, v112
	v_fmac_f32_e32 v114, 0xba000000, v112
	v_mul_f32_e32 v142, v114, v114
	v_mul_f32_e32 v144, v115, v115
	v_mul_f32_e32 v140, v113, v113
	v_mul_f32_e32 v138, v111, v111
	v_pk_add_f32 v[142:143], v[142:143], v[144:145]
	v_pk_add_f32 v[138:139], v[140:141], v[138:139]
	s_nop 0
	v_pk_add_f32 v[138:139], v[142:143], v[138:139]
	s_nop 0
	v_add_f32_e32 v6, v138, v139
	v_mbcnt_lo_u32_b32 v138, -1, 0
	v_mbcnt_hi_u32_b32 v138, -1, v138
	v_ashrrev_i32_e32 v139, 31, v138
	v_lshl_add_u64 v[138:139], v[138:139], 4, s[12:13]
	v_mbcnt_lo_u32_b32 v142, -1, 0
	v_mbcnt_hi_u32_b32 v142, -1, v142
	s_waitcnt lgkmcnt(0)
	s_nop 1
	v_add_f32_dpp v6, v6, v6 quad_perm:[1,0,3,2] row_mask:0xf bank_mask:0xf
	v_ashrrev_i32_e32 v143, 31, v142
	v_lshl_add_u64 v[142:143], v[142:143], 4, s[14:15]
	s_waitcnt lgkmcnt(0)
	s_nop 1
	v_add_f32_dpp v6, v6, v6 quad_perm:[2,3,0,1] row_mask:0xf bank_mask:0xf
	s_waitcnt lgkmcnt(0)
	s_nop 1
	v_add_f32_dpp v6, v6, v6 row_half_mirror row_mask:0xf bank_mask:0xf
	s_waitcnt lgkmcnt(0)
	s_nop 1
	v_add_f32_dpp v6, v6, v6 row_mirror row_mask:0xf bank_mask:0xf
	s_waitcnt lgkmcnt(0)
	v_mov_b32_e32 v32, v6
	s_nop 1
	v_permlane16_swap_b32_e32 v6, v32
	v_add_f32_e32 v6, v6, v32
	s_waitcnt lgkmcnt(0)
; #define GAS __attribute__((address_space(1)))
; #define FLANE lane_id()
; __device__ __forceinline__ void p6_router(Frame& F) {
;     ...
;                 const float rstd = 1.f / sqrtf(wave_sum(s2) * (1.f / D) + LN_EPS);
;                 float am = 0.f;
; #pragma unroll
;                 for (int j = 0; j < 8; ++j) { const f32x4 g = *((const GAS f32x4*)F.ln1_g + FLANE + 64 * j), b = *((const GAS f32x4*)F.ln1_b + FLANE + 64 * j);
;                     v[j] = v[j] * rstd * g + b; am = fmaxf(am, fmaxf(fmaxf(fabsf(v[j][0]), fabsf(v[j][1])), fmaxf(fabsf(v[j][2]), fabsf(v[j][3])))); }
	v_mov_b32_e32 v32, v6
	s_nop 1
	v_permlane32_swap_b32_e32 v6, v32
	v_add_f32_e32 v6, v6, v32
	v_fmamk_f32 v6, v6, 0x3a000000, v166
	v_cmp_gt_f32_e32 vcc, s22, v6
	v_mul_f32_e32 v32, 0x4f800000, v6
	s_nop 0
	v_cndmask_b32_e32 v6, v6, v32, vcc
	v_sqrt_f32_e32 v32, v6
	s_nop 0
	v_add_u32_e32 v110, -1, v32
	v_fma_f32 v130, -v110, v32, v6
	v_cmp_ge_f32_e64 s[4:5], 0, v130
	v_add_u32_e32 v130, 1, v32
	s_nop 0
	v_cndmask_b32_e64 v110, v32, v110, s[4:5]
	v_fma_f32 v32, -v130, v32, v6
	v_cmp_lt_f32_e64 s[4:5], 0, v32
	s_nop 1
	v_cndmask_b32_e64 v32, v110, v130, s[4:5]
	v_mul_f32_e32 v110, 0x37800000, v32
	v_cndmask_b32_e32 v32, v32, v110, vcc
	v_cmp_class_f32_e32 vcc, v6, v167
	s_nop 1
	v_cndmask_b32_e32 v6, v32, v6, vcc
	v_div_scale_f32 v32, s[4:5], v6, v6, 1.0
	v_rcp_f32_e32 v110, v32
	s_add_i32 s4, s42, s0
	s_ashr_i32 s5, s4, 31
	v_fma_f32 v130, -v32, v110, 1.0
	v_fmac_f32_e32 v110, v130, v110
	v_div_scale_f32 v130, vcc, 1.0, v6, 1.0
	v_mul_f32_e32 v132, v130, v110
	v_fma_f32 v134, -v32, v132, v130
	v_fmac_f32_e32 v132, v134, v110
	v_fma_f32 v32, -v32, v132, v130
	v_div_fmas_f32 v32, v32, v110, v132
	v_div_fixup_f32 v32, v32, v6, 1.0
	v_pk_mul_f32 v[146:147], v[108:109], v[32:33] op_sel_hi:[1,0]
	v_pk_mul_f32 v[108:109], v[116:117], v[32:33] op_sel_hi:[1,0]
	v_mov_b32_e32 v134, v7
	v_pk_mul_f32 v[4:5], v[4:5], v[32:33] op_sel_hi:[1,0]
	v_pk_mul_f32 v[2:3], v[2:3], v[32:33] op_sel_hi:[1,0]
	v_pk_mul_f32 v[0:1], v[0:1], v[32:33] op_sel_hi:[1,0]
	v_pk_mul_f32 v[114:115], v[114:115], v[32:33] op_sel_hi:[1,0]
	s_waitcnt vmcnt(0)
	v_pk_fma_f32 v[116:117], v[196:197], v[146:147], v[228:229]
	v_mbcnt_lo_u32_b32 v138, -1, 0
	v_mbcnt_hi_u32_b32 v138, -1, v138
	v_pk_fma_f32 v[108:109], v[198:199], v[108:109], v[230:231]
	v_ashrrev_i32_e32 v139, 31, v138
	v_lshl_add_u64 v[138:139], v[138:139], 4, s[12:13]
	v_mbcnt_lo_u32_b32 v142, -1, 0
	v_mbcnt_hi_u32_b32 v142, -1, v142
	v_pk_mul_f32 v[146:147], v[118:119], v[32:33] op_sel_hi:[1,0]
	v_ashrrev_i32_e32 v143, 31, v142
	v_lshl_add_u64 v[142:143], v[142:143], 4, s[14:15]
	v_pk_mul_f32 v[118:119], v[120:121], v[32:33] op_sel_hi:[1,0]
	v_max_f32_e64 v6, |v108|, |v109|
	v_max3_f32 v6, |v116|, |v117|, v6
	s_waitcnt vmcnt(0)
	v_pk_fma_f32 v[120:121], v[200:201], v[146:147], v[232:233]
	v_mbcnt_lo_u32_b32 v138, -1, 0
	v_mbcnt_hi_u32_b32 v138, -1, v138
	v_pk_fma_f32 v[118:119], v[202:203], v[118:119], v[234:235]
	v_ashrrev_i32_e32 v139, 31, v138
	v_lshl_add_u64 v[138:139], v[138:139], 4, s[12:13]
	v_mbcnt_lo_u32_b32 v142, -1, 0
	v_mbcnt_hi_u32_b32 v142, -1, v142
	v_pk_mul_f32 v[146:147], v[122:123], v[32:33] op_sel_hi:[1,0]
	v_ashrrev_i32_e32 v143, 31, v142
	v_lshl_add_u64 v[142:143], v[142:143], 4, s[14:15]
	v_pk_mul_f32 v[122:123], v[124:125], v[32:33] op_sel_hi:[1,0]
	v_max_f32_e64 v110, |v118|, |v119|
	v_max3_f32 v110, |v120|, |v121|, v110
	v_max3_f32 v6, v6, 0, v110
	s_waitcnt vmcnt(0)
	v_pk_fma_f32 v[124:125], v[204:205], v[146:147], v[236:237]
	v_mbcnt_lo_u32_b32 v138, -1, 0
	v_mbcnt_hi_u32_b32 v138, -1, v138
	v_pk_fma_f32 v[122:123], v[206:207], v[122:123], v[238:239]
	v_ashrrev_i32_e32 v139, 31, v138
	v_lshl_add_u64 v[138:139], v[138:139], 4, s[12:13]
	v_mbcnt_lo_u32_b32 v142, -1, 0
	v_mbcnt_hi_u32_b32 v142, -1, v142
	v_pk_mul_f32 v[146:147], v[126:127], v[32:33] op_sel_hi:[1,0]
	v_ashrrev_i32_e32 v143, 31, v142
	v_lshl_add_u64 v[142:143], v[142:143], 4, s[14:15]
	v_pk_mul_f32 v[126:127], v[128:129], v[32:33] op_sel_hi:[1,0]
	v_max_f32_e64 v110, |v122|, |v123|
	v_max3_f32 v110, |v124|, |v125|, v110
	s_waitcnt vmcnt(0)
	v_pk_fma_f32 v[128:129], v[208:209], v[146:147], v[240:241]
	v_mbcnt_lo_u32_b32 v138, -1, 0
	v_mbcnt_hi_u32_b32 v138, -1, v138
	v_pk_fma_f32 v[126:127], v[210:211], v[126:127], v[242:243]
	v_ashrrev_i32_e32 v139, 31, v138
	v_lshl_add_u64 v[138:139], v[138:139], 4, s[12:13]
	v_add_co_u32_e32 v138, vcc, s23, v138
	v_max_f32_e64 v130, |v126|, |v127|
	s_nop 0
	v_addc_co_u32_e32 v139, vcc, 0, v139, vcc
	v_mbcnt_lo_u32_b32 v142, -1, 0
	v_mbcnt_hi_u32_b32 v142, -1, v142
	v_max3_f32 v130, |v128|, |v129|, v130
	v_ashrrev_i32_e32 v143, 31, v142
	v_lshl_add_u64 v[142:143], v[142:143], 4, s[14:15]
	v_add_co_u32_e32 v142, vcc, s23, v142
	v_max3_f32 v110, v6, v110, v130
	s_nop 0
	v_addc_co_u32_e32 v143, vcc, 0, v143, vcc
	v_mov_b32_e32 v130, v133
	v_pk_mul_f32 v[130:131], v[130:131], v[32:33] op_sel_hi:[1,0]
	v_pk_mul_f32 v[6:7], v[134:135], v[32:33] op_sel_hi:[1,0]
	s_waitcnt vmcnt(0)
	v_pk_fma_f32 v[130:131], v[214:215], v[130:131], v[246:247]
	v_pk_fma_f32 v[132:133], v[212:213], v[6:7], v[244:245]
	v_max_f32_e64 v6, |v130|, |v131|
	v_max3_f32 v146, |v132|, |v133|, v6
	v_mbcnt_lo_u32_b32 v6, -1, 0
	v_mbcnt_hi_u32_b32 v6, -1, v6
	s_nop 0
	v_ashrrev_i32_e32 v7, 31, v6
	v_lshl_add_u64 v[6:7], v[6:7], 4, s[12:13]
	v_add_co_u32_e32 v6, vcc, s23, v6
	s_nop 1
	v_addc_co_u32_e32 v7, vcc, 0, v7, vcc
	v_mbcnt_lo_u32_b32 v6, -1, 0
	v_mbcnt_hi_u32_b32 v6, -1, v6
	s_nop 0
	v_ashrrev_i32_e32 v7, 31, v6
	v_lshl_add_u64 v[6:7], v[6:7], 4, s[14:15]
	v_add_co_u32_e32 v6, vcc, s23, v6
	s_nop 1
	v_addc_co_u32_e32 v7, vcc, 0, v7, vcc
	v_pk_mul_f32 v[6:7], v[136:137], v[32:33] op_sel_hi:[1,0]
	s_waitcnt vmcnt(0)
	v_pk_fma_f32 v[136:137], v[216:217], v[4:5], v[248:249]
	v_pk_fma_f32 v[134:135], v[218:219], v[6:7], v[250:251]
	s_nop 0
	v_max_f32_e64 v4, |v134|, |v135|
	v_max3_f32 v4, |v136|, |v137|, v4
	v_max3_f32 v144, v110, v146, v4
	v_mbcnt_lo_u32_b32 v4, -1, 0
	v_mbcnt_hi_u32_b32 v4, -1, v4
	v_mov_b32_e32 v110, v113
	v_ashrrev_i32_e32 v5, 31, v4
	v_lshl_add_u64 v[4:5], v[4:5], 4, s[12:13]
	v_add_co_u32_e32 v4, vcc, s23, v4
	v_pk_mul_f32 v[110:111], v[110:111], v[32:33] op_sel_hi:[1,0]
	s_nop 0
	v_addc_co_u32_e32 v5, vcc, 0, v5, vcc
	v_mbcnt_lo_u32_b32 v138, -1, 0
	v_mbcnt_hi_u32_b32 v138, -1, v138
	s_nop 0
	v_ashrrev_i32_e32 v139, 31, v138
	v_lshl_add_u64 v[138:139], v[138:139], 4, s[14:15]
	v_add_co_u32_e32 v138, vcc, s23, v138
	s_nop 1
	v_addc_co_u32_e32 v139, vcc, 0, v139, vcc
	s_waitcnt vmcnt(0)
; #define FLANE lane_id()
; __device__ __forceinline__ void p6_router(Frame& F) {
;     ...
;                     v[j] = v[j] * rstd * g + b; am = fmaxf(am, fmaxf(fmaxf(fabsf(v[j][0]), fabsf(v[j][1])), fmaxf(fabsf(v[j][2]), fabsf(v[j][3])))); }
; #pragma unroll
;                 for (int o = 1; o < 64; o <<= 1) am = fmaxf(am, __shfl_xor(am, o));
;                 const float sc = am > 0.f ? am * (1.f / 127.f) : 1.f, inv = 1.f / sc;
; #pragma unroll
;                 for (int j = 0; j < 8; ++j) { const int q0 = (int)__builtin_rintf(v[j][0] * inv), q1 = (int)__builtin_rintf(v[j][1] * inv), q2 = (int)__builtin_rintf(v[j][2] * inv), q3 = (int)__builtin_rintf(v[j][3] * inv);
;                     h1q[(size_t)m * (D / 4) + FLANE + 64 * j] = (unsigned)(q0 & 0xff) | ((unsigned)(q1 & 0xff) << 8) | ((unsigned)(q2 & 0xff) << 16) | ((unsigned)(q3 & 0xff) << 24); }
	v_pk_fma_f32 v[138:139], v[2:3], v[222:223], v[184:185]
	v_pk_fma_f32 v[140:141], v[0:1], v[220:221], v[182:183]
	v_max_f32_e64 v0, |v138|, |v139|
	v_max3_f32 v142, |v140|, |v141|, v0
	v_mbcnt_lo_u32_b32 v0, -1, 0
	v_mbcnt_hi_u32_b32 v0, -1, v0
	s_nop 0
	v_ashrrev_i32_e32 v1, 31, v0
	v_lshl_add_u64 v[0:1], v[0:1], 4, s[12:13]
	v_add_co_u32_e32 v0, vcc, s23, v0
	s_nop 1
	v_addc_co_u32_e32 v1, vcc, 0, v1, vcc
	v_mbcnt_lo_u32_b32 v4, -1, 0
	v_mbcnt_hi_u32_b32 v4, -1, v4
	s_nop 0
	v_ashrrev_i32_e32 v5, 31, v4
	v_lshl_add_u64 v[4:5], v[4:5], 4, s[14:15]
	v_add_co_u32_e32 v4, vcc, s23, v4
	s_nop 1
	v_addc_co_u32_e32 v5, vcc, 0, v5, vcc
	s_waitcnt vmcnt(0)
	v_pk_fma_f32 v[2:3], v[110:111], v[226:227], v[188:189]
	v_pk_fma_f32 v[4:5], v[114:115], v[224:225], v[186:187]
	v_max_f32_e64 v0, |v2|, |v3|
	v_max3_f32 v0, |v4|, |v5|, v0
	v_max3_f32 v0, v144, v142, v0
	s_waitcnt lgkmcnt(0)
	s_nop 1
	v_max_f32_dpp v0, v0, v0 quad_perm:[1,0,3,2] row_mask:0xf bank_mask:0xf
	s_waitcnt lgkmcnt(0)
	s_nop 1
	v_max_f32_dpp v0, v0, v0 quad_perm:[2,3,0,1] row_mask:0xf bank_mask:0xf
	s_waitcnt lgkmcnt(0)
	s_nop 1
	v_max_f32_dpp v0, v0, v0 row_half_mirror row_mask:0xf bank_mask:0xf
	s_waitcnt lgkmcnt(0)
	s_nop 1
	v_max_f32_dpp v0, v0, v0 row_mirror row_mask:0xf bank_mask:0xf
	s_waitcnt lgkmcnt(0)
	v_mov_b32_e32 v1, v0
	s_nop 1
	v_permlane16_swap_b32_e32 v0, v1
	v_max_f32_e32 v0, v0, v1
	s_waitcnt lgkmcnt(0)
	v_mov_b32_e32 v1, v0
	s_nop 1
	v_permlane32_swap_b32_e32 v0, v1
	v_max_f32_e32 v0, v0, v1
	v_cmp_lt_f32_e32 vcc, 0, v0
	v_mul_f32_e32 v0, 0x3c010204, v0
	s_nop 0
	v_cndmask_b32_e32 v0, 1.0, v0, vcc
	v_div_scale_f32 v1, s[6:7], v0, v0, 1.0
	v_rcp_f32_e32 v6, v1
	s_lshl_b64 s[6:7], s[4:5], 11
	s_add_u32 s6, s3, s6
	s_addc_u32 s7, s24, s7
	v_fma_f32 v7, -v1, v6, 1.0
	v_fmac_f32_e32 v6, v7, v6
	v_div_scale_f32 v7, vcc, 1.0, v0, 1.0
	v_mul_f32_e32 v110, v7, v6
	v_fma_f32 v111, -v1, v110, v7
	v_fmac_f32_e32 v110, v111, v6
	v_fma_f32 v1, -v1, v110, v7
	v_div_fmas_f32 v1, v1, v6, v110
	v_div_fixup_f32 v1, v1, v0, 1.0
	v_mul_f32_e32 v7, v117, v1
	v_mul_f32_e32 v6, v116, v1
	v_rndne_f32_e32 v7, v7
	v_mul_f32_e32 v108, v108, v1
	v_mul_f32_e32 v109, v109, v1
	v_rndne_f32_e32 v6, v6
	v_cvt_i32_f32_e32 v7, v7
	v_rndne_f32_e32 v108, v108
	v_rndne_f32_e32 v109, v109
	v_cvt_i32_f32_e32 v6, v6
	v_cvt_i32_f32_sdwa v108, v108 dst_sel:WORD_1 dst_unused:UNUSED_PAD src0_sel:DWORD
	v_cvt_i32_f32_e32 v109, v109
	v_lshlrev_b32_e32 v7, 8, v7
	v_and_b32_e32 v7, 0xff00, v7
	v_and_b32_e32 v108, 0xff0000, v108
	v_perm_b32 v6, v109, v6, s1
	v_or3_b32 v108, v6, v7, v108
	v_mbcnt_lo_u32_b32 v6, -1, 0
	v_mbcnt_hi_u32_b32 v6, -1, v6
	v_mul_f32_e32 v109, v119, v1
	v_ashrrev_i32_e32 v7, 31, v6
	v_lshl_add_u64 v[6:7], v[6:7], 2, s[6:7]
	global_store_dword v[6:7], v108, off
	v_mul_f32_e32 v7, v121, v1
	v_mul_f32_e32 v6, v120, v1
	v_rndne_f32_e32 v7, v7
	v_mul_f32_e32 v108, v118, v1
	v_rndne_f32_e32 v6, v6
	v_cvt_i32_f32_e32 v7, v7
	v_rndne_f32_e32 v108, v108
	v_rndne_f32_e32 v109, v109
	v_cvt_i32_f32_e32 v6, v6
	v_cvt_i32_f32_sdwa v108, v108 dst_sel:WORD_1 dst_unused:UNUSED_PAD src0_sel:DWORD
	v_cvt_i32_f32_e32 v109, v109
	v_lshlrev_b32_e32 v7, 8, v7
	v_and_b32_e32 v7, 0xff00, v7
	v_and_b32_e32 v108, 0xff0000, v108
	v_perm_b32 v6, v109, v6, s1
	v_or3_b32 v108, v6, v7, v108
	v_mbcnt_lo_u32_b32 v6, -1, 0
	v_mbcnt_hi_u32_b32 v6, -1, v6
	v_mul_f32_e32 v109, v123, v1
	v_ashrrev_i32_e32 v7, 31, v6
	v_lshl_add_u64 v[6:7], v[6:7], 2, s[6:7]
	global_store_dword v[6:7], v108, off offset:256
	v_mul_f32_e32 v7, v125, v1
	v_mul_f32_e32 v6, v124, v1
	v_rndne_f32_e32 v7, v7
	v_mul_f32_e32 v108, v122, v1
	v_rndne_f32_e32 v6, v6
	v_cvt_i32_f32_e32 v7, v7
	v_rndne_f32_e32 v108, v108
	v_rndne_f32_e32 v109, v109
	v_cvt_i32_f32_e32 v6, v6
	v_cvt_i32_f32_sdwa v108, v108 dst_sel:WORD_1 dst_unused:UNUSED_PAD src0_sel:DWORD
	v_cvt_i32_f32_e32 v109, v109
	v_lshlrev_b32_e32 v7, 8, v7
	v_and_b32_e32 v7, 0xff00, v7
	v_and_b32_e32 v108, 0xff0000, v108
	v_perm_b32 v6, v109, v6, s1
	v_or3_b32 v108, v6, v7, v108
	v_mbcnt_lo_u32_b32 v6, -1, 0
	v_mbcnt_hi_u32_b32 v6, -1, v6
	v_mul_f32_e32 v109, v127, v1
	v_ashrrev_i32_e32 v7, 31, v6
	v_lshl_add_u64 v[6:7], v[6:7], 2, s[6:7]
	global_store_dword v[6:7], v108, off offset:512
	v_mul_f32_e32 v7, v129, v1
	v_mul_f32_e32 v6, v128, v1
	v_rndne_f32_e32 v7, v7
	v_mul_f32_e32 v108, v126, v1
	v_rndne_f32_e32 v6, v6
	v_cvt_i32_f32_e32 v7, v7
	v_rndne_f32_e32 v108, v108
	v_rndne_f32_e32 v109, v109
	v_cvt_i32_f32_e32 v6, v6
	v_cvt_i32_f32_sdwa v108, v108 dst_sel:WORD_1 dst_unused:UNUSED_PAD src0_sel:DWORD
	v_cvt_i32_f32_e32 v109, v109
	v_lshlrev_b32_e32 v7, 8, v7
	v_and_b32_e32 v7, 0xff00, v7
	v_and_b32_e32 v108, 0xff0000, v108
	v_perm_b32 v6, v109, v6, s1
	v_or3_b32 v108, v6, v7, v108
	v_mbcnt_lo_u32_b32 v6, -1, 0
	v_mbcnt_hi_u32_b32 v6, -1, v6
	v_mul_f32_e32 v109, v131, v1
	v_ashrrev_i32_e32 v7, 31, v6
	v_lshl_add_u64 v[6:7], v[6:7], 2, s[6:7]
	global_store_dword v[6:7], v108, off offset:768
	v_mul_f32_e32 v7, v133, v1
	v_mul_f32_e32 v6, v132, v1
	v_rndne_f32_e32 v7, v7
	v_mul_f32_e32 v108, v130, v1
	v_rndne_f32_e32 v6, v6
	v_cvt_i32_f32_e32 v7, v7
	v_rndne_f32_e32 v108, v108
	v_rndne_f32_e32 v109, v109
	v_cvt_i32_f32_e32 v6, v6
	v_cvt_i32_f32_sdwa v108, v108 dst_sel:WORD_1 dst_unused:UNUSED_PAD src0_sel:DWORD
	v_cvt_i32_f32_e32 v109, v109
	v_lshlrev_b32_e32 v7, 8, v7
	v_and_b32_e32 v7, 0xff00, v7
	v_and_b32_e32 v108, 0xff0000, v108
	v_perm_b32 v6, v109, v6, s1
	v_or3_b32 v108, v6, v7, v108
	v_mbcnt_lo_u32_b32 v6, -1, 0
	v_mbcnt_hi_u32_b32 v6, -1, v6
	v_mul_f32_e32 v109, v135, v1
	v_ashrrev_i32_e32 v7, 31, v6
	v_lshl_add_u64 v[6:7], v[6:7], 2, s[6:7]
	global_store_dword v[6:7], v108, off offset:1024
; #define FLANE lane_id()
; __device__ __forceinline__ void p6_router(Frame& F) {
;     ...
;             for (int rr = 0; rr < 8; ++rr) { const int row = F.wave * 8 + rr, m = t0 + row;
;                 f32x4 v[8]; float s = 0.f;
; #pragma unroll
;                 for (int j = 0; j < 8; ++j) { const v2u w = raw[rr][j]; v[j] = (f32x4){bf_lo(w.x), bf_hi(w.x), bf_lo(w.y), bf_hi(w.y)}; s += (v[j][0] + v[j][1]) + (v[j][2] + v[j][3]); }
;                 const float mean = wave_sum(s) * (1.f / D); float s2 = 0.f;
;     ...
;                     h1q[(size_t)m * (D / 4) + FLANE + 64 * j] = (unsigned)(q0 & 0xff) | ((unsigned)(q1 & 0xff) << 8) | ((unsigned)(q2 & 0xff) << 16) | ((unsigned)(q3 & 0xff) << 24); }
;                 if (FLANE == 0) { st1[2 * m] = mean; st1[2 * m + 1] = rstd; stl[2 * row] = mean; stl[2 * row + 1] = rstd; sxg[m] = sc; sxl[row] = sc; }
	v_mul_f32_e32 v7, v137, v1
	v_mul_f32_e32 v6, v136, v1
	v_rndne_f32_e32 v7, v7
	v_mul_f32_e32 v108, v134, v1
	v_rndne_f32_e32 v6, v6
	v_cvt_i32_f32_e32 v7, v7
	v_rndne_f32_e32 v108, v108
	v_rndne_f32_e32 v109, v109
	v_cvt_i32_f32_e32 v6, v6
	v_cvt_i32_f32_sdwa v108, v108 dst_sel:WORD_1 dst_unused:UNUSED_PAD src0_sel:DWORD
	v_cvt_i32_f32_e32 v109, v109
	v_lshlrev_b32_e32 v7, 8, v7
	v_and_b32_e32 v7, 0xff00, v7
	v_and_b32_e32 v108, 0xff0000, v108
	v_perm_b32 v6, v109, v6, s1
	v_or3_b32 v108, v6, v7, v108
	v_mbcnt_lo_u32_b32 v6, -1, 0
	v_mbcnt_hi_u32_b32 v6, -1, v6
	v_mul_f32_e32 v109, v139, v1
	v_ashrrev_i32_e32 v7, 31, v6
	v_lshl_add_u64 v[6:7], v[6:7], 2, s[6:7]
	global_store_dword v[6:7], v108, off offset:1280
	v_mul_f32_e32 v7, v141, v1
	v_mul_f32_e32 v6, v140, v1
	v_rndne_f32_e32 v7, v7
	v_mul_f32_e32 v108, v138, v1
	v_rndne_f32_e32 v6, v6
	v_cvt_i32_f32_e32 v7, v7
	v_rndne_f32_e32 v108, v108
	v_rndne_f32_e32 v109, v109
	v_mul_f32_e32 v5, v5, v1
	v_cvt_i32_f32_e32 v6, v6
	v_cvt_i32_f32_sdwa v108, v108 dst_sel:WORD_1 dst_unused:UNUSED_PAD src0_sel:DWORD
	v_cvt_i32_f32_e32 v109, v109
	v_mul_f32_e32 v4, v4, v1
	v_rndne_f32_e32 v5, v5
	v_mul_f32_e32 v2, v2, v1
	v_mul_f32_e32 v1, v3, v1
	v_rndne_f32_e32 v4, v4
	v_cvt_i32_f32_e32 v5, v5
	v_rndne_f32_e32 v2, v2
	v_rndne_f32_e32 v1, v1
	v_cvt_i32_f32_e32 v4, v4
	v_cvt_i32_f32_sdwa v2, v2 dst_sel:WORD_1 dst_unused:UNUSED_PAD src0_sel:DWORD
	v_cvt_i32_f32_e32 v1, v1
	v_lshlrev_b32_e32 v7, 8, v7
	v_and_b32_e32 v7, 0xff00, v7
	v_and_b32_e32 v108, 0xff0000, v108
	v_perm_b32 v6, v109, v6, s1
	v_or3_b32 v108, v6, v7, v108
	v_mbcnt_lo_u32_b32 v6, -1, 0
	v_mbcnt_hi_u32_b32 v6, -1, v6
	v_lshlrev_b32_e32 v3, 8, v5
	v_ashrrev_i32_e32 v7, 31, v6
	v_lshl_add_u64 v[6:7], v[6:7], 2, s[6:7]
	v_and_b32_e32 v3, 0xff00, v3
	v_and_b32_e32 v2, 0xff0000, v2
	v_perm_b32 v1, v1, v4, s1
	global_store_dword v[6:7], v108, off offset:1536
	v_or3_b32 v1, v1, v3, v2
	v_mbcnt_lo_u32_b32 v2, -1, 0
	v_mbcnt_hi_u32_b32 v2, -1, v2
	s_nop 0
	v_ashrrev_i32_e32 v3, 31, v2
	v_lshl_add_u64 v[2:3], v[2:3], 2, s[6:7]
	global_store_dword v[2:3], v1, off offset:1792
	v_mbcnt_lo_u32_b32 v1, -1, 0
	v_mbcnt_hi_u32_b32 v1, -1, v1
	s_nop 0
	v_cmp_eq_u32_e32 vcc, 0, v1
	s_and_saveexec_b64 s[6:7], vcc
	s_cbranch_execz .LBB0_1485
	s_lshl_b32 s8, s4, 1
	s_ashr_i32 s9, s8, 31
	s_lshl_b64 s[8:9], s[8:9], 2
	s_add_u32 s8, s27, s8
	s_addc_u32 s9, s64, s9
	v_readlane_b32 s0, v255, 42
	s_lshl_b64 s[4:5], s[4:5], 2
	v_mul_f32_e32 v2, 0x3a000000, v112
	v_mov_b32_e32 v3, v32
	v_mov_b32_e32 v1, s0
	s_add_u32 s4, s25, s4
	v_readlane_b32 s0, v255, 24
	ds_write_b64 v1, v[2:3]
	s_addc_u32 s5, s26, s5
	v_mov_b32_e32 v1, s0
	global_store_dwordx2 v33, v[2:3], s[8:9]
	global_store_dword v33, v0, s[4:5]
	ds_write_b32 v1, v0
.LBB0_1485:
	s_or_b64 exec, exec, s[6:7]
	v_lshlrev_b32_e32 v109, 16, v106
	v_lshlrev_b32_e32 v108, 16, v104
	v_and_b32_e32 v121, 0xffff0000, v106
	v_and_b32_e32 v120, 0xffff0000, v104
	v_lshlrev_b32_e32 v123, 16, v107
	v_lshlrev_b32_e32 v122, 16, v105
	v_and_b32_e32 v125, 0xffff0000, v107
	v_and_b32_e32 v124, 0xffff0000, v105
	v_pk_add_f32 v[0:1], v[108:109], v[120:121]
	v_pk_add_f32 v[2:3], v[122:123], v[124:125]
	v_lshlrev_b32_e32 v107, 16, v103
	v_pk_add_f32 v[0:1], v[0:1], v[2:3]
	v_lshlrev_b32_e32 v106, 16, v102
	v_add_f32_e32 v0, 0, v0
	v_and_b32_e32 v127, 0xffff0000, v103
	v_and_b32_e32 v126, 0xffff0000, v102
	v_add_f32_e32 v6, v0, v1
	v_pk_add_f32 v[0:1], v[106:107], v[126:127]
	v_lshlrev_b32_e32 v110, 16, v100
	v_and_b32_e32 v111, 0xffff0000, v100
	v_lshlrev_b32_e32 v112, 16, v101
	v_and_b32_e32 v113, 0xffff0000, v101
	v_and_b32_e32 v119, 0xffff0000, v98
	v_pk_add_f32 v[0:1], v[0:1], v[0:1] op_sel:[0,1] op_sel_hi:[1,0]
	v_add_f32_e32 v116, v110, v111
	v_add_f32_e32 v114, v112, v113
	v_lshlrev_b32_e32 v7, 16, v98
	v_lshlrev_b32_e32 v117, 16, v99
	v_and_b32_e32 v115, 0xffff0000, v99
	v_mov_b32_e32 v1, v119
	v_pk_add_f32 v[0:1], v[6:7], v[0:1]
	v_pk_add_f32 v[2:3], v[116:117], v[114:115]
	v_lshlrev_b32_e32 v5, 16, v97
	v_lshlrev_b32_e32 v4, 16, v96
	v_and_b32_e32 v129, 0xffff0000, v97
	v_and_b32_e32 v128, 0xffff0000, v96
	v_pk_add_f32 v[100:101], v[0:1], v[2:3]
	v_pk_add_f32 v[102:103], v[4:5], v[128:129]
	v_lshlrev_b32_e32 v0, 16, v94
	v_and_b32_e32 v1, 0xffff0000, v94
	v_lshlrev_b32_e32 v2, 16, v95
	v_and_b32_e32 v3, 0xffff0000, v95
	v_lshlrev_b32_e32 v98, 16, v92
	v_and_b32_e32 v99, 0xffff0000, v92
	v_lshlrev_b32_e32 v97, 16, v93
	v_and_b32_e32 v95, 0xffff0000, v93
	v_pk_add_f32 v[92:93], v[100:101], v[100:101] op_sel:[0,1] op_sel_hi:[1,0]
	v_pk_add_f32 v[100:101], v[102:103], v[102:103] op_sel:[0,1] op_sel_hi:[1,0]
	v_add_f32_e32 v96, v0, v1
	v_add_f32_e32 v94, v2, v3
	v_mov_b32_e32 v93, v98
	v_mov_b32_e32 v101, v99
	v_pk_add_f32 v[92:93], v[92:93], v[100:101]
	v_pk_add_f32 v[100:101], v[96:97], v[94:95]
	v_readlane_b32 s0, v255, 18
	v_pk_add_f32 v[92:93], v[92:93], v[100:101]
	s_nop 0
	v_add_f32_e32 v6, v92, v93
	s_waitcnt lgkmcnt(0)
	s_nop 1
	v_add_f32_dpp v6, v6, v6 quad_perm:[1,0,3,2] row_mask:0xf bank_mask:0xf
	s_waitcnt lgkmcnt(0)
	s_nop 1
	v_add_f32_dpp v6, v6, v6 quad_perm:[2,3,0,1] row_mask:0xf bank_mask:0xf
	s_waitcnt lgkmcnt(0)
	s_nop 1
	v_add_f32_dpp v6, v6, v6 row_half_mirror row_mask:0xf bank_mask:0xf
	s_waitcnt lgkmcnt(0)
	s_nop 1
	v_add_f32_dpp v6, v6, v6 row_mirror row_mask:0xf bank_mask:0xf
	s_waitcnt lgkmcnt(0)
	v_mov_b32_e32 v32, v6
	s_nop 1
	v_permlane16_swap_b32_e32 v6, v32
	v_add_f32_e32 v6, v6, v32
	s_waitcnt lgkmcnt(0)
; #define GAS __attribute__((address_space(1)))
; #define FLANE lane_id()
; __device__ __forceinline__ void p6_router(Frame& F) {
;     ...
;                 const float mean = wave_sum(s) * (1.f / D); float s2 = 0.f;
; #pragma unroll
;                 for (int j = 0; j < 8; ++j) { v[j] = v[j] - mean; s2 += (v[j][0] * v[j][0] + v[j][1] * v[j][1]) + (v[j][2] * v[j][2] + v[j][3] * v[j][3]); }
;                 const float rstd = 1.f / sqrtf(wave_sum(s2) * (1.f / D) + LN_EPS);
;                 float am = 0.f;
; #pragma unroll
;                 for (int j = 0; j < 8; ++j) { const f32x4 g = *((const GAS f32x4*)F.ln1_g + FLANE + 64 * j), b = *((const GAS f32x4*)F.ln1_b + FLANE + 64 * j);
	v_mov_b32_e32 v32, v6
	s_nop 1
	v_permlane32_swap_b32_e32 v6, v32
	v_add_f32_e32 v96, v6, v32
	v_fmac_f32_e32 v124, 0xba000000, v96
	v_fmac_f32_e32 v120, 0xba000000, v96
	v_fmac_f32_e32 v125, 0xba000000, v96
	v_fmac_f32_e32 v121, 0xba000000, v96
	v_fmac_f32_e32 v122, 0xba000000, v96
	v_fmac_f32_e32 v108, 0xba000000, v96
	v_fmac_f32_e32 v123, 0xba000000, v96
	v_fmac_f32_e32 v109, 0xba000000, v96
	v_mov_b32_e32 v103, v121
	v_mov_b32_e32 v93, v120
	v_pk_mul_f32 v[100:101], v[120:121], v[120:121]
	v_pk_mul_f32 v[120:121], v[124:125], v[124:125]
	v_mov_b32_e32 v102, v109
	v_mov_b32_e32 v92, v108
	v_pk_fma_f32 v[108:109], v[108:109], v[108:109], v[100:101]
	v_pk_fma_f32 v[120:121], v[122:123], v[122:123], v[120:121]
	v_fmac_f32_e32 v126, 0xba000000, v96
	v_pk_add_f32 v[108:109], v[108:109], v[120:121]
	v_fmac_f32_e32 v127, 0xba000000, v96
	v_fmac_f32_e32 v107, 0xba000000, v96
	v_pk_add_f32 v[120:121], v[108:109], v[108:109] op_sel_hi:[0,1]
	v_fmac_f32_e32 v106, 0xba000000, v96
	v_mov_b32_e32 v108, v107
	v_mov_b32_e32 v109, v127
	v_mov_b32_e32 v107, v126
	v_mov_b32_e32 v104, v123
	v_mov_b32_e32 v105, v125
	v_mov_b32_e32 v100, v122
	v_mov_b32_e32 v101, v124
	v_pk_mul_f32 v[122:123], v[108:109], v[108:109]
	v_pk_mul_f32 v[124:125], v[106:107], v[106:107]
	v_fmac_f32_e32 v110, 0xba000000, v96
	v_pk_mov_b32 v[126:127], v[124:125], v[122:123] op_sel:[1,0]
	v_mov_b32_e32 v125, v123
	v_fmac_f32_e32 v111, 0xba000000, v96
	v_fmac_f32_e32 v112, 0xba000000, v96
	v_mul_f32_e32 v6, v110, v110
	v_pk_add_f32 v[122:123], v[126:127], v[124:125]
	v_fmac_f32_e32 v113, 0xba000000, v96
	v_pk_fma_f32 v[124:125], v[110:111], v[110:111], v[6:7] op_sel_hi:[1,1,0]
	v_mul_f32_e32 v6, v112, v112
	v_pk_add_f32 v[122:123], v[122:123], v[122:123] op_sel_hi:[0,1]
	v_pk_fma_f32 v[126:127], v[112:113], v[112:113], v[6:7] op_sel_hi:[1,1,0]
	v_fmac_f32_e32 v115, 0xba000000, v96
	v_fmac_f32_e32 v117, 0xba000000, v96
	v_fmac_f32_e32 v119, 0xba000000, v96
	v_fmac_f32_e32 v7, 0xba000000, v96
	v_mul_f32_e32 v124, v7, v7
	v_mul_f32_e32 v126, v119, v119
	v_mul_f32_e32 v122, v117, v117
	v_mul_f32_e32 v120, v115, v115
	v_pk_add_f32 v[124:125], v[124:125], v[126:127]
	v_pk_add_f32 v[120:121], v[122:123], v[120:121]
	v_fmac_f32_e32 v128, 0xba000000, v96
	v_pk_add_f32 v[120:121], v[124:125], v[120:121]
	v_fmac_f32_e32 v129, 0xba000000, v96
	v_fmac_f32_e32 v5, 0xba000000, v96
	v_pk_add_f32 v[122:123], v[120:121], v[120:121] op_sel_hi:[0,1]
	v_fmac_f32_e32 v4, 0xba000000, v96
	v_mov_b32_e32 v120, v5
	v_mov_b32_e32 v121, v129
	v_mov_b32_e32 v5, v128
	v_pk_mul_f32 v[124:125], v[120:121], v[120:121]
	v_pk_mul_f32 v[126:127], v[4:5], v[4:5]
	v_fmac_f32_e32 v0, 0xba000000, v96
	v_pk_mov_b32 v[128:129], v[126:127], v[124:125] op_sel:[1,0]
	v_mov_b32_e32 v127, v125
	v_fmac_f32_e32 v1, 0xba000000, v96
	v_fmac_f32_e32 v2, 0xba000000, v96
	v_mul_f32_e32 v6, v0, v0
	v_pk_add_f32 v[124:125], v[128:129], v[126:127]
	v_fmac_f32_e32 v3, 0xba000000, v96
	v_pk_fma_f32 v[126:127], v[0:1], v[0:1], v[6:7] op_sel_hi:[1,1,0]
	v_mul_f32_e32 v6, v2, v2
	v_pk_add_f32 v[124:125], v[124:125], v[124:125] op_sel_hi:[0,1]
	v_pk_fma_f32 v[128:129], v[2:3], v[2:3], v[6:7] op_sel_hi:[1,1,0]
	v_fmac_f32_e32 v95, 0xba000000, v96
	v_fmac_f32_e32 v97, 0xba000000, v96
	v_fmac_f32_e32 v99, 0xba000000, v96
	v_fmac_f32_e32 v98, 0xba000000, v96
	v_mul_f32_e32 v126, v98, v98
	v_mul_f32_e32 v128, v99, v99
	v_mul_f32_e32 v124, v97, v97
	v_mul_f32_e32 v122, v95, v95
	v_pk_add_f32 v[126:127], v[126:127], v[128:129]
	v_pk_add_f32 v[122:123], v[124:125], v[122:123]
	s_nop 0
	v_pk_add_f32 v[122:123], v[126:127], v[122:123]
	s_nop 0
	v_add_f32_e32 v6, v122, v123
	v_mbcnt_lo_u32_b32 v122, -1, 0
	v_mbcnt_hi_u32_b32 v122, -1, v122
	v_ashrrev_i32_e32 v123, 31, v122
	v_lshl_add_u64 v[122:123], v[122:123], 4, s[12:13]
	v_mbcnt_lo_u32_b32 v126, -1, 0
	v_mbcnt_hi_u32_b32 v126, -1, v126
	s_waitcnt lgkmcnt(0)
	s_nop 1
	v_add_f32_dpp v6, v6, v6 quad_perm:[1,0,3,2] row_mask:0xf bank_mask:0xf
	v_ashrrev_i32_e32 v127, 31, v126
	v_lshl_add_u64 v[126:127], v[126:127], 4, s[14:15]
	s_waitcnt lgkmcnt(0)
	s_nop 1
	v_add_f32_dpp v6, v6, v6 quad_perm:[2,3,0,1] row_mask:0xf bank_mask:0xf
	s_waitcnt lgkmcnt(0)
	s_nop 1
	v_add_f32_dpp v6, v6, v6 row_half_mirror row_mask:0xf bank_mask:0xf
	s_waitcnt lgkmcnt(0)
	s_nop 1
	v_add_f32_dpp v6, v6, v6 row_mirror row_mask:0xf bank_mask:0xf
	s_waitcnt lgkmcnt(0)
	v_mov_b32_e32 v32, v6
	s_nop 1
	v_permlane16_swap_b32_e32 v6, v32
	v_add_f32_e32 v6, v6, v32
	s_waitcnt lgkmcnt(0)
	v_mov_b32_e32 v32, v6
	s_nop 1
	v_permlane32_swap_b32_e32 v6, v32
	v_add_f32_e32 v6, v6, v32
	v_fmamk_f32 v6, v6, 0x3a000000, v166
	v_cmp_gt_f32_e32 vcc, s22, v6
	v_mul_f32_e32 v32, 0x4f800000, v6
	s_nop 0
	v_cndmask_b32_e32 v6, v6, v32, vcc
	v_sqrt_f32_e32 v32, v6
	s_nop 0
	v_add_u32_e32 v94, -1, v32
	v_fma_f32 v114, -v94, v32, v6
	v_cmp_ge_f32_e64 s[4:5], 0, v114
	v_add_u32_e32 v114, 1, v32
	s_nop 0
	v_cndmask_b32_e64 v94, v32, v94, s[4:5]
	v_fma_f32 v32, -v114, v32, v6
	v_cmp_lt_f32_e64 s[4:5], 0, v32
	s_nop 1
	v_cndmask_b32_e64 v32, v94, v114, s[4:5]
	v_mul_f32_e32 v94, 0x37800000, v32
	v_cndmask_b32_e32 v32, v32, v94, vcc
	v_cmp_class_f32_e32 vcc, v6, v167
	s_nop 1
	v_cndmask_b32_e32 v6, v32, v6, vcc
	v_div_scale_f32 v32, s[4:5], v6, v6, 1.0
	v_rcp_f32_e32 v94, v32
	s_add_i32 s4, s42, s0
	s_ashr_i32 s5, s4, 31
	v_fma_f32 v114, -v32, v94, 1.0
	v_fmac_f32_e32 v94, v114, v94
	v_div_scale_f32 v114, vcc, 1.0, v6, 1.0
	v_mul_f32_e32 v116, v114, v94
	v_fma_f32 v118, -v32, v116, v114
	v_fmac_f32_e32 v116, v118, v94
	v_fma_f32 v32, -v32, v116, v114
	v_div_fmas_f32 v32, v32, v94, v116
	v_div_fixup_f32 v32, v32, v6, 1.0
	v_pk_mul_f32 v[130:131], v[92:93], v[32:33] op_sel_hi:[1,0]
	v_pk_mul_f32 v[92:93], v[100:101], v[32:33] op_sel_hi:[1,0]
	v_mov_b32_e32 v118, v7
	v_pk_mul_f32 v[4:5], v[4:5], v[32:33] op_sel_hi:[1,0]
	v_pk_mul_f32 v[2:3], v[2:3], v[32:33] op_sel_hi:[1,0]
	v_pk_mul_f32 v[0:1], v[0:1], v[32:33] op_sel_hi:[1,0]
	v_pk_mul_f32 v[98:99], v[98:99], v[32:33] op_sel_hi:[1,0]
	s_waitcnt vmcnt(0)
; #define GAS __attribute__((address_space(1)))
; #define FLANE lane_id()
; __device__ __forceinline__ void p6_router(Frame& F) {
;     ...
;                 for (int j = 0; j < 8; ++j) { const f32x4 g = *((const GAS f32x4*)F.ln1_g + FLANE + 64 * j), b = *((const GAS f32x4*)F.ln1_b + FLANE + 64 * j);
;                     v[j] = v[j] * rstd * g + b; am = fmaxf(am, fmaxf(fmaxf(fabsf(v[j][0]), fabsf(v[j][1])), fmaxf(fabsf(v[j][2]), fabsf(v[j][3])))); }
	v_pk_fma_f32 v[100:101], v[196:197], v[130:131], v[228:229]
	v_mbcnt_lo_u32_b32 v122, -1, 0
	v_mbcnt_hi_u32_b32 v122, -1, v122
	v_pk_fma_f32 v[92:93], v[198:199], v[92:93], v[230:231]
	v_ashrrev_i32_e32 v123, 31, v122
	v_lshl_add_u64 v[122:123], v[122:123], 4, s[12:13]
	v_mbcnt_lo_u32_b32 v126, -1, 0
	v_mbcnt_hi_u32_b32 v126, -1, v126
	v_pk_mul_f32 v[130:131], v[102:103], v[32:33] op_sel_hi:[1,0]
	v_ashrrev_i32_e32 v127, 31, v126
	v_lshl_add_u64 v[126:127], v[126:127], 4, s[14:15]
	v_pk_mul_f32 v[102:103], v[104:105], v[32:33] op_sel_hi:[1,0]
	v_max_f32_e64 v6, |v92|, |v93|
	v_max3_f32 v6, |v100|, |v101|, v6
	s_waitcnt vmcnt(0)
	v_pk_fma_f32 v[104:105], v[200:201], v[130:131], v[232:233]
	v_mbcnt_lo_u32_b32 v122, -1, 0
	v_mbcnt_hi_u32_b32 v122, -1, v122
	v_pk_fma_f32 v[102:103], v[202:203], v[102:103], v[234:235]
	v_ashrrev_i32_e32 v123, 31, v122
	v_lshl_add_u64 v[122:123], v[122:123], 4, s[12:13]
	v_mbcnt_lo_u32_b32 v126, -1, 0
	v_mbcnt_hi_u32_b32 v126, -1, v126
	v_pk_mul_f32 v[130:131], v[106:107], v[32:33] op_sel_hi:[1,0]
	v_ashrrev_i32_e32 v127, 31, v126
	v_lshl_add_u64 v[126:127], v[126:127], 4, s[14:15]
	v_pk_mul_f32 v[106:107], v[108:109], v[32:33] op_sel_hi:[1,0]
	v_max_f32_e64 v94, |v102|, |v103|
	v_max3_f32 v94, |v104|, |v105|, v94
	v_max3_f32 v6, v6, 0, v94
	s_waitcnt vmcnt(0)
	v_pk_fma_f32 v[108:109], v[204:205], v[130:131], v[236:237]
	v_mbcnt_lo_u32_b32 v122, -1, 0
	v_mbcnt_hi_u32_b32 v122, -1, v122
	v_pk_fma_f32 v[106:107], v[206:207], v[106:107], v[238:239]
	v_ashrrev_i32_e32 v123, 31, v122
	v_lshl_add_u64 v[122:123], v[122:123], 4, s[12:13]
	v_mbcnt_lo_u32_b32 v126, -1, 0
	v_mbcnt_hi_u32_b32 v126, -1, v126
	v_pk_mul_f32 v[130:131], v[110:111], v[32:33] op_sel_hi:[1,0]
	v_ashrrev_i32_e32 v127, 31, v126
	v_lshl_add_u64 v[126:127], v[126:127], 4, s[14:15]
	v_pk_mul_f32 v[110:111], v[112:113], v[32:33] op_sel_hi:[1,0]
	v_max_f32_e64 v94, |v106|, |v107|
	v_max3_f32 v94, |v108|, |v109|, v94
	s_waitcnt vmcnt(0)
	v_pk_fma_f32 v[112:113], v[208:209], v[130:131], v[240:241]
	v_mbcnt_lo_u32_b32 v122, -1, 0
	v_mbcnt_hi_u32_b32 v122, -1, v122
	v_pk_fma_f32 v[110:111], v[210:211], v[110:111], v[242:243]
	v_ashrrev_i32_e32 v123, 31, v122
	v_lshl_add_u64 v[122:123], v[122:123], 4, s[12:13]
	v_add_co_u32_e32 v122, vcc, s23, v122
	v_max_f32_e64 v114, |v110|, |v111|
	s_nop 0
	v_addc_co_u32_e32 v123, vcc, 0, v123, vcc
	v_mbcnt_lo_u32_b32 v126, -1, 0
	v_mbcnt_hi_u32_b32 v126, -1, v126
	v_max3_f32 v114, |v112|, |v113|, v114
	v_ashrrev_i32_e32 v127, 31, v126
	v_lshl_add_u64 v[126:127], v[126:127], 4, s[14:15]
	v_add_co_u32_e32 v126, vcc, s23, v126
	v_max3_f32 v94, v6, v94, v114
	s_nop 0
	v_addc_co_u32_e32 v127, vcc, 0, v127, vcc
	v_mov_b32_e32 v114, v117
	v_pk_mul_f32 v[114:115], v[114:115], v[32:33] op_sel_hi:[1,0]
	v_pk_mul_f32 v[6:7], v[118:119], v[32:33] op_sel_hi:[1,0]
	s_waitcnt vmcnt(0)
	v_pk_fma_f32 v[114:115], v[214:215], v[114:115], v[246:247]
	v_pk_fma_f32 v[116:117], v[212:213], v[6:7], v[244:245]
	v_max_f32_e64 v6, |v114|, |v115|
	v_max3_f32 v130, |v116|, |v117|, v6
	v_mbcnt_lo_u32_b32 v6, -1, 0
	v_mbcnt_hi_u32_b32 v6, -1, v6
	s_nop 0
	v_ashrrev_i32_e32 v7, 31, v6
	v_lshl_add_u64 v[6:7], v[6:7], 4, s[12:13]
	v_add_co_u32_e32 v6, vcc, s23, v6
	s_nop 1
	v_addc_co_u32_e32 v7, vcc, 0, v7, vcc
	v_mbcnt_lo_u32_b32 v6, -1, 0
	v_mbcnt_hi_u32_b32 v6, -1, v6
	s_nop 0
	v_ashrrev_i32_e32 v7, 31, v6
	v_lshl_add_u64 v[6:7], v[6:7], 4, s[14:15]
	v_add_co_u32_e32 v6, vcc, s23, v6
	s_nop 1
	v_addc_co_u32_e32 v7, vcc, 0, v7, vcc
	v_pk_mul_f32 v[6:7], v[120:121], v[32:33] op_sel_hi:[1,0]
	s_waitcnt vmcnt(0)
	v_pk_fma_f32 v[120:121], v[216:217], v[4:5], v[248:249]
	v_pk_fma_f32 v[118:119], v[218:219], v[6:7], v[250:251]
	s_nop 0
	v_max_f32_e64 v4, |v118|, |v119|
	v_max3_f32 v4, |v120|, |v121|, v4
	v_max3_f32 v128, v94, v130, v4
	v_mbcnt_lo_u32_b32 v4, -1, 0
	v_mbcnt_hi_u32_b32 v4, -1, v4
	v_mov_b32_e32 v94, v97
	v_ashrrev_i32_e32 v5, 31, v4
	v_lshl_add_u64 v[4:5], v[4:5], 4, s[12:13]
	v_add_co_u32_e32 v4, vcc, s23, v4
	v_pk_mul_f32 v[94:95], v[94:95], v[32:33] op_sel_hi:[1,0]
	s_nop 0
	v_addc_co_u32_e32 v5, vcc, 0, v5, vcc
	v_mbcnt_lo_u32_b32 v122, -1, 0
	v_mbcnt_hi_u32_b32 v122, -1, v122
	s_nop 0
	v_ashrrev_i32_e32 v123, 31, v122
	v_lshl_add_u64 v[122:123], v[122:123], 4, s[14:15]
	v_add_co_u32_e32 v122, vcc, s23, v122
	s_nop 1
	v_addc_co_u32_e32 v123, vcc, 0, v123, vcc
	s_waitcnt vmcnt(0)
	v_pk_fma_f32 v[122:123], v[2:3], v[222:223], v[184:185]
	v_pk_fma_f32 v[124:125], v[0:1], v[220:221], v[182:183]
	v_max_f32_e64 v0, |v122|, |v123|
	v_max3_f32 v126, |v124|, |v125|, v0
	v_mbcnt_lo_u32_b32 v0, -1, 0
	v_mbcnt_hi_u32_b32 v0, -1, v0
	s_nop 0
	v_ashrrev_i32_e32 v1, 31, v0
	v_lshl_add_u64 v[0:1], v[0:1], 4, s[12:13]
	v_add_co_u32_e32 v0, vcc, s23, v0
	s_nop 1
	v_addc_co_u32_e32 v1, vcc, 0, v1, vcc
	v_mbcnt_lo_u32_b32 v4, -1, 0
	v_mbcnt_hi_u32_b32 v4, -1, v4
	s_nop 0
	v_ashrrev_i32_e32 v5, 31, v4
	v_lshl_add_u64 v[4:5], v[4:5], 4, s[14:15]
	v_add_co_u32_e32 v4, vcc, s23, v4
	s_nop 1
	v_addc_co_u32_e32 v5, vcc, 0, v5, vcc
	s_waitcnt vmcnt(0)
	v_pk_fma_f32 v[2:3], v[94:95], v[226:227], v[188:189]
	v_pk_fma_f32 v[4:5], v[98:99], v[224:225], v[186:187]
	v_max_f32_e64 v0, |v2|, |v3|
	v_max3_f32 v0, |v4|, |v5|, v0
	v_max3_f32 v0, v128, v126, v0
	s_waitcnt lgkmcnt(0)
	s_nop 1
	v_max_f32_dpp v0, v0, v0 quad_perm:[1,0,3,2] row_mask:0xf bank_mask:0xf
	s_waitcnt lgkmcnt(0)
	s_nop 1
	v_max_f32_dpp v0, v0, v0 quad_perm:[2,3,0,1] row_mask:0xf bank_mask:0xf
	s_waitcnt lgkmcnt(0)
	s_nop 1
	v_max_f32_dpp v0, v0, v0 row_half_mirror row_mask:0xf bank_mask:0xf
	s_waitcnt lgkmcnt(0)
	s_nop 1
	v_max_f32_dpp v0, v0, v0 row_mirror row_mask:0xf bank_mask:0xf
	s_waitcnt lgkmcnt(0)
; #define FLANE lane_id()
; __device__ __forceinline__ void p6_router(Frame& F) {
;     ...
; #pragma unroll
;                 for (int o = 1; o < 64; o <<= 1) am = fmaxf(am, __shfl_xor(am, o));
;                 const float sc = am > 0.f ? am * (1.f / 127.f) : 1.f, inv = 1.f / sc;
; #pragma unroll
;                 for (int j = 0; j < 8; ++j) { const int q0 = (int)__builtin_rintf(v[j][0] * inv), q1 = (int)__builtin_rintf(v[j][1] * inv), q2 = (int)__builtin_rintf(v[j][2] * inv), q3 = (int)__builtin_rintf(v[j][3] * inv);
;                     h1q[(size_t)m * (D / 4) + FLANE + 64 * j] = (unsigned)(q0 & 0xff) | ((unsigned)(q1 & 0xff) << 8) | ((unsigned)(q2 & 0xff) << 16) | ((unsigned)(q3 & 0xff) << 24); }
;                 if (FLANE == 0) { st1[2 * m] = mean; st1[2 * m + 1] = rstd; stl[2 * row] = mean; stl[2 * row + 1] = rstd; sxg[m] = sc; sxl[row] = sc; }
	v_mov_b32_e32 v1, v0
	s_nop 1
	v_permlane16_swap_b32_e32 v0, v1
	v_max_f32_e32 v0, v0, v1
	s_waitcnt lgkmcnt(0)
	v_mov_b32_e32 v1, v0
	s_nop 1
	v_permlane32_swap_b32_e32 v0, v1
	v_max_f32_e32 v0, v0, v1
	v_cmp_lt_f32_e32 vcc, 0, v0
	v_mul_f32_e32 v0, 0x3c010204, v0
	s_nop 0
	v_cndmask_b32_e32 v0, 1.0, v0, vcc
	v_div_scale_f32 v1, s[6:7], v0, v0, 1.0
	v_rcp_f32_e32 v6, v1
	s_lshl_b64 s[6:7], s[4:5], 11
	s_add_u32 s6, s3, s6
	s_addc_u32 s7, s24, s7
	v_fma_f32 v7, -v1, v6, 1.0
	v_fmac_f32_e32 v6, v7, v6
	v_div_scale_f32 v7, vcc, 1.0, v0, 1.0
	v_mul_f32_e32 v94, v7, v6
	v_fma_f32 v95, -v1, v94, v7
	v_fmac_f32_e32 v94, v95, v6
	v_fma_f32 v1, -v1, v94, v7
	v_div_fmas_f32 v1, v1, v6, v94
	v_div_fixup_f32 v1, v1, v0, 1.0
	v_mul_f32_e32 v7, v101, v1
	v_mul_f32_e32 v6, v100, v1
	v_rndne_f32_e32 v7, v7
	v_mul_f32_e32 v92, v92, v1
	v_mul_f32_e32 v93, v93, v1
	v_rndne_f32_e32 v6, v6
	v_cvt_i32_f32_e32 v7, v7
	v_rndne_f32_e32 v92, v92
	v_rndne_f32_e32 v93, v93
	v_cvt_i32_f32_e32 v6, v6
	v_cvt_i32_f32_sdwa v92, v92 dst_sel:WORD_1 dst_unused:UNUSED_PAD src0_sel:DWORD
	v_cvt_i32_f32_e32 v93, v93
	v_lshlrev_b32_e32 v7, 8, v7
	v_and_b32_e32 v7, 0xff00, v7
	v_and_b32_e32 v92, 0xff0000, v92
	v_perm_b32 v6, v93, v6, s1
	v_or3_b32 v92, v6, v7, v92
	v_mbcnt_lo_u32_b32 v6, -1, 0
	v_mbcnt_hi_u32_b32 v6, -1, v6
	v_mul_f32_e32 v93, v103, v1
	v_ashrrev_i32_e32 v7, 31, v6
	v_lshl_add_u64 v[6:7], v[6:7], 2, s[6:7]
	global_store_dword v[6:7], v92, off
	v_mul_f32_e32 v7, v105, v1
	v_mul_f32_e32 v6, v104, v1
	v_rndne_f32_e32 v7, v7
	v_mul_f32_e32 v92, v102, v1
	v_rndne_f32_e32 v6, v6
	v_cvt_i32_f32_e32 v7, v7
	v_rndne_f32_e32 v92, v92
	v_rndne_f32_e32 v93, v93
	v_cvt_i32_f32_e32 v6, v6
	v_cvt_i32_f32_sdwa v92, v92 dst_sel:WORD_1 dst_unused:UNUSED_PAD src0_sel:DWORD
	v_cvt_i32_f32_e32 v93, v93
	v_lshlrev_b32_e32 v7, 8, v7
	v_and_b32_e32 v7, 0xff00, v7
	v_and_b32_e32 v92, 0xff0000, v92
	v_perm_b32 v6, v93, v6, s1
	v_or3_b32 v92, v6, v7, v92
	v_mbcnt_lo_u32_b32 v6, -1, 0
	v_mbcnt_hi_u32_b32 v6, -1, v6
	v_mul_f32_e32 v93, v107, v1
	v_ashrrev_i32_e32 v7, 31, v6
	v_lshl_add_u64 v[6:7], v[6:7], 2, s[6:7]
	global_store_dword v[6:7], v92, off offset:256
	v_mul_f32_e32 v7, v109, v1
	v_mul_f32_e32 v6, v108, v1
	v_rndne_f32_e32 v7, v7
	v_mul_f32_e32 v92, v106, v1
	v_rndne_f32_e32 v6, v6
	v_cvt_i32_f32_e32 v7, v7
	v_rndne_f32_e32 v92, v92
	v_rndne_f32_e32 v93, v93
	v_cvt_i32_f32_e32 v6, v6
	v_cvt_i32_f32_sdwa v92, v92 dst_sel:WORD_1 dst_unused:UNUSED_PAD src0_sel:DWORD
	v_cvt_i32_f32_e32 v93, v93
	v_lshlrev_b32_e32 v7, 8, v7
	v_and_b32_e32 v7, 0xff00, v7
	v_and_b32_e32 v92, 0xff0000, v92
	v_perm_b32 v6, v93, v6, s1
	v_or3_b32 v92, v6, v7, v92
	v_mbcnt_lo_u32_b32 v6, -1, 0
	v_mbcnt_hi_u32_b32 v6, -1, v6
	v_mul_f32_e32 v93, v111, v1
	v_ashrrev_i32_e32 v7, 31, v6
	v_lshl_add_u64 v[6:7], v[6:7], 2, s[6:7]
	global_store_dword v[6:7], v92, off offset:512
	v_mul_f32_e32 v7, v113, v1
	v_mul_f32_e32 v6, v112, v1
	v_rndne_f32_e32 v7, v7
	v_mul_f32_e32 v92, v110, v1
	v_rndne_f32_e32 v6, v6
	v_cvt_i32_f32_e32 v7, v7
	v_rndne_f32_e32 v92, v92
	v_rndne_f32_e32 v93, v93
	v_cvt_i32_f32_e32 v6, v6
	v_cvt_i32_f32_sdwa v92, v92 dst_sel:WORD_1 dst_unused:UNUSED_PAD src0_sel:DWORD
	v_cvt_i32_f32_e32 v93, v93
	v_lshlrev_b32_e32 v7, 8, v7
	v_and_b32_e32 v7, 0xff00, v7
	v_and_b32_e32 v92, 0xff0000, v92
	v_perm_b32 v6, v93, v6, s1
	v_or3_b32 v92, v6, v7, v92
	v_mbcnt_lo_u32_b32 v6, -1, 0
	v_mbcnt_hi_u32_b32 v6, -1, v6
	v_mul_f32_e32 v93, v115, v1
	v_ashrrev_i32_e32 v7, 31, v6
	v_lshl_add_u64 v[6:7], v[6:7], 2, s[6:7]
	global_store_dword v[6:7], v92, off offset:768
	v_mul_f32_e32 v7, v117, v1
	v_mul_f32_e32 v6, v116, v1
	v_rndne_f32_e32 v7, v7
	v_mul_f32_e32 v92, v114, v1
	v_rndne_f32_e32 v6, v6
	v_cvt_i32_f32_e32 v7, v7
	v_rndne_f32_e32 v92, v92
	v_rndne_f32_e32 v93, v93
	v_cvt_i32_f32_e32 v6, v6
	v_cvt_i32_f32_sdwa v92, v92 dst_sel:WORD_1 dst_unused:UNUSED_PAD src0_sel:DWORD
	v_cvt_i32_f32_e32 v93, v93
	v_lshlrev_b32_e32 v7, 8, v7
	v_and_b32_e32 v7, 0xff00, v7
	v_and_b32_e32 v92, 0xff0000, v92
	v_perm_b32 v6, v93, v6, s1
	v_or3_b32 v92, v6, v7, v92
	v_mbcnt_lo_u32_b32 v6, -1, 0
	v_mbcnt_hi_u32_b32 v6, -1, v6
	v_mul_f32_e32 v93, v119, v1
	v_ashrrev_i32_e32 v7, 31, v6
	v_lshl_add_u64 v[6:7], v[6:7], 2, s[6:7]
	global_store_dword v[6:7], v92, off offset:1024
	v_mul_f32_e32 v7, v121, v1
	v_mul_f32_e32 v6, v120, v1
	v_rndne_f32_e32 v7, v7
	v_mul_f32_e32 v92, v118, v1
	v_rndne_f32_e32 v6, v6
	v_cvt_i32_f32_e32 v7, v7
	v_rndne_f32_e32 v92, v92
	v_rndne_f32_e32 v93, v93
	v_cvt_i32_f32_e32 v6, v6
	v_cvt_i32_f32_sdwa v92, v92 dst_sel:WORD_1 dst_unused:UNUSED_PAD src0_sel:DWORD
	v_cvt_i32_f32_e32 v93, v93
	v_lshlrev_b32_e32 v7, 8, v7
	v_and_b32_e32 v7, 0xff00, v7
	v_and_b32_e32 v92, 0xff0000, v92
	v_perm_b32 v6, v93, v6, s1
	v_or3_b32 v92, v6, v7, v92
	v_mbcnt_lo_u32_b32 v6, -1, 0
	v_mbcnt_hi_u32_b32 v6, -1, v6
	v_mul_f32_e32 v93, v123, v1
	v_ashrrev_i32_e32 v7, 31, v6
	v_lshl_add_u64 v[6:7], v[6:7], 2, s[6:7]
	global_store_dword v[6:7], v92, off offset:1280
	v_mul_f32_e32 v7, v125, v1
	v_mul_f32_e32 v6, v124, v1
	v_rndne_f32_e32 v7, v7
	v_mul_f32_e32 v92, v122, v1
	v_rndne_f32_e32 v6, v6
	v_cvt_i32_f32_e32 v7, v7
	v_rndne_f32_e32 v92, v92
	v_rndne_f32_e32 v93, v93
	v_mul_f32_e32 v5, v5, v1
	v_cvt_i32_f32_e32 v6, v6
	v_cvt_i32_f32_sdwa v92, v92 dst_sel:WORD_1 dst_unused:UNUSED_PAD src0_sel:DWORD
	v_cvt_i32_f32_e32 v93, v93
	v_mul_f32_e32 v4, v4, v1
	v_rndne_f32_e32 v5, v5
	v_mul_f32_e32 v2, v2, v1
	v_mul_f32_e32 v1, v3, v1
	v_rndne_f32_e32 v4, v4
	v_cvt_i32_f32_e32 v5, v5
	v_rndne_f32_e32 v2, v2
	v_rndne_f32_e32 v1, v1
	v_cvt_i32_f32_e32 v4, v4
	v_cvt_i32_f32_sdwa v2, v2 dst_sel:WORD_1 dst_unused:UNUSED_PAD src0_sel:DWORD
	v_cvt_i32_f32_e32 v1, v1
	v_lshlrev_b32_e32 v7, 8, v7
	v_and_b32_e32 v7, 0xff00, v7
	v_and_b32_e32 v92, 0xff0000, v92
	v_perm_b32 v6, v93, v6, s1
	v_or3_b32 v92, v6, v7, v92
	v_mbcnt_lo_u32_b32 v6, -1, 0
	v_mbcnt_hi_u32_b32 v6, -1, v6
	v_lshlrev_b32_e32 v3, 8, v5
	v_ashrrev_i32_e32 v7, 31, v6
	v_lshl_add_u64 v[6:7], v[6:7], 2, s[6:7]
	v_and_b32_e32 v3, 0xff00, v3
	v_and_b32_e32 v2, 0xff0000, v2
	v_perm_b32 v1, v1, v4, s1
	global_store_dword v[6:7], v92, off offset:1536
	v_or3_b32 v1, v1, v3, v2
	v_mbcnt_lo_u32_b32 v2, -1, 0
	v_mbcnt_hi_u32_b32 v2, -1, v2
	s_nop 0
	v_ashrrev_i32_e32 v3, 31, v2
	v_lshl_add_u64 v[2:3], v[2:3], 2, s[6:7]
	global_store_dword v[2:3], v1, off offset:1792
	v_mbcnt_lo_u32_b32 v1, -1, 0
	v_mbcnt_hi_u32_b32 v1, -1, v1
	s_nop 0
	v_cmp_eq_u32_e32 vcc, 0, v1
	s_and_saveexec_b64 s[6:7], vcc
	s_cbranch_execz .LBB0_1487
	s_lshl_b32 s8, s4, 1
	s_ashr_i32 s9, s8, 31
	s_lshl_b64 s[8:9], s[8:9], 2
	s_add_u32 s8, s27, s8
	s_addc_u32 s9, s64, s9
	v_readlane_b32 s0, v255, 43
	s_lshl_b64 s[4:5], s[4:5], 2
	v_mul_f32_e32 v2, 0x3a000000, v96
	v_mov_b32_e32 v3, v32
	v_mov_b32_e32 v1, s0
	s_add_u32 s4, s25, s4
	v_readlane_b32 s0, v255, 29
	ds_write_b64 v1, v[2:3]
	s_addc_u32 s5, s26, s5
	v_mov_b32_e32 v1, s0
	global_store_dwordx2 v33, v[2:3], s[8:9]
	global_store_dword v33, v0, s[4:5]
	ds_write_b32 v1, v0
; __device__ __forceinline__ void p6_router(Frame& F) {
;     ...
;                 f32x4 v[8]; float s = 0.f;
; #pragma unroll
;                 for (int j = 0; j < 8; ++j) { const v2u w = raw[rr][j]; v[j] = (f32x4){bf_lo(w.x), bf_hi(w.x), bf_lo(w.y), bf_hi(w.y)}; s += (v[j][0] + v[j][1]) + (v[j][2] + v[j][3]); }
;                 const float mean = wave_sum(s) * (1.f / D); float s2 = 0.f;
; #pragma unroll
;                 for (int j = 0; j < 8; ++j) { v[j] = v[j] - mean; s2 += (v[j][0] * v[j][0] + v[j][1] * v[j][1]) + (v[j][2] * v[j][2] + v[j][3] * v[j][3]); }
.LBB0_1487:
	s_or_b64 exec, exec, s[6:7]
	v_lshlrev_b32_e32 v93, 16, v90
	v_lshlrev_b32_e32 v92, 16, v88
	v_and_b32_e32 v105, 0xffff0000, v90
	v_and_b32_e32 v104, 0xffff0000, v88
	v_lshlrev_b32_e32 v107, 16, v91
	v_lshlrev_b32_e32 v106, 16, v89
	v_and_b32_e32 v109, 0xffff0000, v91
	v_and_b32_e32 v108, 0xffff0000, v89
	v_pk_add_f32 v[0:1], v[92:93], v[104:105]
	v_pk_add_f32 v[2:3], v[106:107], v[108:109]
	v_lshlrev_b32_e32 v91, 16, v87
	v_pk_add_f32 v[0:1], v[0:1], v[2:3]
	v_lshlrev_b32_e32 v90, 16, v86
	v_add_f32_e32 v0, 0, v0
	v_and_b32_e32 v111, 0xffff0000, v87
	v_and_b32_e32 v110, 0xffff0000, v86
	v_add_f32_e32 v6, v0, v1
	v_pk_add_f32 v[0:1], v[90:91], v[110:111]
	v_lshlrev_b32_e32 v94, 16, v84
	v_and_b32_e32 v95, 0xffff0000, v84
	v_lshlrev_b32_e32 v96, 16, v85
	v_and_b32_e32 v97, 0xffff0000, v85
	v_and_b32_e32 v103, 0xffff0000, v82
	v_pk_add_f32 v[0:1], v[0:1], v[0:1] op_sel:[0,1] op_sel_hi:[1,0]
	v_add_f32_e32 v100, v94, v95
	v_add_f32_e32 v98, v96, v97
	v_lshlrev_b32_e32 v7, 16, v82
	v_lshlrev_b32_e32 v101, 16, v83
	v_and_b32_e32 v99, 0xffff0000, v83
	v_mov_b32_e32 v1, v103
	v_pk_add_f32 v[0:1], v[6:7], v[0:1]
	v_pk_add_f32 v[2:3], v[100:101], v[98:99]
	v_lshlrev_b32_e32 v5, 16, v81
	v_lshlrev_b32_e32 v4, 16, v80
	v_and_b32_e32 v113, 0xffff0000, v81
	v_and_b32_e32 v112, 0xffff0000, v80
	v_pk_add_f32 v[84:85], v[0:1], v[2:3]
	v_pk_add_f32 v[86:87], v[4:5], v[112:113]
	v_lshlrev_b32_e32 v0, 16, v78
	v_and_b32_e32 v1, 0xffff0000, v78
	v_lshlrev_b32_e32 v2, 16, v79
	v_and_b32_e32 v3, 0xffff0000, v79
	v_lshlrev_b32_e32 v82, 16, v76
	v_and_b32_e32 v83, 0xffff0000, v76
	v_lshlrev_b32_e32 v81, 16, v77
	v_and_b32_e32 v79, 0xffff0000, v77
	v_pk_add_f32 v[76:77], v[84:85], v[84:85] op_sel:[0,1] op_sel_hi:[1,0]
	v_pk_add_f32 v[84:85], v[86:87], v[86:87] op_sel:[0,1] op_sel_hi:[1,0]
	v_add_f32_e32 v80, v0, v1
	v_add_f32_e32 v78, v2, v3
	v_mov_b32_e32 v77, v82
	v_mov_b32_e32 v85, v83
	v_pk_add_f32 v[76:77], v[76:77], v[84:85]
	v_pk_add_f32 v[84:85], v[80:81], v[78:79]
	s_nop 0
	v_pk_add_f32 v[76:77], v[76:77], v[84:85]
	s_nop 0
	v_add_f32_e32 v6, v76, v77
	s_waitcnt lgkmcnt(0)
	s_nop 1
	v_add_f32_dpp v6, v6, v6 quad_perm:[1,0,3,2] row_mask:0xf bank_mask:0xf
	s_waitcnt lgkmcnt(0)
	s_nop 1
	v_add_f32_dpp v6, v6, v6 quad_perm:[2,3,0,1] row_mask:0xf bank_mask:0xf
	s_waitcnt lgkmcnt(0)
	s_nop 1
	v_add_f32_dpp v6, v6, v6 row_half_mirror row_mask:0xf bank_mask:0xf
	s_waitcnt lgkmcnt(0)
	s_nop 1
	v_add_f32_dpp v6, v6, v6 row_mirror row_mask:0xf bank_mask:0xf
	s_waitcnt lgkmcnt(0)
	v_mov_b32_e32 v32, v6
	s_nop 1
	v_permlane16_swap_b32_e32 v6, v32
	v_add_f32_e32 v6, v6, v32
	s_waitcnt lgkmcnt(0)
	v_mov_b32_e32 v32, v6
	s_nop 1
	v_permlane32_swap_b32_e32 v6, v32
	v_add_f32_e32 v80, v6, v32
	v_fmac_f32_e32 v108, 0xba000000, v80
	v_fmac_f32_e32 v104, 0xba000000, v80
	v_fmac_f32_e32 v109, 0xba000000, v80
	v_fmac_f32_e32 v105, 0xba000000, v80
	v_fmac_f32_e32 v106, 0xba000000, v80
	v_fmac_f32_e32 v92, 0xba000000, v80
	v_fmac_f32_e32 v107, 0xba000000, v80
	v_fmac_f32_e32 v93, 0xba000000, v80
	v_mov_b32_e32 v87, v105
	v_mov_b32_e32 v77, v104
	v_pk_mul_f32 v[84:85], v[104:105], v[104:105]
	v_pk_mul_f32 v[104:105], v[108:109], v[108:109]
	v_mov_b32_e32 v86, v93
	v_mov_b32_e32 v76, v92
	v_pk_fma_f32 v[92:93], v[92:93], v[92:93], v[84:85]
	v_pk_fma_f32 v[104:105], v[106:107], v[106:107], v[104:105]
	v_fmac_f32_e32 v110, 0xba000000, v80
	v_pk_add_f32 v[92:93], v[92:93], v[104:105]
	v_fmac_f32_e32 v111, 0xba000000, v80
	v_fmac_f32_e32 v91, 0xba000000, v80
	v_pk_add_f32 v[104:105], v[92:93], v[92:93] op_sel_hi:[0,1]
	v_fmac_f32_e32 v90, 0xba000000, v80
	v_mov_b32_e32 v92, v91
	v_mov_b32_e32 v93, v111
	v_mov_b32_e32 v91, v110
	v_mov_b32_e32 v88, v107
	v_mov_b32_e32 v89, v109
	v_mov_b32_e32 v84, v106
	v_mov_b32_e32 v85, v108
	v_pk_mul_f32 v[106:107], v[92:93], v[92:93]
	v_pk_mul_f32 v[108:109], v[90:91], v[90:91]
	v_fmac_f32_e32 v94, 0xba000000, v80
	v_pk_mov_b32 v[110:111], v[108:109], v[106:107] op_sel:[1,0]
	v_mov_b32_e32 v109, v107
	v_fmac_f32_e32 v95, 0xba000000, v80
	v_fmac_f32_e32 v96, 0xba000000, v80
	v_mul_f32_e32 v6, v94, v94
	v_pk_add_f32 v[106:107], v[110:111], v[108:109]
	v_fmac_f32_e32 v97, 0xba000000, v80
	v_pk_fma_f32 v[108:109], v[94:95], v[94:95], v[6:7] op_sel_hi:[1,1,0]
	v_mul_f32_e32 v6, v96, v96
	v_pk_add_f32 v[106:107], v[106:107], v[106:107] op_sel_hi:[0,1]
	v_pk_fma_f32 v[110:111], v[96:97], v[96:97], v[6:7] op_sel_hi:[1,1,0]
	v_fmac_f32_e32 v99, 0xba000000, v80
	v_fmac_f32_e32 v101, 0xba000000, v80
	v_fmac_f32_e32 v103, 0xba000000, v80
	v_fmac_f32_e32 v7, 0xba000000, v80
	v_mul_f32_e32 v108, v7, v7
	v_mul_f32_e32 v110, v103, v103
	v_mul_f32_e32 v106, v101, v101
	v_mul_f32_e32 v104, v99, v99
	v_pk_add_f32 v[108:109], v[108:109], v[110:111]
	v_pk_add_f32 v[104:105], v[106:107], v[104:105]
	v_fmac_f32_e32 v112, 0xba000000, v80
	v_pk_add_f32 v[104:105], v[108:109], v[104:105]
	v_fmac_f32_e32 v113, 0xba000000, v80
	v_fmac_f32_e32 v5, 0xba000000, v80
	v_pk_add_f32 v[106:107], v[104:105], v[104:105] op_sel_hi:[0,1]
	v_fmac_f32_e32 v4, 0xba000000, v80
	v_mov_b32_e32 v104, v5
	v_mov_b32_e32 v105, v113
	v_mov_b32_e32 v5, v112
	v_pk_mul_f32 v[108:109], v[104:105], v[104:105]
	v_pk_mul_f32 v[110:111], v[4:5], v[4:5]
	v_fmac_f32_e32 v0, 0xba000000, v80
	v_pk_mov_b32 v[112:113], v[110:111], v[108:109] op_sel:[1,0]
	v_mov_b32_e32 v111, v109
	v_fmac_f32_e32 v1, 0xba000000, v80
	v_fmac_f32_e32 v2, 0xba000000, v80
	v_mul_f32_e32 v6, v0, v0
	v_pk_add_f32 v[108:109], v[112:113], v[110:111]
	v_fmac_f32_e32 v3, 0xba000000, v80
	v_pk_fma_f32 v[110:111], v[0:1], v[0:1], v[6:7] op_sel_hi:[1,1,0]
	v_mul_f32_e32 v6, v2, v2
	v_pk_add_f32 v[108:109], v[108:109], v[108:109] op_sel_hi:[0,1]
	v_pk_fma_f32 v[112:113], v[2:3], v[2:3], v[6:7] op_sel_hi:[1,1,0]
	v_fmac_f32_e32 v79, 0xba000000, v80
	v_fmac_f32_e32 v81, 0xba000000, v80
	v_fmac_f32_e32 v83, 0xba000000, v80
	v_fmac_f32_e32 v82, 0xba000000, v80
	v_mul_f32_e32 v110, v82, v82
	v_mul_f32_e32 v112, v83, v83
	v_mul_f32_e32 v108, v81, v81
	v_mul_f32_e32 v106, v79, v79
	v_pk_add_f32 v[110:111], v[110:111], v[112:113]
	v_pk_add_f32 v[106:107], v[108:109], v[106:107]
	s_nop 0
	v_pk_add_f32 v[106:107], v[110:111], v[106:107]
	s_nop 0
	v_add_f32_e32 v6, v106, v107
	v_mbcnt_lo_u32_b32 v106, -1, 0
	v_mbcnt_hi_u32_b32 v106, -1, v106
	v_ashrrev_i32_e32 v107, 31, v106
	v_lshl_add_u64 v[106:107], v[106:107], 4, s[12:13]
	v_mbcnt_lo_u32_b32 v110, -1, 0
	v_mbcnt_hi_u32_b32 v110, -1, v110
	s_waitcnt lgkmcnt(0)
; #define GAS __attribute__((address_space(1)))
; #define FLANE lane_id()
; __device__ __forceinline__ void p6_router(Frame& F) {
;     ...
;                 for (int j = 0; j < 8; ++j) { v[j] = v[j] - mean; s2 += (v[j][0] * v[j][0] + v[j][1] * v[j][1]) + (v[j][2] * v[j][2] + v[j][3] * v[j][3]); }
;                 const float rstd = 1.f / sqrtf(wave_sum(s2) * (1.f / D) + LN_EPS);
;                 float am = 0.f;
; #pragma unroll
;                 for (int j = 0; j < 8; ++j) { const f32x4 g = *((const GAS f32x4*)F.ln1_g + FLANE + 64 * j), b = *((const GAS f32x4*)F.ln1_b + FLANE + 64 * j);
;                     v[j] = v[j] * rstd * g + b; am = fmaxf(am, fmaxf(fmaxf(fabsf(v[j][0]), fabsf(v[j][1])), fmaxf(fabsf(v[j][2]), fabsf(v[j][3])))); }
	s_nop 1
	v_add_f32_dpp v6, v6, v6 quad_perm:[1,0,3,2] row_mask:0xf bank_mask:0xf
	v_ashrrev_i32_e32 v111, 31, v110
	v_lshl_add_u64 v[110:111], v[110:111], 4, s[14:15]
	s_waitcnt lgkmcnt(0)
	s_nop 1
	v_add_f32_dpp v6, v6, v6 quad_perm:[2,3,0,1] row_mask:0xf bank_mask:0xf
	s_waitcnt lgkmcnt(0)
	s_nop 1
	v_add_f32_dpp v6, v6, v6 row_half_mirror row_mask:0xf bank_mask:0xf
	s_waitcnt lgkmcnt(0)
	s_nop 1
	v_add_f32_dpp v6, v6, v6 row_mirror row_mask:0xf bank_mask:0xf
	s_waitcnt lgkmcnt(0)
	v_mov_b32_e32 v32, v6
	s_nop 1
	v_permlane16_swap_b32_e32 v6, v32
	v_add_f32_e32 v6, v6, v32
	s_waitcnt lgkmcnt(0)
	v_mov_b32_e32 v32, v6
	s_nop 1
	v_permlane32_swap_b32_e32 v6, v32
	v_add_f32_e32 v6, v6, v32
	v_fmamk_f32 v6, v6, 0x3a000000, v166
	v_cmp_gt_f32_e32 vcc, s22, v6
	v_mul_f32_e32 v32, 0x4f800000, v6
	s_nop 0
	v_cndmask_b32_e32 v6, v6, v32, vcc
	v_sqrt_f32_e32 v32, v6
	s_nop 0
	v_add_u32_e32 v78, -1, v32
	v_fma_f32 v98, -v78, v32, v6
	v_cmp_ge_f32_e64 s[4:5], 0, v98
	v_add_u32_e32 v98, 1, v32
	s_nop 0
	v_cndmask_b32_e64 v78, v32, v78, s[4:5]
	v_fma_f32 v32, -v98, v32, v6
	v_cmp_lt_f32_e64 s[4:5], 0, v32
	s_nop 1
	v_cndmask_b32_e64 v32, v78, v98, s[4:5]
	v_mul_f32_e32 v78, 0x37800000, v32
	v_cndmask_b32_e32 v32, v32, v78, vcc
	v_cmp_class_f32_e32 vcc, v6, v167
	s_nop 1
	v_cndmask_b32_e32 v6, v32, v6, vcc
	v_div_scale_f32 v32, s[4:5], v6, v6, 1.0
	v_rcp_f32_e32 v78, v32
	s_add_i32 s4, s42, s71
	s_ashr_i32 s5, s4, 31
	v_fma_f32 v98, -v32, v78, 1.0
	v_fmac_f32_e32 v78, v98, v78
	v_div_scale_f32 v98, vcc, 1.0, v6, 1.0
	v_mul_f32_e32 v100, v98, v78
	v_fma_f32 v102, -v32, v100, v98
	v_fmac_f32_e32 v100, v102, v78
	v_fma_f32 v32, -v32, v100, v98
	v_div_fmas_f32 v32, v32, v78, v100
	v_div_fixup_f32 v32, v32, v6, 1.0
	v_pk_mul_f32 v[114:115], v[76:77], v[32:33] op_sel_hi:[1,0]
	v_pk_mul_f32 v[76:77], v[84:85], v[32:33] op_sel_hi:[1,0]
	v_mov_b32_e32 v102, v7
	v_pk_mul_f32 v[4:5], v[4:5], v[32:33] op_sel_hi:[1,0]
	v_pk_mul_f32 v[2:3], v[2:3], v[32:33] op_sel_hi:[1,0]
	v_pk_mul_f32 v[0:1], v[0:1], v[32:33] op_sel_hi:[1,0]
	v_pk_mul_f32 v[82:83], v[82:83], v[32:33] op_sel_hi:[1,0]
	s_waitcnt vmcnt(0)
	v_pk_fma_f32 v[84:85], v[196:197], v[114:115], v[228:229]
	v_mbcnt_lo_u32_b32 v106, -1, 0
	v_mbcnt_hi_u32_b32 v106, -1, v106
	v_pk_fma_f32 v[76:77], v[198:199], v[76:77], v[230:231]
	v_ashrrev_i32_e32 v107, 31, v106
	v_lshl_add_u64 v[106:107], v[106:107], 4, s[12:13]
	v_mbcnt_lo_u32_b32 v110, -1, 0
	v_mbcnt_hi_u32_b32 v110, -1, v110
	v_pk_mul_f32 v[114:115], v[86:87], v[32:33] op_sel_hi:[1,0]
	v_ashrrev_i32_e32 v111, 31, v110
	v_lshl_add_u64 v[110:111], v[110:111], 4, s[14:15]
	v_pk_mul_f32 v[86:87], v[88:89], v[32:33] op_sel_hi:[1,0]
	v_max_f32_e64 v6, |v76|, |v77|
	v_max3_f32 v6, |v84|, |v85|, v6
	s_waitcnt vmcnt(0)
	v_pk_fma_f32 v[88:89], v[200:201], v[114:115], v[232:233]
	v_mbcnt_lo_u32_b32 v106, -1, 0
	v_mbcnt_hi_u32_b32 v106, -1, v106
	v_pk_fma_f32 v[86:87], v[202:203], v[86:87], v[234:235]
	v_ashrrev_i32_e32 v107, 31, v106
	v_lshl_add_u64 v[106:107], v[106:107], 4, s[12:13]
	v_mbcnt_lo_u32_b32 v110, -1, 0
	v_mbcnt_hi_u32_b32 v110, -1, v110
	v_pk_mul_f32 v[114:115], v[90:91], v[32:33] op_sel_hi:[1,0]
	v_ashrrev_i32_e32 v111, 31, v110
	v_lshl_add_u64 v[110:111], v[110:111], 4, s[14:15]
	v_pk_mul_f32 v[90:91], v[92:93], v[32:33] op_sel_hi:[1,0]
	v_max_f32_e64 v78, |v86|, |v87|
	v_max3_f32 v78, |v88|, |v89|, v78
	v_max3_f32 v6, v6, 0, v78
	s_waitcnt vmcnt(0)
	v_pk_fma_f32 v[92:93], v[204:205], v[114:115], v[236:237]
	v_mbcnt_lo_u32_b32 v106, -1, 0
	v_mbcnt_hi_u32_b32 v106, -1, v106
	v_pk_fma_f32 v[90:91], v[206:207], v[90:91], v[238:239]
	v_ashrrev_i32_e32 v107, 31, v106
	v_lshl_add_u64 v[106:107], v[106:107], 4, s[12:13]
	v_mbcnt_lo_u32_b32 v110, -1, 0
	v_mbcnt_hi_u32_b32 v110, -1, v110
	v_pk_mul_f32 v[114:115], v[94:95], v[32:33] op_sel_hi:[1,0]
	v_ashrrev_i32_e32 v111, 31, v110
	v_lshl_add_u64 v[110:111], v[110:111], 4, s[14:15]
	v_pk_mul_f32 v[94:95], v[96:97], v[32:33] op_sel_hi:[1,0]
	v_max_f32_e64 v78, |v90|, |v91|
	v_max3_f32 v78, |v92|, |v93|, v78
	s_waitcnt vmcnt(0)
	v_pk_fma_f32 v[96:97], v[208:209], v[114:115], v[240:241]
	v_mbcnt_lo_u32_b32 v106, -1, 0
	v_mbcnt_hi_u32_b32 v106, -1, v106
	v_pk_fma_f32 v[94:95], v[210:211], v[94:95], v[242:243]
	v_ashrrev_i32_e32 v107, 31, v106
	v_lshl_add_u64 v[106:107], v[106:107], 4, s[12:13]
	v_add_co_u32_e32 v106, vcc, s23, v106
	v_max_f32_e64 v98, |v94|, |v95|
	s_nop 0
	v_addc_co_u32_e32 v107, vcc, 0, v107, vcc
	v_mbcnt_lo_u32_b32 v110, -1, 0
	v_mbcnt_hi_u32_b32 v110, -1, v110
	v_max3_f32 v98, |v96|, |v97|, v98
	v_ashrrev_i32_e32 v111, 31, v110
	v_lshl_add_u64 v[110:111], v[110:111], 4, s[14:15]
	v_add_co_u32_e32 v110, vcc, s23, v110
	v_max3_f32 v78, v6, v78, v98
	s_nop 0
	v_addc_co_u32_e32 v111, vcc, 0, v111, vcc
	v_mov_b32_e32 v98, v101
	v_pk_mul_f32 v[98:99], v[98:99], v[32:33] op_sel_hi:[1,0]
	v_pk_mul_f32 v[6:7], v[102:103], v[32:33] op_sel_hi:[1,0]
	s_waitcnt vmcnt(0)
	v_pk_fma_f32 v[98:99], v[214:215], v[98:99], v[246:247]
	v_pk_fma_f32 v[100:101], v[212:213], v[6:7], v[244:245]
	v_max_f32_e64 v6, |v98|, |v99|
	v_max3_f32 v114, |v100|, |v101|, v6
	v_mbcnt_lo_u32_b32 v6, -1, 0
	v_mbcnt_hi_u32_b32 v6, -1, v6
	s_nop 0
	v_ashrrev_i32_e32 v7, 31, v6
	v_lshl_add_u64 v[6:7], v[6:7], 4, s[12:13]
	v_add_co_u32_e32 v6, vcc, s23, v6
	s_nop 1
	v_addc_co_u32_e32 v7, vcc, 0, v7, vcc
	v_mbcnt_lo_u32_b32 v6, -1, 0
	v_mbcnt_hi_u32_b32 v6, -1, v6
	s_nop 0
	v_ashrrev_i32_e32 v7, 31, v6
	v_lshl_add_u64 v[6:7], v[6:7], 4, s[14:15]
	v_add_co_u32_e32 v6, vcc, s23, v6
	s_nop 1
	v_addc_co_u32_e32 v7, vcc, 0, v7, vcc
	v_pk_mul_f32 v[6:7], v[104:105], v[32:33] op_sel_hi:[1,0]
	s_waitcnt vmcnt(0)
; #define GAS __attribute__((address_space(1)))
; #define FLANE lane_id()
; __device__ __forceinline__ void p6_router(Frame& F) {
;     ...
;                 for (int j = 0; j < 8; ++j) { const f32x4 g = *((const GAS f32x4*)F.ln1_g + FLANE + 64 * j), b = *((const GAS f32x4*)F.ln1_b + FLANE + 64 * j);
;                     v[j] = v[j] * rstd * g + b; am = fmaxf(am, fmaxf(fmaxf(fabsf(v[j][0]), fabsf(v[j][1])), fmaxf(fabsf(v[j][2]), fabsf(v[j][3])))); }
; #pragma unroll
;                 for (int o = 1; o < 64; o <<= 1) am = fmaxf(am, __shfl_xor(am, o));
;                 const float sc = am > 0.f ? am * (1.f / 127.f) : 1.f, inv = 1.f / sc;
; #pragma unroll
;                 for (int j = 0; j < 8; ++j) { const int q0 = (int)__builtin_rintf(v[j][0] * inv), q1 = (int)__builtin_rintf(v[j][1] * inv), q2 = (int)__builtin_rintf(v[j][2] * inv), q3 = (int)__builtin_rintf(v[j][3] * inv);
;                     h1q[(size_t)m * (D / 4) + FLANE + 64 * j] = (unsigned)(q0 & 0xff) | ((unsigned)(q1 & 0xff) << 8) | ((unsigned)(q2 & 0xff) << 16) | ((unsigned)(q3 & 0xff) << 24); }
	v_pk_fma_f32 v[104:105], v[216:217], v[4:5], v[248:249]
	v_pk_fma_f32 v[102:103], v[218:219], v[6:7], v[250:251]
	s_nop 0
	v_max_f32_e64 v4, |v102|, |v103|
	v_max3_f32 v4, |v104|, |v105|, v4
	v_max3_f32 v112, v78, v114, v4
	v_mbcnt_lo_u32_b32 v4, -1, 0
	v_mbcnt_hi_u32_b32 v4, -1, v4
	v_mov_b32_e32 v78, v81
	v_ashrrev_i32_e32 v5, 31, v4
	v_lshl_add_u64 v[4:5], v[4:5], 4, s[12:13]
	v_add_co_u32_e32 v4, vcc, s23, v4
	v_pk_mul_f32 v[78:79], v[78:79], v[32:33] op_sel_hi:[1,0]
	s_nop 0
	v_addc_co_u32_e32 v5, vcc, 0, v5, vcc
	v_mbcnt_lo_u32_b32 v106, -1, 0
	v_mbcnt_hi_u32_b32 v106, -1, v106
	s_nop 0
	v_ashrrev_i32_e32 v107, 31, v106
	v_lshl_add_u64 v[106:107], v[106:107], 4, s[14:15]
	v_add_co_u32_e32 v106, vcc, s23, v106
	s_nop 1
	v_addc_co_u32_e32 v107, vcc, 0, v107, vcc
	s_waitcnt vmcnt(0)
	v_pk_fma_f32 v[106:107], v[2:3], v[222:223], v[184:185]
	v_pk_fma_f32 v[108:109], v[0:1], v[220:221], v[182:183]
	v_max_f32_e64 v0, |v106|, |v107|
	v_max3_f32 v110, |v108|, |v109|, v0
	v_mbcnt_lo_u32_b32 v0, -1, 0
	v_mbcnt_hi_u32_b32 v0, -1, v0
	s_nop 0
	v_ashrrev_i32_e32 v1, 31, v0
	v_lshl_add_u64 v[0:1], v[0:1], 4, s[12:13]
	v_add_co_u32_e32 v0, vcc, s23, v0
	s_nop 1
	v_addc_co_u32_e32 v1, vcc, 0, v1, vcc
	v_mbcnt_lo_u32_b32 v4, -1, 0
	v_mbcnt_hi_u32_b32 v4, -1, v4
	s_nop 0
	v_ashrrev_i32_e32 v5, 31, v4
	v_lshl_add_u64 v[4:5], v[4:5], 4, s[14:15]
	v_add_co_u32_e32 v4, vcc, s23, v4
	s_nop 1
	v_addc_co_u32_e32 v5, vcc, 0, v5, vcc
	s_waitcnt vmcnt(0)
	v_pk_fma_f32 v[2:3], v[78:79], v[226:227], v[188:189]
	v_pk_fma_f32 v[4:5], v[82:83], v[224:225], v[186:187]
	v_max_f32_e64 v0, |v2|, |v3|
	v_max3_f32 v0, |v4|, |v5|, v0
	v_max3_f32 v0, v112, v110, v0
	s_waitcnt lgkmcnt(0)
	s_nop 1
	v_max_f32_dpp v0, v0, v0 quad_perm:[1,0,3,2] row_mask:0xf bank_mask:0xf
	s_waitcnt lgkmcnt(0)
	s_nop 1
	v_max_f32_dpp v0, v0, v0 quad_perm:[2,3,0,1] row_mask:0xf bank_mask:0xf
	s_waitcnt lgkmcnt(0)
	s_nop 1
	v_max_f32_dpp v0, v0, v0 row_half_mirror row_mask:0xf bank_mask:0xf
	s_waitcnt lgkmcnt(0)
	s_nop 1
	v_max_f32_dpp v0, v0, v0 row_mirror row_mask:0xf bank_mask:0xf
	s_waitcnt lgkmcnt(0)
	v_mov_b32_e32 v1, v0
	s_nop 1
	v_permlane16_swap_b32_e32 v0, v1
	v_max_f32_e32 v0, v0, v1
	s_waitcnt lgkmcnt(0)
	v_mov_b32_e32 v1, v0
	s_nop 1
	v_permlane32_swap_b32_e32 v0, v1
	v_max_f32_e32 v0, v0, v1
	v_cmp_lt_f32_e32 vcc, 0, v0
	v_mul_f32_e32 v0, 0x3c010204, v0
	s_nop 0
	v_cndmask_b32_e32 v0, 1.0, v0, vcc
	v_div_scale_f32 v1, s[6:7], v0, v0, 1.0
	v_rcp_f32_e32 v6, v1
	s_lshl_b64 s[6:7], s[4:5], 11
	s_add_u32 s6, s3, s6
	s_addc_u32 s7, s24, s7
	v_fma_f32 v7, -v1, v6, 1.0
	v_fmac_f32_e32 v6, v7, v6
	v_div_scale_f32 v7, vcc, 1.0, v0, 1.0
	v_mul_f32_e32 v78, v7, v6
	v_fma_f32 v79, -v1, v78, v7
	v_fmac_f32_e32 v78, v79, v6
	v_fma_f32 v1, -v1, v78, v7
	v_div_fmas_f32 v1, v1, v6, v78
	v_div_fixup_f32 v1, v1, v0, 1.0
	v_mul_f32_e32 v7, v85, v1
	v_mul_f32_e32 v6, v84, v1
	v_rndne_f32_e32 v7, v7
	v_mul_f32_e32 v76, v76, v1
	v_mul_f32_e32 v77, v77, v1
	v_rndne_f32_e32 v6, v6
	v_cvt_i32_f32_e32 v7, v7
	v_rndne_f32_e32 v76, v76
	v_rndne_f32_e32 v77, v77
	v_cvt_i32_f32_e32 v6, v6
	v_cvt_i32_f32_sdwa v76, v76 dst_sel:WORD_1 dst_unused:UNUSED_PAD src0_sel:DWORD
	v_cvt_i32_f32_e32 v77, v77
	v_lshlrev_b32_e32 v7, 8, v7
	v_and_b32_e32 v7, 0xff00, v7
	v_and_b32_e32 v76, 0xff0000, v76
	v_perm_b32 v6, v77, v6, s1
	v_or3_b32 v76, v6, v7, v76
	v_mbcnt_lo_u32_b32 v6, -1, 0
	v_mbcnt_hi_u32_b32 v6, -1, v6
	v_mul_f32_e32 v77, v87, v1
	v_ashrrev_i32_e32 v7, 31, v6
	v_lshl_add_u64 v[6:7], v[6:7], 2, s[6:7]
	global_store_dword v[6:7], v76, off
	v_mul_f32_e32 v7, v89, v1
	v_mul_f32_e32 v6, v88, v1
	v_rndne_f32_e32 v7, v7
	v_mul_f32_e32 v76, v86, v1
	v_rndne_f32_e32 v6, v6
	v_cvt_i32_f32_e32 v7, v7
	v_rndne_f32_e32 v76, v76
	v_rndne_f32_e32 v77, v77
	v_cvt_i32_f32_e32 v6, v6
	v_cvt_i32_f32_sdwa v76, v76 dst_sel:WORD_1 dst_unused:UNUSED_PAD src0_sel:DWORD
	v_cvt_i32_f32_e32 v77, v77
	v_lshlrev_b32_e32 v7, 8, v7
	v_and_b32_e32 v7, 0xff00, v7
	v_and_b32_e32 v76, 0xff0000, v76
	v_perm_b32 v6, v77, v6, s1
	v_or3_b32 v76, v6, v7, v76
	v_mbcnt_lo_u32_b32 v6, -1, 0
	v_mbcnt_hi_u32_b32 v6, -1, v6
	v_mul_f32_e32 v77, v91, v1
	v_ashrrev_i32_e32 v7, 31, v6
	v_lshl_add_u64 v[6:7], v[6:7], 2, s[6:7]
	global_store_dword v[6:7], v76, off offset:256
	v_mul_f32_e32 v7, v93, v1
	v_mul_f32_e32 v6, v92, v1
	v_rndne_f32_e32 v7, v7
	v_mul_f32_e32 v76, v90, v1
	v_rndne_f32_e32 v6, v6
	v_cvt_i32_f32_e32 v7, v7
	v_rndne_f32_e32 v76, v76
	v_rndne_f32_e32 v77, v77
	v_cvt_i32_f32_e32 v6, v6
	v_cvt_i32_f32_sdwa v76, v76 dst_sel:WORD_1 dst_unused:UNUSED_PAD src0_sel:DWORD
	v_cvt_i32_f32_e32 v77, v77
	v_lshlrev_b32_e32 v7, 8, v7
	v_and_b32_e32 v7, 0xff00, v7
	v_and_b32_e32 v76, 0xff0000, v76
	v_perm_b32 v6, v77, v6, s1
	v_or3_b32 v76, v6, v7, v76
	v_mbcnt_lo_u32_b32 v6, -1, 0
	v_mbcnt_hi_u32_b32 v6, -1, v6
	v_mul_f32_e32 v77, v95, v1
	v_ashrrev_i32_e32 v7, 31, v6
	v_lshl_add_u64 v[6:7], v[6:7], 2, s[6:7]
	global_store_dword v[6:7], v76, off offset:512
	v_mul_f32_e32 v7, v97, v1
	v_mul_f32_e32 v6, v96, v1
	v_rndne_f32_e32 v7, v7
	v_mul_f32_e32 v76, v94, v1
	v_rndne_f32_e32 v6, v6
	v_cvt_i32_f32_e32 v7, v7
	v_rndne_f32_e32 v76, v76
	v_rndne_f32_e32 v77, v77
	v_cvt_i32_f32_e32 v6, v6
	v_cvt_i32_f32_sdwa v76, v76 dst_sel:WORD_1 dst_unused:UNUSED_PAD src0_sel:DWORD
	v_cvt_i32_f32_e32 v77, v77
	v_lshlrev_b32_e32 v7, 8, v7
	v_and_b32_e32 v7, 0xff00, v7
	v_and_b32_e32 v76, 0xff0000, v76
	v_perm_b32 v6, v77, v6, s1
	v_or3_b32 v76, v6, v7, v76
	v_mbcnt_lo_u32_b32 v6, -1, 0
	v_mbcnt_hi_u32_b32 v6, -1, v6
	v_mul_f32_e32 v77, v99, v1
	v_ashrrev_i32_e32 v7, 31, v6
	v_lshl_add_u64 v[6:7], v[6:7], 2, s[6:7]
	global_store_dword v[6:7], v76, off offset:768
; #define FLANE lane_id()
; __device__ __forceinline__ void p6_router(Frame& F) {
;     ...
;                 f32x4 v[8]; float s = 0.f;
; #pragma unroll
;                 for (int j = 0; j < 8; ++j) { const v2u w = raw[rr][j]; v[j] = (f32x4){bf_lo(w.x), bf_hi(w.x), bf_lo(w.y), bf_hi(w.y)}; s += (v[j][0] + v[j][1]) + (v[j][2] + v[j][3]); }
;                 const float mean = wave_sum(s) * (1.f / D); float s2 = 0.f;
;     ...
;                 for (int j = 0; j < 8; ++j) { const int q0 = (int)__builtin_rintf(v[j][0] * inv), q1 = (int)__builtin_rintf(v[j][1] * inv), q2 = (int)__builtin_rintf(v[j][2] * inv), q3 = (int)__builtin_rintf(v[j][3] * inv);
;                     h1q[(size_t)m * (D / 4) + FLANE + 64 * j] = (unsigned)(q0 & 0xff) | ((unsigned)(q1 & 0xff) << 8) | ((unsigned)(q2 & 0xff) << 16) | ((unsigned)(q3 & 0xff) << 24); }
;                 if (FLANE == 0) { st1[2 * m] = mean; st1[2 * m + 1] = rstd; stl[2 * row] = mean; stl[2 * row + 1] = rstd; sxg[m] = sc; sxl[row] = sc; }
	v_mul_f32_e32 v7, v101, v1
	v_mul_f32_e32 v6, v100, v1
	v_rndne_f32_e32 v7, v7
	v_mul_f32_e32 v76, v98, v1
	v_rndne_f32_e32 v6, v6
	v_cvt_i32_f32_e32 v7, v7
	v_rndne_f32_e32 v76, v76
	v_rndne_f32_e32 v77, v77
	v_cvt_i32_f32_e32 v6, v6
	v_cvt_i32_f32_sdwa v76, v76 dst_sel:WORD_1 dst_unused:UNUSED_PAD src0_sel:DWORD
	v_cvt_i32_f32_e32 v77, v77
	v_lshlrev_b32_e32 v7, 8, v7
	v_and_b32_e32 v7, 0xff00, v7
	v_and_b32_e32 v76, 0xff0000, v76
	v_perm_b32 v6, v77, v6, s1
	v_or3_b32 v76, v6, v7, v76
	v_mbcnt_lo_u32_b32 v6, -1, 0
	v_mbcnt_hi_u32_b32 v6, -1, v6
	v_mul_f32_e32 v77, v103, v1
	v_ashrrev_i32_e32 v7, 31, v6
	v_lshl_add_u64 v[6:7], v[6:7], 2, s[6:7]
	global_store_dword v[6:7], v76, off offset:1024
	v_mul_f32_e32 v7, v105, v1
	v_mul_f32_e32 v6, v104, v1
	v_rndne_f32_e32 v7, v7
	v_mul_f32_e32 v76, v102, v1
	v_rndne_f32_e32 v6, v6
	v_cvt_i32_f32_e32 v7, v7
	v_rndne_f32_e32 v76, v76
	v_rndne_f32_e32 v77, v77
	v_cvt_i32_f32_e32 v6, v6
	v_cvt_i32_f32_sdwa v76, v76 dst_sel:WORD_1 dst_unused:UNUSED_PAD src0_sel:DWORD
	v_cvt_i32_f32_e32 v77, v77
	v_lshlrev_b32_e32 v7, 8, v7
	v_and_b32_e32 v7, 0xff00, v7
	v_and_b32_e32 v76, 0xff0000, v76
	v_perm_b32 v6, v77, v6, s1
	v_or3_b32 v76, v6, v7, v76
	v_mbcnt_lo_u32_b32 v6, -1, 0
	v_mbcnt_hi_u32_b32 v6, -1, v6
	v_mul_f32_e32 v77, v107, v1
	v_ashrrev_i32_e32 v7, 31, v6
	v_lshl_add_u64 v[6:7], v[6:7], 2, s[6:7]
	global_store_dword v[6:7], v76, off offset:1280
	v_mul_f32_e32 v7, v109, v1
	v_mul_f32_e32 v6, v108, v1
	v_rndne_f32_e32 v7, v7
	v_mul_f32_e32 v76, v106, v1
	v_rndne_f32_e32 v6, v6
	v_cvt_i32_f32_e32 v7, v7
	v_rndne_f32_e32 v76, v76
	v_rndne_f32_e32 v77, v77
	v_mul_f32_e32 v5, v5, v1
	v_cvt_i32_f32_e32 v6, v6
	v_cvt_i32_f32_sdwa v76, v76 dst_sel:WORD_1 dst_unused:UNUSED_PAD src0_sel:DWORD
	v_cvt_i32_f32_e32 v77, v77
	v_mul_f32_e32 v4, v4, v1
	v_rndne_f32_e32 v5, v5
	v_mul_f32_e32 v2, v2, v1
	v_mul_f32_e32 v1, v3, v1
	v_rndne_f32_e32 v4, v4
	v_cvt_i32_f32_e32 v5, v5
	v_rndne_f32_e32 v2, v2
	v_rndne_f32_e32 v1, v1
	v_cvt_i32_f32_e32 v4, v4
	v_cvt_i32_f32_sdwa v2, v2 dst_sel:WORD_1 dst_unused:UNUSED_PAD src0_sel:DWORD
	v_cvt_i32_f32_e32 v1, v1
	v_lshlrev_b32_e32 v7, 8, v7
	v_and_b32_e32 v7, 0xff00, v7
	v_and_b32_e32 v76, 0xff0000, v76
	v_perm_b32 v6, v77, v6, s1
	v_or3_b32 v76, v6, v7, v76
	v_mbcnt_lo_u32_b32 v6, -1, 0
	v_mbcnt_hi_u32_b32 v6, -1, v6
	v_lshlrev_b32_e32 v3, 8, v5
	v_ashrrev_i32_e32 v7, 31, v6
	v_lshl_add_u64 v[6:7], v[6:7], 2, s[6:7]
	v_and_b32_e32 v3, 0xff00, v3
	v_and_b32_e32 v2, 0xff0000, v2
	v_perm_b32 v1, v1, v4, s1
	global_store_dword v[6:7], v76, off offset:1536
	v_or3_b32 v1, v1, v3, v2
	v_mbcnt_lo_u32_b32 v2, -1, 0
	v_mbcnt_hi_u32_b32 v2, -1, v2
	s_nop 0
	v_ashrrev_i32_e32 v3, 31, v2
	v_lshl_add_u64 v[2:3], v[2:3], 2, s[6:7]
	global_store_dword v[2:3], v1, off offset:1792
	v_mbcnt_lo_u32_b32 v1, -1, 0
	v_mbcnt_hi_u32_b32 v1, -1, v1
	s_nop 0
	v_cmp_eq_u32_e32 vcc, 0, v1
	s_and_saveexec_b64 s[6:7], vcc
	s_cbranch_execz .LBB0_1489
	s_lshl_b32 s8, s4, 1
	s_ashr_i32 s9, s8, 31
	s_lshl_b64 s[8:9], s[8:9], 2
	s_add_u32 s8, s27, s8
	s_addc_u32 s9, s64, s9
	v_readlane_b32 s0, v255, 44
	s_lshl_b64 s[4:5], s[4:5], 2
	v_mul_f32_e32 v2, 0x3a000000, v80
	v_mov_b32_e32 v3, v32
	v_mov_b32_e32 v1, s0
	s_add_u32 s4, s25, s4
	v_readlane_b32 s0, v255, 31
	ds_write_b64 v1, v[2:3]
	s_addc_u32 s5, s26, s5
	v_mov_b32_e32 v1, s0
	global_store_dwordx2 v33, v[2:3], s[8:9]
	global_store_dword v33, v0, s[4:5]
	ds_write_b32 v1, v0
.LBB0_1489:
	s_or_b64 exec, exec, s[6:7]
	v_lshlrev_b32_e32 v77, 16, v74
	v_lshlrev_b32_e32 v76, 16, v72
	v_and_b32_e32 v89, 0xffff0000, v74
	v_and_b32_e32 v88, 0xffff0000, v72
	v_lshlrev_b32_e32 v91, 16, v75
	v_lshlrev_b32_e32 v90, 16, v73
	v_and_b32_e32 v93, 0xffff0000, v75
	v_and_b32_e32 v92, 0xffff0000, v73
	v_pk_add_f32 v[0:1], v[76:77], v[88:89]
	v_pk_add_f32 v[2:3], v[90:91], v[92:93]
	v_lshlrev_b32_e32 v75, 16, v71
	v_pk_add_f32 v[0:1], v[0:1], v[2:3]
	v_lshlrev_b32_e32 v74, 16, v70
	v_add_f32_e32 v0, 0, v0
	v_and_b32_e32 v95, 0xffff0000, v71
	v_and_b32_e32 v94, 0xffff0000, v70
	v_add_f32_e32 v6, v0, v1
	v_pk_add_f32 v[0:1], v[74:75], v[94:95]
	v_lshlrev_b32_e32 v78, 16, v68
	v_and_b32_e32 v79, 0xffff0000, v68
	v_lshlrev_b32_e32 v80, 16, v69
	v_and_b32_e32 v81, 0xffff0000, v69
	v_and_b32_e32 v87, 0xffff0000, v66
	v_pk_add_f32 v[0:1], v[0:1], v[0:1] op_sel:[0,1] op_sel_hi:[1,0]
	v_add_f32_e32 v84, v78, v79
	v_add_f32_e32 v82, v80, v81
	v_lshlrev_b32_e32 v7, 16, v66
	v_lshlrev_b32_e32 v85, 16, v67
	v_and_b32_e32 v83, 0xffff0000, v67
	v_mov_b32_e32 v1, v87
	v_pk_add_f32 v[0:1], v[6:7], v[0:1]
	v_pk_add_f32 v[2:3], v[84:85], v[82:83]
	v_lshlrev_b32_e32 v5, 16, v65
	v_lshlrev_b32_e32 v4, 16, v64
	v_and_b32_e32 v97, 0xffff0000, v65
	v_and_b32_e32 v96, 0xffff0000, v64
	v_pk_add_f32 v[68:69], v[0:1], v[2:3]
	v_pk_add_f32 v[70:71], v[4:5], v[96:97]
	v_lshlrev_b32_e32 v0, 16, v62
	v_and_b32_e32 v1, 0xffff0000, v62
	v_lshlrev_b32_e32 v2, 16, v63
	v_and_b32_e32 v3, 0xffff0000, v63
	v_lshlrev_b32_e32 v66, 16, v60
	v_and_b32_e32 v67, 0xffff0000, v60
	v_lshlrev_b32_e32 v65, 16, v61
	v_and_b32_e32 v63, 0xffff0000, v61
	v_pk_add_f32 v[60:61], v[68:69], v[68:69] op_sel:[0,1] op_sel_hi:[1,0]
	v_pk_add_f32 v[68:69], v[70:71], v[70:71] op_sel:[0,1] op_sel_hi:[1,0]
	v_add_f32_e32 v64, v0, v1
	v_add_f32_e32 v62, v2, v3
	v_mov_b32_e32 v61, v66
	v_mov_b32_e32 v69, v67
	v_pk_add_f32 v[60:61], v[60:61], v[68:69]
	v_pk_add_f32 v[68:69], v[64:65], v[62:63]
	s_nop 0
	v_pk_add_f32 v[60:61], v[60:61], v[68:69]
	s_nop 0
	v_add_f32_e32 v6, v60, v61
	s_waitcnt lgkmcnt(0)
	s_nop 1
	v_add_f32_dpp v6, v6, v6 quad_perm:[1,0,3,2] row_mask:0xf bank_mask:0xf
	s_waitcnt lgkmcnt(0)
; __device__ __forceinline__ void p6_router(Frame& F) {
;     ...
;                 const float mean = wave_sum(s) * (1.f / D); float s2 = 0.f;
; #pragma unroll
;                 for (int j = 0; j < 8; ++j) { v[j] = v[j] - mean; s2 += (v[j][0] * v[j][0] + v[j][1] * v[j][1]) + (v[j][2] * v[j][2] + v[j][3] * v[j][3]); }
;                 const float rstd = 1.f / sqrtf(wave_sum(s2) * (1.f / D) + LN_EPS);
	s_nop 1
	v_add_f32_dpp v6, v6, v6 quad_perm:[2,3,0,1] row_mask:0xf bank_mask:0xf
	s_waitcnt lgkmcnt(0)
	s_nop 1
	v_add_f32_dpp v6, v6, v6 row_half_mirror row_mask:0xf bank_mask:0xf
	s_waitcnt lgkmcnt(0)
	s_nop 1
	v_add_f32_dpp v6, v6, v6 row_mirror row_mask:0xf bank_mask:0xf
	s_waitcnt lgkmcnt(0)
	v_mov_b32_e32 v32, v6
	s_nop 1
	v_permlane16_swap_b32_e32 v6, v32
	v_add_f32_e32 v6, v6, v32
	s_waitcnt lgkmcnt(0)
	v_mov_b32_e32 v32, v6
	s_nop 1
	v_permlane32_swap_b32_e32 v6, v32
	v_add_f32_e32 v64, v6, v32
	v_fmac_f32_e32 v92, 0xba000000, v64
	v_fmac_f32_e32 v88, 0xba000000, v64
	v_fmac_f32_e32 v93, 0xba000000, v64
	v_fmac_f32_e32 v89, 0xba000000, v64
	v_fmac_f32_e32 v90, 0xba000000, v64
	v_fmac_f32_e32 v76, 0xba000000, v64
	v_fmac_f32_e32 v91, 0xba000000, v64
	v_fmac_f32_e32 v77, 0xba000000, v64
	v_mov_b32_e32 v71, v89
	v_mov_b32_e32 v61, v88
	v_pk_mul_f32 v[68:69], v[88:89], v[88:89]
	v_pk_mul_f32 v[88:89], v[92:93], v[92:93]
	v_mov_b32_e32 v70, v77
	v_mov_b32_e32 v60, v76
	v_pk_fma_f32 v[76:77], v[76:77], v[76:77], v[68:69]
	v_pk_fma_f32 v[88:89], v[90:91], v[90:91], v[88:89]
	v_fmac_f32_e32 v94, 0xba000000, v64
	v_pk_add_f32 v[76:77], v[76:77], v[88:89]
	v_fmac_f32_e32 v95, 0xba000000, v64
	v_fmac_f32_e32 v75, 0xba000000, v64
	v_pk_add_f32 v[88:89], v[76:77], v[76:77] op_sel_hi:[0,1]
	v_fmac_f32_e32 v74, 0xba000000, v64
	v_mov_b32_e32 v76, v75
	v_mov_b32_e32 v77, v95
	v_mov_b32_e32 v75, v94
	v_mov_b32_e32 v72, v91
	v_mov_b32_e32 v73, v93
	v_mov_b32_e32 v68, v90
	v_mov_b32_e32 v69, v92
	v_pk_mul_f32 v[90:91], v[76:77], v[76:77]
	v_pk_mul_f32 v[92:93], v[74:75], v[74:75]
	v_fmac_f32_e32 v78, 0xba000000, v64
	v_pk_mov_b32 v[94:95], v[92:93], v[90:91] op_sel:[1,0]
	v_mov_b32_e32 v93, v91
	v_fmac_f32_e32 v79, 0xba000000, v64
	v_fmac_f32_e32 v80, 0xba000000, v64
	v_mul_f32_e32 v6, v78, v78
	v_pk_add_f32 v[90:91], v[94:95], v[92:93]
	v_fmac_f32_e32 v81, 0xba000000, v64
	v_pk_fma_f32 v[92:93], v[78:79], v[78:79], v[6:7] op_sel_hi:[1,1,0]
	v_mul_f32_e32 v6, v80, v80
	v_pk_add_f32 v[90:91], v[90:91], v[90:91] op_sel_hi:[0,1]
	v_pk_fma_f32 v[94:95], v[80:81], v[80:81], v[6:7] op_sel_hi:[1,1,0]
	v_fmac_f32_e32 v83, 0xba000000, v64
	v_fmac_f32_e32 v85, 0xba000000, v64
	v_fmac_f32_e32 v87, 0xba000000, v64
	v_fmac_f32_e32 v7, 0xba000000, v64
	v_mul_f32_e32 v92, v7, v7
	v_mul_f32_e32 v94, v87, v87
	v_mul_f32_e32 v90, v85, v85
	v_mul_f32_e32 v88, v83, v83
	v_pk_add_f32 v[92:93], v[92:93], v[94:95]
	v_pk_add_f32 v[88:89], v[90:91], v[88:89]
	v_fmac_f32_e32 v96, 0xba000000, v64
	v_pk_add_f32 v[88:89], v[92:93], v[88:89]
	v_fmac_f32_e32 v97, 0xba000000, v64
	v_fmac_f32_e32 v5, 0xba000000, v64
	v_pk_add_f32 v[90:91], v[88:89], v[88:89] op_sel_hi:[0,1]
	v_fmac_f32_e32 v4, 0xba000000, v64
	v_mov_b32_e32 v88, v5
	v_mov_b32_e32 v89, v97
	v_mov_b32_e32 v5, v96
	v_pk_mul_f32 v[92:93], v[88:89], v[88:89]
	v_pk_mul_f32 v[94:95], v[4:5], v[4:5]
	v_fmac_f32_e32 v0, 0xba000000, v64
	v_pk_mov_b32 v[96:97], v[94:95], v[92:93] op_sel:[1,0]
	v_mov_b32_e32 v95, v93
	v_fmac_f32_e32 v1, 0xba000000, v64
	v_fmac_f32_e32 v2, 0xba000000, v64
	v_mul_f32_e32 v6, v0, v0
	v_pk_add_f32 v[92:93], v[96:97], v[94:95]
	v_fmac_f32_e32 v3, 0xba000000, v64
	v_pk_fma_f32 v[94:95], v[0:1], v[0:1], v[6:7] op_sel_hi:[1,1,0]
	v_mul_f32_e32 v6, v2, v2
	v_pk_add_f32 v[92:93], v[92:93], v[92:93] op_sel_hi:[0,1]
	v_pk_fma_f32 v[96:97], v[2:3], v[2:3], v[6:7] op_sel_hi:[1,1,0]
	v_fmac_f32_e32 v63, 0xba000000, v64
	v_fmac_f32_e32 v65, 0xba000000, v64
	v_fmac_f32_e32 v67, 0xba000000, v64
	v_fmac_f32_e32 v66, 0xba000000, v64
	v_mul_f32_e32 v94, v66, v66
	v_mul_f32_e32 v96, v67, v67
	v_mul_f32_e32 v92, v65, v65
	v_mul_f32_e32 v90, v63, v63
	v_pk_add_f32 v[94:95], v[94:95], v[96:97]
	v_pk_add_f32 v[90:91], v[92:93], v[90:91]
	s_nop 0
	v_pk_add_f32 v[90:91], v[94:95], v[90:91]
	s_nop 0
	v_add_f32_e32 v6, v90, v91
	v_mbcnt_lo_u32_b32 v90, -1, 0
	v_mbcnt_hi_u32_b32 v90, -1, v90
	v_ashrrev_i32_e32 v91, 31, v90
	v_lshl_add_u64 v[90:91], v[90:91], 4, s[12:13]
	v_mbcnt_lo_u32_b32 v94, -1, 0
	v_mbcnt_hi_u32_b32 v94, -1, v94
	s_waitcnt lgkmcnt(0)
	s_nop 1
	v_add_f32_dpp v6, v6, v6 quad_perm:[1,0,3,2] row_mask:0xf bank_mask:0xf
	v_ashrrev_i32_e32 v95, 31, v94
	v_lshl_add_u64 v[94:95], v[94:95], 4, s[14:15]
	s_waitcnt lgkmcnt(0)
	s_nop 1
	v_add_f32_dpp v6, v6, v6 quad_perm:[2,3,0,1] row_mask:0xf bank_mask:0xf
	s_waitcnt lgkmcnt(0)
	s_nop 1
	v_add_f32_dpp v6, v6, v6 row_half_mirror row_mask:0xf bank_mask:0xf
	s_waitcnt lgkmcnt(0)
	s_nop 1
	v_add_f32_dpp v6, v6, v6 row_mirror row_mask:0xf bank_mask:0xf
	s_waitcnt lgkmcnt(0)
	v_mov_b32_e32 v32, v6
	s_nop 1
	v_permlane16_swap_b32_e32 v6, v32
	v_add_f32_e32 v6, v6, v32
	s_waitcnt lgkmcnt(0)
	v_mov_b32_e32 v32, v6
	s_nop 1
	v_permlane32_swap_b32_e32 v6, v32
	v_add_f32_e32 v6, v6, v32
	v_fmamk_f32 v6, v6, 0x3a000000, v166
	v_cmp_gt_f32_e32 vcc, s22, v6
	v_mul_f32_e32 v32, 0x4f800000, v6
	s_nop 0
	v_cndmask_b32_e32 v6, v6, v32, vcc
	v_sqrt_f32_e32 v32, v6
	s_nop 0
	v_add_u32_e32 v62, -1, v32
	v_fma_f32 v82, -v62, v32, v6
	v_cmp_ge_f32_e64 s[4:5], 0, v82
	v_add_u32_e32 v82, 1, v32
	s_nop 0
	v_cndmask_b32_e64 v62, v32, v62, s[4:5]
	v_fma_f32 v32, -v82, v32, v6
	v_cmp_lt_f32_e64 s[4:5], 0, v32
	s_nop 1
	v_cndmask_b32_e64 v32, v62, v82, s[4:5]
	v_mul_f32_e32 v62, 0x37800000, v32
	v_cndmask_b32_e32 v32, v32, v62, vcc
	v_cmp_class_f32_e32 vcc, v6, v167
	s_nop 1
	v_cndmask_b32_e32 v6, v32, v6, vcc
	v_div_scale_f32 v32, s[4:5], v6, v6, 1.0
	v_rcp_f32_e32 v62, v32
	s_add_i32 s4, s42, s73
	s_ashr_i32 s5, s4, 31
	v_fma_f32 v82, -v32, v62, 1.0
	v_fmac_f32_e32 v62, v82, v62
	v_div_scale_f32 v82, vcc, 1.0, v6, 1.0
	v_mul_f32_e32 v84, v82, v62
	v_fma_f32 v86, -v32, v84, v82
	v_fmac_f32_e32 v84, v86, v62
	v_fma_f32 v32, -v32, v84, v82
	v_div_fmas_f32 v32, v32, v62, v84
	v_div_fixup_f32 v32, v32, v6, 1.0
	v_pk_mul_f32 v[98:99], v[60:61], v[32:33] op_sel_hi:[1,0]
	v_pk_mul_f32 v[60:61], v[68:69], v[32:33] op_sel_hi:[1,0]
	v_mov_b32_e32 v86, v7
	v_pk_mul_f32 v[4:5], v[4:5], v[32:33] op_sel_hi:[1,0]
	v_pk_mul_f32 v[2:3], v[2:3], v[32:33] op_sel_hi:[1,0]
	v_pk_mul_f32 v[0:1], v[0:1], v[32:33] op_sel_hi:[1,0]
	v_pk_mul_f32 v[66:67], v[66:67], v[32:33] op_sel_hi:[1,0]
	s_waitcnt vmcnt(0)
; #define GAS __attribute__((address_space(1)))
; #define FLANE lane_id()
; __device__ __forceinline__ void p6_router(Frame& F) {
;     ...
;                 for (int j = 0; j < 8; ++j) { const f32x4 g = *((const GAS f32x4*)F.ln1_g + FLANE + 64 * j), b = *((const GAS f32x4*)F.ln1_b + FLANE + 64 * j);
;                     v[j] = v[j] * rstd * g + b; am = fmaxf(am, fmaxf(fmaxf(fabsf(v[j][0]), fabsf(v[j][1])), fmaxf(fabsf(v[j][2]), fabsf(v[j][3])))); }
	v_pk_fma_f32 v[68:69], v[196:197], v[98:99], v[228:229]
	v_mbcnt_lo_u32_b32 v90, -1, 0
	v_mbcnt_hi_u32_b32 v90, -1, v90
	v_pk_fma_f32 v[60:61], v[198:199], v[60:61], v[230:231]
	v_ashrrev_i32_e32 v91, 31, v90
	v_lshl_add_u64 v[90:91], v[90:91], 4, s[12:13]
	v_mbcnt_lo_u32_b32 v94, -1, 0
	v_mbcnt_hi_u32_b32 v94, -1, v94
	v_pk_mul_f32 v[98:99], v[70:71], v[32:33] op_sel_hi:[1,0]
	v_ashrrev_i32_e32 v95, 31, v94
	v_lshl_add_u64 v[94:95], v[94:95], 4, s[14:15]
	v_pk_mul_f32 v[70:71], v[72:73], v[32:33] op_sel_hi:[1,0]
	v_max_f32_e64 v6, |v60|, |v61|
	v_max3_f32 v6, |v68|, |v69|, v6
	s_waitcnt vmcnt(0)
	v_pk_fma_f32 v[72:73], v[200:201], v[98:99], v[232:233]
	v_mbcnt_lo_u32_b32 v90, -1, 0
	v_mbcnt_hi_u32_b32 v90, -1, v90
	v_pk_fma_f32 v[70:71], v[202:203], v[70:71], v[234:235]
	v_ashrrev_i32_e32 v91, 31, v90
	v_lshl_add_u64 v[90:91], v[90:91], 4, s[12:13]
	v_mbcnt_lo_u32_b32 v94, -1, 0
	v_mbcnt_hi_u32_b32 v94, -1, v94
	v_pk_mul_f32 v[98:99], v[74:75], v[32:33] op_sel_hi:[1,0]
	v_ashrrev_i32_e32 v95, 31, v94
	v_lshl_add_u64 v[94:95], v[94:95], 4, s[14:15]
	v_pk_mul_f32 v[74:75], v[76:77], v[32:33] op_sel_hi:[1,0]
	v_max_f32_e64 v62, |v70|, |v71|
	v_max3_f32 v62, |v72|, |v73|, v62
	v_max3_f32 v6, v6, 0, v62
	s_waitcnt vmcnt(0)
	v_pk_fma_f32 v[76:77], v[204:205], v[98:99], v[236:237]
	v_mbcnt_lo_u32_b32 v90, -1, 0
	v_mbcnt_hi_u32_b32 v90, -1, v90
	v_pk_fma_f32 v[74:75], v[206:207], v[74:75], v[238:239]
	v_ashrrev_i32_e32 v91, 31, v90
	v_lshl_add_u64 v[90:91], v[90:91], 4, s[12:13]
	v_mbcnt_lo_u32_b32 v94, -1, 0
	v_mbcnt_hi_u32_b32 v94, -1, v94
	v_pk_mul_f32 v[98:99], v[78:79], v[32:33] op_sel_hi:[1,0]
	v_ashrrev_i32_e32 v95, 31, v94
	v_lshl_add_u64 v[94:95], v[94:95], 4, s[14:15]
	v_pk_mul_f32 v[78:79], v[80:81], v[32:33] op_sel_hi:[1,0]
	v_max_f32_e64 v62, |v74|, |v75|
	v_max3_f32 v62, |v76|, |v77|, v62
	s_waitcnt vmcnt(0)
	v_pk_fma_f32 v[80:81], v[208:209], v[98:99], v[240:241]
	v_mbcnt_lo_u32_b32 v90, -1, 0
	v_mbcnt_hi_u32_b32 v90, -1, v90
	v_pk_fma_f32 v[78:79], v[210:211], v[78:79], v[242:243]
	v_ashrrev_i32_e32 v91, 31, v90
	v_lshl_add_u64 v[90:91], v[90:91], 4, s[12:13]
	v_add_co_u32_e32 v90, vcc, s23, v90
	v_max_f32_e64 v82, |v78|, |v79|
	s_nop 0
	v_addc_co_u32_e32 v91, vcc, 0, v91, vcc
	v_mbcnt_lo_u32_b32 v94, -1, 0
	v_mbcnt_hi_u32_b32 v94, -1, v94
	v_max3_f32 v82, |v80|, |v81|, v82
	v_ashrrev_i32_e32 v95, 31, v94
	v_lshl_add_u64 v[94:95], v[94:95], 4, s[14:15]
	v_add_co_u32_e32 v94, vcc, s23, v94
	v_max3_f32 v62, v6, v62, v82
	s_nop 0
	v_addc_co_u32_e32 v95, vcc, 0, v95, vcc
	v_mov_b32_e32 v82, v85
	v_pk_mul_f32 v[82:83], v[82:83], v[32:33] op_sel_hi:[1,0]
	v_pk_mul_f32 v[6:7], v[86:87], v[32:33] op_sel_hi:[1,0]
	s_waitcnt vmcnt(0)
	v_pk_fma_f32 v[82:83], v[214:215], v[82:83], v[246:247]
	v_pk_fma_f32 v[84:85], v[212:213], v[6:7], v[244:245]
	v_max_f32_e64 v6, |v82|, |v83|
	v_max3_f32 v98, |v84|, |v85|, v6
	v_mbcnt_lo_u32_b32 v6, -1, 0
	v_mbcnt_hi_u32_b32 v6, -1, v6
	s_nop 0
	v_ashrrev_i32_e32 v7, 31, v6
	v_lshl_add_u64 v[6:7], v[6:7], 4, s[12:13]
	v_add_co_u32_e32 v6, vcc, s23, v6
	s_nop 1
	v_addc_co_u32_e32 v7, vcc, 0, v7, vcc
	v_mbcnt_lo_u32_b32 v6, -1, 0
	v_mbcnt_hi_u32_b32 v6, -1, v6
	s_nop 0
	v_ashrrev_i32_e32 v7, 31, v6
	v_lshl_add_u64 v[6:7], v[6:7], 4, s[14:15]
	v_add_co_u32_e32 v6, vcc, s23, v6
	s_nop 1
	v_addc_co_u32_e32 v7, vcc, 0, v7, vcc
	v_pk_mul_f32 v[6:7], v[88:89], v[32:33] op_sel_hi:[1,0]
	s_waitcnt vmcnt(0)
	v_pk_fma_f32 v[88:89], v[216:217], v[4:5], v[248:249]
	v_pk_fma_f32 v[86:87], v[218:219], v[6:7], v[250:251]
	s_nop 0
	v_max_f32_e64 v4, |v86|, |v87|
	v_max3_f32 v4, |v88|, |v89|, v4
	v_max3_f32 v96, v62, v98, v4
	v_mbcnt_lo_u32_b32 v4, -1, 0
	v_mbcnt_hi_u32_b32 v4, -1, v4
	v_mov_b32_e32 v62, v65
	v_ashrrev_i32_e32 v5, 31, v4
	v_lshl_add_u64 v[4:5], v[4:5], 4, s[12:13]
	v_add_co_u32_e32 v4, vcc, s23, v4
	v_pk_mul_f32 v[62:63], v[62:63], v[32:33] op_sel_hi:[1,0]
	s_nop 0
	v_addc_co_u32_e32 v5, vcc, 0, v5, vcc
	v_mbcnt_lo_u32_b32 v90, -1, 0
	v_mbcnt_hi_u32_b32 v90, -1, v90
	s_nop 0
	v_ashrrev_i32_e32 v91, 31, v90
	v_lshl_add_u64 v[90:91], v[90:91], 4, s[14:15]
	v_add_co_u32_e32 v90, vcc, s23, v90
	s_nop 1
	v_addc_co_u32_e32 v91, vcc, 0, v91, vcc
	s_waitcnt vmcnt(0)
	v_pk_fma_f32 v[90:91], v[2:3], v[222:223], v[184:185]
	v_pk_fma_f32 v[92:93], v[0:1], v[220:221], v[182:183]
	v_max_f32_e64 v0, |v90|, |v91|
	v_max3_f32 v94, |v92|, |v93|, v0
	v_mbcnt_lo_u32_b32 v0, -1, 0
	v_mbcnt_hi_u32_b32 v0, -1, v0
	s_nop 0
	v_ashrrev_i32_e32 v1, 31, v0
	v_lshl_add_u64 v[0:1], v[0:1], 4, s[12:13]
	v_add_co_u32_e32 v0, vcc, s23, v0
	s_nop 1
	v_addc_co_u32_e32 v1, vcc, 0, v1, vcc
	v_mbcnt_lo_u32_b32 v4, -1, 0
	v_mbcnt_hi_u32_b32 v4, -1, v4
	s_nop 0
	v_ashrrev_i32_e32 v5, 31, v4
	v_lshl_add_u64 v[4:5], v[4:5], 4, s[14:15]
	v_add_co_u32_e32 v4, vcc, s23, v4
	s_nop 1
	v_addc_co_u32_e32 v5, vcc, 0, v5, vcc
	s_waitcnt vmcnt(0)
	v_pk_fma_f32 v[2:3], v[62:63], v[226:227], v[188:189]
	v_pk_fma_f32 v[4:5], v[66:67], v[224:225], v[186:187]
	v_max_f32_e64 v0, |v2|, |v3|
	v_max3_f32 v0, |v4|, |v5|, v0
	v_max3_f32 v0, v96, v94, v0
	s_waitcnt lgkmcnt(0)
	s_nop 1
	v_max_f32_dpp v0, v0, v0 quad_perm:[1,0,3,2] row_mask:0xf bank_mask:0xf
	s_waitcnt lgkmcnt(0)
	s_nop 1
	v_max_f32_dpp v0, v0, v0 quad_perm:[2,3,0,1] row_mask:0xf bank_mask:0xf
	s_waitcnt lgkmcnt(0)
	s_nop 1
	v_max_f32_dpp v0, v0, v0 row_half_mirror row_mask:0xf bank_mask:0xf
	s_waitcnt lgkmcnt(0)
	s_nop 1
	v_max_f32_dpp v0, v0, v0 row_mirror row_mask:0xf bank_mask:0xf
	s_waitcnt lgkmcnt(0)
	v_mov_b32_e32 v1, v0
	s_nop 1
	v_permlane16_swap_b32_e32 v0, v1
	v_max_f32_e32 v0, v0, v1
	s_waitcnt lgkmcnt(0)
; #define FLANE lane_id()
; __device__ __forceinline__ void p6_router(Frame& F) {
;     ...
; #pragma unroll
;                 for (int o = 1; o < 64; o <<= 1) am = fmaxf(am, __shfl_xor(am, o));
;                 const float sc = am > 0.f ? am * (1.f / 127.f) : 1.f, inv = 1.f / sc;
; #pragma unroll
;                 for (int j = 0; j < 8; ++j) { const int q0 = (int)__builtin_rintf(v[j][0] * inv), q1 = (int)__builtin_rintf(v[j][1] * inv), q2 = (int)__builtin_rintf(v[j][2] * inv), q3 = (int)__builtin_rintf(v[j][3] * inv);
;                     h1q[(size_t)m * (D / 4) + FLANE + 64 * j] = (unsigned)(q0 & 0xff) | ((unsigned)(q1 & 0xff) << 8) | ((unsigned)(q2 & 0xff) << 16) | ((unsigned)(q3 & 0xff) << 24); }
;                 if (FLANE == 0) { st1[2 * m] = mean; st1[2 * m + 1] = rstd; stl[2 * row] = mean; stl[2 * row + 1] = rstd; sxg[m] = sc; sxl[row] = sc; }
	v_mov_b32_e32 v1, v0
	s_nop 1
	v_permlane32_swap_b32_e32 v0, v1
	v_max_f32_e32 v0, v0, v1
	v_cmp_lt_f32_e32 vcc, 0, v0
	v_mul_f32_e32 v0, 0x3c010204, v0
	s_nop 0
	v_cndmask_b32_e32 v0, 1.0, v0, vcc
	v_div_scale_f32 v1, s[6:7], v0, v0, 1.0
	v_rcp_f32_e32 v6, v1
	s_lshl_b64 s[6:7], s[4:5], 11
	s_add_u32 s6, s3, s6
	s_addc_u32 s7, s24, s7
	v_fma_f32 v7, -v1, v6, 1.0
	v_fmac_f32_e32 v6, v7, v6
	v_div_scale_f32 v7, vcc, 1.0, v0, 1.0
	v_mul_f32_e32 v62, v7, v6
	v_fma_f32 v63, -v1, v62, v7
	v_fmac_f32_e32 v62, v63, v6
	v_fma_f32 v1, -v1, v62, v7
	v_div_fmas_f32 v1, v1, v6, v62
	v_div_fixup_f32 v1, v1, v0, 1.0
	v_mul_f32_e32 v7, v69, v1
	v_mul_f32_e32 v6, v68, v1
	v_rndne_f32_e32 v7, v7
	v_mul_f32_e32 v60, v60, v1
	v_mul_f32_e32 v61, v61, v1
	v_rndne_f32_e32 v6, v6
	v_cvt_i32_f32_e32 v7, v7
	v_rndne_f32_e32 v60, v60
	v_rndne_f32_e32 v61, v61
	v_cvt_i32_f32_e32 v6, v6
	v_cvt_i32_f32_sdwa v60, v60 dst_sel:WORD_1 dst_unused:UNUSED_PAD src0_sel:DWORD
	v_cvt_i32_f32_e32 v61, v61
	v_lshlrev_b32_e32 v7, 8, v7
	v_and_b32_e32 v7, 0xff00, v7
	v_and_b32_e32 v60, 0xff0000, v60
	v_perm_b32 v6, v61, v6, s1
	v_or3_b32 v60, v6, v7, v60
	v_mbcnt_lo_u32_b32 v6, -1, 0
	v_mbcnt_hi_u32_b32 v6, -1, v6
	v_mul_f32_e32 v61, v71, v1
	v_ashrrev_i32_e32 v7, 31, v6
	v_lshl_add_u64 v[6:7], v[6:7], 2, s[6:7]
	global_store_dword v[6:7], v60, off
	v_mul_f32_e32 v7, v73, v1
	v_mul_f32_e32 v6, v72, v1
	v_rndne_f32_e32 v7, v7
	v_mul_f32_e32 v60, v70, v1
	v_rndne_f32_e32 v6, v6
	v_cvt_i32_f32_e32 v7, v7
	v_rndne_f32_e32 v60, v60
	v_rndne_f32_e32 v61, v61
	v_cvt_i32_f32_e32 v6, v6
	v_cvt_i32_f32_sdwa v60, v60 dst_sel:WORD_1 dst_unused:UNUSED_PAD src0_sel:DWORD
	v_cvt_i32_f32_e32 v61, v61
	v_lshlrev_b32_e32 v7, 8, v7
	v_and_b32_e32 v7, 0xff00, v7
	v_and_b32_e32 v60, 0xff0000, v60
	v_perm_b32 v6, v61, v6, s1
	v_or3_b32 v60, v6, v7, v60
	v_mbcnt_lo_u32_b32 v6, -1, 0
	v_mbcnt_hi_u32_b32 v6, -1, v6
	v_mul_f32_e32 v61, v75, v1
	v_ashrrev_i32_e32 v7, 31, v6
	v_lshl_add_u64 v[6:7], v[6:7], 2, s[6:7]
	global_store_dword v[6:7], v60, off offset:256
	v_mul_f32_e32 v7, v77, v1
	v_mul_f32_e32 v6, v76, v1
	v_rndne_f32_e32 v7, v7
	v_mul_f32_e32 v60, v74, v1
	v_rndne_f32_e32 v6, v6
	v_cvt_i32_f32_e32 v7, v7
	v_rndne_f32_e32 v60, v60
	v_rndne_f32_e32 v61, v61
	v_cvt_i32_f32_e32 v6, v6
	v_cvt_i32_f32_sdwa v60, v60 dst_sel:WORD_1 dst_unused:UNUSED_PAD src0_sel:DWORD
	v_cvt_i32_f32_e32 v61, v61
	v_lshlrev_b32_e32 v7, 8, v7
	v_and_b32_e32 v7, 0xff00, v7
	v_and_b32_e32 v60, 0xff0000, v60
	v_perm_b32 v6, v61, v6, s1
	v_or3_b32 v60, v6, v7, v60
	v_mbcnt_lo_u32_b32 v6, -1, 0
	v_mbcnt_hi_u32_b32 v6, -1, v6
	v_mul_f32_e32 v61, v79, v1
	v_ashrrev_i32_e32 v7, 31, v6
	v_lshl_add_u64 v[6:7], v[6:7], 2, s[6:7]
	global_store_dword v[6:7], v60, off offset:512
	v_mul_f32_e32 v7, v81, v1
	v_mul_f32_e32 v6, v80, v1
	v_rndne_f32_e32 v7, v7
	v_mul_f32_e32 v60, v78, v1
	v_rndne_f32_e32 v6, v6
	v_cvt_i32_f32_e32 v7, v7
	v_rndne_f32_e32 v60, v60
	v_rndne_f32_e32 v61, v61
	v_cvt_i32_f32_e32 v6, v6
	v_cvt_i32_f32_sdwa v60, v60 dst_sel:WORD_1 dst_unused:UNUSED_PAD src0_sel:DWORD
	v_cvt_i32_f32_e32 v61, v61
	v_lshlrev_b32_e32 v7, 8, v7
	v_and_b32_e32 v7, 0xff00, v7
	v_and_b32_e32 v60, 0xff0000, v60
	v_perm_b32 v6, v61, v6, s1
	v_or3_b32 v60, v6, v7, v60
	v_mbcnt_lo_u32_b32 v6, -1, 0
	v_mbcnt_hi_u32_b32 v6, -1, v6
	v_mul_f32_e32 v61, v83, v1
	v_ashrrev_i32_e32 v7, 31, v6
	v_lshl_add_u64 v[6:7], v[6:7], 2, s[6:7]
	global_store_dword v[6:7], v60, off offset:768
	v_mul_f32_e32 v7, v85, v1
	v_mul_f32_e32 v6, v84, v1
	v_rndne_f32_e32 v7, v7
	v_mul_f32_e32 v60, v82, v1
	v_rndne_f32_e32 v6, v6
	v_cvt_i32_f32_e32 v7, v7
	v_rndne_f32_e32 v60, v60
	v_rndne_f32_e32 v61, v61
	v_cvt_i32_f32_e32 v6, v6
	v_cvt_i32_f32_sdwa v60, v60 dst_sel:WORD_1 dst_unused:UNUSED_PAD src0_sel:DWORD
	v_cvt_i32_f32_e32 v61, v61
	v_lshlrev_b32_e32 v7, 8, v7
	v_and_b32_e32 v7, 0xff00, v7
	v_and_b32_e32 v60, 0xff0000, v60
	v_perm_b32 v6, v61, v6, s1
	v_or3_b32 v60, v6, v7, v60
	v_mbcnt_lo_u32_b32 v6, -1, 0
	v_mbcnt_hi_u32_b32 v6, -1, v6
	v_mul_f32_e32 v61, v87, v1
	v_ashrrev_i32_e32 v7, 31, v6
	v_lshl_add_u64 v[6:7], v[6:7], 2, s[6:7]
	global_store_dword v[6:7], v60, off offset:1024
	v_mul_f32_e32 v7, v89, v1
	v_mul_f32_e32 v6, v88, v1
	v_rndne_f32_e32 v7, v7
	v_mul_f32_e32 v60, v86, v1
	v_rndne_f32_e32 v6, v6
	v_cvt_i32_f32_e32 v7, v7
	v_rndne_f32_e32 v60, v60
	v_rndne_f32_e32 v61, v61
	v_cvt_i32_f32_e32 v6, v6
	v_cvt_i32_f32_sdwa v60, v60 dst_sel:WORD_1 dst_unused:UNUSED_PAD src0_sel:DWORD
	v_cvt_i32_f32_e32 v61, v61
	v_lshlrev_b32_e32 v7, 8, v7
	v_and_b32_e32 v7, 0xff00, v7
	v_and_b32_e32 v60, 0xff0000, v60
	v_perm_b32 v6, v61, v6, s1
	v_or3_b32 v60, v6, v7, v60
	v_mbcnt_lo_u32_b32 v6, -1, 0
	v_mbcnt_hi_u32_b32 v6, -1, v6
	v_mul_f32_e32 v61, v91, v1
	v_ashrrev_i32_e32 v7, 31, v6
	v_lshl_add_u64 v[6:7], v[6:7], 2, s[6:7]
	global_store_dword v[6:7], v60, off offset:1280
	v_mul_f32_e32 v7, v93, v1
	v_mul_f32_e32 v6, v92, v1
	v_rndne_f32_e32 v7, v7
	v_mul_f32_e32 v60, v90, v1
	v_rndne_f32_e32 v6, v6
	v_cvt_i32_f32_e32 v7, v7
	v_rndne_f32_e32 v60, v60
	v_rndne_f32_e32 v61, v61
	v_mul_f32_e32 v5, v5, v1
	v_cvt_i32_f32_e32 v6, v6
	v_cvt_i32_f32_sdwa v60, v60 dst_sel:WORD_1 dst_unused:UNUSED_PAD src0_sel:DWORD
	v_cvt_i32_f32_e32 v61, v61
	v_mul_f32_e32 v4, v4, v1
	v_rndne_f32_e32 v5, v5
	v_mul_f32_e32 v2, v2, v1
	v_mul_f32_e32 v1, v3, v1
	v_rndne_f32_e32 v4, v4
	v_cvt_i32_f32_e32 v5, v5
	v_rndne_f32_e32 v2, v2
	v_rndne_f32_e32 v1, v1
	v_cvt_i32_f32_e32 v4, v4
	v_cvt_i32_f32_sdwa v2, v2 dst_sel:WORD_1 dst_unused:UNUSED_PAD src0_sel:DWORD
	v_cvt_i32_f32_e32 v1, v1
	v_lshlrev_b32_e32 v7, 8, v7
	v_and_b32_e32 v7, 0xff00, v7
	v_and_b32_e32 v60, 0xff0000, v60
	v_perm_b32 v6, v61, v6, s1
	v_or3_b32 v60, v6, v7, v60
	v_mbcnt_lo_u32_b32 v6, -1, 0
	v_mbcnt_hi_u32_b32 v6, -1, v6
	v_lshlrev_b32_e32 v3, 8, v5
	v_ashrrev_i32_e32 v7, 31, v6
	v_lshl_add_u64 v[6:7], v[6:7], 2, s[6:7]
	v_and_b32_e32 v3, 0xff00, v3
	v_and_b32_e32 v2, 0xff0000, v2
	v_perm_b32 v1, v1, v4, s1
	global_store_dword v[6:7], v60, off offset:1536
	v_or3_b32 v1, v1, v3, v2
	v_mbcnt_lo_u32_b32 v2, -1, 0
	v_mbcnt_hi_u32_b32 v2, -1, v2
	s_nop 0
	v_ashrrev_i32_e32 v3, 31, v2
	v_lshl_add_u64 v[2:3], v[2:3], 2, s[6:7]
	global_store_dword v[2:3], v1, off offset:1792
	v_mbcnt_lo_u32_b32 v1, -1, 0
	v_mbcnt_hi_u32_b32 v1, -1, v1
	s_nop 0
	v_cmp_eq_u32_e32 vcc, 0, v1
	s_and_saveexec_b64 s[6:7], vcc
	s_cbranch_execz .LBB0_1491
	s_lshl_b32 s8, s4, 1
	s_ashr_i32 s9, s8, 31
	s_lshl_b64 s[8:9], s[8:9], 2
	s_add_u32 s8, s27, s8
	s_addc_u32 s9, s64, s9
	v_readlane_b32 s0, v255, 45
	s_lshl_b64 s[4:5], s[4:5], 2
	v_mul_f32_e32 v2, 0x3a000000, v64
	v_mov_b32_e32 v3, v32
	v_mov_b32_e32 v1, s0
	s_add_u32 s4, s25, s4
	v_readlane_b32 s0, v255, 32
	ds_write_b64 v1, v[2:3]
	s_addc_u32 s5, s26, s5
	v_mov_b32_e32 v1, s0
	global_store_dwordx2 v33, v[2:3], s[8:9]
	global_store_dword v33, v0, s[4:5]
	ds_write_b32 v1, v0
; __device__ __forceinline__ void p6_router(Frame& F) {
;     ...
;                 f32x4 v[8]; float s = 0.f;
; #pragma unroll
;                 for (int j = 0; j < 8; ++j) { const v2u w = raw[rr][j]; v[j] = (f32x4){bf_lo(w.x), bf_hi(w.x), bf_lo(w.y), bf_hi(w.y)}; s += (v[j][0] + v[j][1]) + (v[j][2] + v[j][3]); }
;                 const float mean = wave_sum(s) * (1.f / D); float s2 = 0.f;
; #pragma unroll
;                 for (int j = 0; j < 8; ++j) { v[j] = v[j] - mean; s2 += (v[j][0] * v[j][0] + v[j][1] * v[j][1]) + (v[j][2] * v[j][2] + v[j][3] * v[j][3]); }
.LBB0_1491:
	s_or_b64 exec, exec, s[6:7]
	v_lshlrev_b32_e32 v61, 16, v58
	v_lshlrev_b32_e32 v60, 16, v56
	v_and_b32_e32 v73, 0xffff0000, v58
	v_and_b32_e32 v72, 0xffff0000, v56
	v_lshlrev_b32_e32 v75, 16, v59
	v_lshlrev_b32_e32 v74, 16, v57
	v_and_b32_e32 v77, 0xffff0000, v59
	v_and_b32_e32 v76, 0xffff0000, v57
	v_pk_add_f32 v[0:1], v[60:61], v[72:73]
	v_pk_add_f32 v[2:3], v[74:75], v[76:77]
	v_lshlrev_b32_e32 v59, 16, v55
	v_pk_add_f32 v[0:1], v[0:1], v[2:3]
	v_lshlrev_b32_e32 v58, 16, v54
	v_add_f32_e32 v0, 0, v0
	v_and_b32_e32 v79, 0xffff0000, v55
	v_and_b32_e32 v78, 0xffff0000, v54
	v_add_f32_e32 v6, v0, v1
	v_pk_add_f32 v[0:1], v[58:59], v[78:79]
	v_lshlrev_b32_e32 v62, 16, v52
	v_and_b32_e32 v63, 0xffff0000, v52
	v_lshlrev_b32_e32 v64, 16, v53
	v_and_b32_e32 v65, 0xffff0000, v53
	v_and_b32_e32 v71, 0xffff0000, v50
	v_pk_add_f32 v[0:1], v[0:1], v[0:1] op_sel:[0,1] op_sel_hi:[1,0]
	v_add_f32_e32 v68, v62, v63
	v_add_f32_e32 v66, v64, v65
	v_lshlrev_b32_e32 v7, 16, v50
	v_lshlrev_b32_e32 v69, 16, v51
	v_and_b32_e32 v67, 0xffff0000, v51
	v_mov_b32_e32 v1, v71
	v_pk_add_f32 v[0:1], v[6:7], v[0:1]
	v_pk_add_f32 v[2:3], v[68:69], v[66:67]
	v_lshlrev_b32_e32 v5, 16, v49
	v_lshlrev_b32_e32 v4, 16, v48
	v_and_b32_e32 v81, 0xffff0000, v49
	v_and_b32_e32 v80, 0xffff0000, v48
	v_pk_add_f32 v[52:53], v[0:1], v[2:3]
	v_pk_add_f32 v[54:55], v[4:5], v[80:81]
	v_lshlrev_b32_e32 v0, 16, v46
	v_and_b32_e32 v1, 0xffff0000, v46
	v_lshlrev_b32_e32 v2, 16, v47
	v_and_b32_e32 v3, 0xffff0000, v47
	v_lshlrev_b32_e32 v50, 16, v44
	v_and_b32_e32 v51, 0xffff0000, v44
	v_lshlrev_b32_e32 v49, 16, v45
	v_and_b32_e32 v47, 0xffff0000, v45
	v_pk_add_f32 v[44:45], v[52:53], v[52:53] op_sel:[0,1] op_sel_hi:[1,0]
	v_pk_add_f32 v[52:53], v[54:55], v[54:55] op_sel:[0,1] op_sel_hi:[1,0]
	v_add_f32_e32 v48, v0, v1
	v_add_f32_e32 v46, v2, v3
	v_mov_b32_e32 v45, v50
	v_mov_b32_e32 v53, v51
	v_pk_add_f32 v[44:45], v[44:45], v[52:53]
	v_pk_add_f32 v[52:53], v[48:49], v[46:47]
	s_nop 0
	v_pk_add_f32 v[44:45], v[44:45], v[52:53]
	s_nop 0
	v_add_f32_e32 v6, v44, v45
	s_waitcnt lgkmcnt(0)
	s_nop 1
	v_add_f32_dpp v6, v6, v6 quad_perm:[1,0,3,2] row_mask:0xf bank_mask:0xf
	s_waitcnt lgkmcnt(0)
	s_nop 1
	v_add_f32_dpp v6, v6, v6 quad_perm:[2,3,0,1] row_mask:0xf bank_mask:0xf
	s_waitcnt lgkmcnt(0)
	s_nop 1
	v_add_f32_dpp v6, v6, v6 row_half_mirror row_mask:0xf bank_mask:0xf
	s_waitcnt lgkmcnt(0)
	s_nop 1
	v_add_f32_dpp v6, v6, v6 row_mirror row_mask:0xf bank_mask:0xf
	s_waitcnt lgkmcnt(0)
	v_mov_b32_e32 v32, v6
	s_nop 1
	v_permlane16_swap_b32_e32 v6, v32
	v_add_f32_e32 v6, v6, v32
	s_waitcnt lgkmcnt(0)
	v_mov_b32_e32 v32, v6
	s_nop 1
	v_permlane32_swap_b32_e32 v6, v32
	v_add_f32_e32 v48, v6, v32
	v_fmac_f32_e32 v76, 0xba000000, v48
	v_fmac_f32_e32 v72, 0xba000000, v48
	v_fmac_f32_e32 v77, 0xba000000, v48
	v_fmac_f32_e32 v73, 0xba000000, v48
	v_fmac_f32_e32 v74, 0xba000000, v48
	v_fmac_f32_e32 v60, 0xba000000, v48
	v_fmac_f32_e32 v75, 0xba000000, v48
	v_fmac_f32_e32 v61, 0xba000000, v48
	v_mov_b32_e32 v55, v73
	v_mov_b32_e32 v45, v72
	v_pk_mul_f32 v[52:53], v[72:73], v[72:73]
	v_pk_mul_f32 v[72:73], v[76:77], v[76:77]
	v_mov_b32_e32 v54, v61
	v_mov_b32_e32 v44, v60
	v_pk_fma_f32 v[60:61], v[60:61], v[60:61], v[52:53]
	v_pk_fma_f32 v[72:73], v[74:75], v[74:75], v[72:73]
	v_fmac_f32_e32 v78, 0xba000000, v48
	v_pk_add_f32 v[60:61], v[60:61], v[72:73]
	v_fmac_f32_e32 v79, 0xba000000, v48
	v_fmac_f32_e32 v59, 0xba000000, v48
	v_pk_add_f32 v[72:73], v[60:61], v[60:61] op_sel_hi:[0,1]
	v_fmac_f32_e32 v58, 0xba000000, v48
	v_mov_b32_e32 v60, v59
	v_mov_b32_e32 v61, v79
	v_mov_b32_e32 v59, v78
	v_mov_b32_e32 v56, v75
	v_mov_b32_e32 v57, v77
	v_mov_b32_e32 v52, v74
	v_mov_b32_e32 v53, v76
	v_pk_mul_f32 v[74:75], v[60:61], v[60:61]
	v_pk_mul_f32 v[76:77], v[58:59], v[58:59]
	v_fmac_f32_e32 v62, 0xba000000, v48
	v_pk_mov_b32 v[78:79], v[76:77], v[74:75] op_sel:[1,0]
	v_mov_b32_e32 v77, v75
	v_fmac_f32_e32 v63, 0xba000000, v48
	v_fmac_f32_e32 v64, 0xba000000, v48
	v_mul_f32_e32 v6, v62, v62
	v_pk_add_f32 v[74:75], v[78:79], v[76:77]
	v_fmac_f32_e32 v65, 0xba000000, v48
	v_pk_fma_f32 v[76:77], v[62:63], v[62:63], v[6:7] op_sel_hi:[1,1,0]
	v_mul_f32_e32 v6, v64, v64
	v_pk_add_f32 v[74:75], v[74:75], v[74:75] op_sel_hi:[0,1]
	v_pk_fma_f32 v[78:79], v[64:65], v[64:65], v[6:7] op_sel_hi:[1,1,0]
	v_fmac_f32_e32 v67, 0xba000000, v48
	v_fmac_f32_e32 v69, 0xba000000, v48
	v_fmac_f32_e32 v71, 0xba000000, v48
	v_fmac_f32_e32 v7, 0xba000000, v48
	v_mul_f32_e32 v76, v7, v7
	v_mul_f32_e32 v78, v71, v71
	v_mul_f32_e32 v74, v69, v69
	v_mul_f32_e32 v72, v67, v67
	v_pk_add_f32 v[76:77], v[76:77], v[78:79]
	v_pk_add_f32 v[72:73], v[74:75], v[72:73]
	v_fmac_f32_e32 v80, 0xba000000, v48
	v_pk_add_f32 v[72:73], v[76:77], v[72:73]
	v_fmac_f32_e32 v81, 0xba000000, v48
	v_fmac_f32_e32 v5, 0xba000000, v48
	v_pk_add_f32 v[74:75], v[72:73], v[72:73] op_sel_hi:[0,1]
	v_fmac_f32_e32 v4, 0xba000000, v48
	v_mov_b32_e32 v72, v5
	v_mov_b32_e32 v73, v81
	v_mov_b32_e32 v5, v80
	v_pk_mul_f32 v[76:77], v[72:73], v[72:73]
	v_pk_mul_f32 v[78:79], v[4:5], v[4:5]
	v_fmac_f32_e32 v0, 0xba000000, v48
	v_pk_mov_b32 v[80:81], v[78:79], v[76:77] op_sel:[1,0]
	v_mov_b32_e32 v79, v77
	v_fmac_f32_e32 v1, 0xba000000, v48
	v_fmac_f32_e32 v2, 0xba000000, v48
	v_mul_f32_e32 v6, v0, v0
	v_pk_add_f32 v[76:77], v[80:81], v[78:79]
	v_fmac_f32_e32 v3, 0xba000000, v48
	v_pk_fma_f32 v[78:79], v[0:1], v[0:1], v[6:7] op_sel_hi:[1,1,0]
	v_mul_f32_e32 v6, v2, v2
	v_pk_add_f32 v[76:77], v[76:77], v[76:77] op_sel_hi:[0,1]
	v_pk_fma_f32 v[80:81], v[2:3], v[2:3], v[6:7] op_sel_hi:[1,1,0]
	v_fmac_f32_e32 v47, 0xba000000, v48
	v_fmac_f32_e32 v49, 0xba000000, v48
	v_fmac_f32_e32 v51, 0xba000000, v48
	v_fmac_f32_e32 v50, 0xba000000, v48
	v_mul_f32_e32 v78, v50, v50
	v_mul_f32_e32 v80, v51, v51
	v_mul_f32_e32 v76, v49, v49
	v_mul_f32_e32 v74, v47, v47
	v_pk_add_f32 v[78:79], v[78:79], v[80:81]
	v_pk_add_f32 v[74:75], v[76:77], v[74:75]
	s_nop 0
	v_pk_add_f32 v[74:75], v[78:79], v[74:75]
	s_nop 0
	v_add_f32_e32 v6, v74, v75
	v_mbcnt_lo_u32_b32 v74, -1, 0
	v_mbcnt_hi_u32_b32 v74, -1, v74
	v_ashrrev_i32_e32 v75, 31, v74
	v_lshl_add_u64 v[74:75], v[74:75], 4, s[12:13]
	v_mbcnt_lo_u32_b32 v78, -1, 0
	v_mbcnt_hi_u32_b32 v78, -1, v78
	s_waitcnt lgkmcnt(0)
; #define GAS __attribute__((address_space(1)))
; #define FLANE lane_id()
; __device__ __forceinline__ void p6_router(Frame& F) {
;     ...
;                 for (int j = 0; j < 8; ++j) { v[j] = v[j] - mean; s2 += (v[j][0] * v[j][0] + v[j][1] * v[j][1]) + (v[j][2] * v[j][2] + v[j][3] * v[j][3]); }
;                 const float rstd = 1.f / sqrtf(wave_sum(s2) * (1.f / D) + LN_EPS);
;                 float am = 0.f;
; #pragma unroll
;                 for (int j = 0; j < 8; ++j) { const f32x4 g = *((const GAS f32x4*)F.ln1_g + FLANE + 64 * j), b = *((const GAS f32x4*)F.ln1_b + FLANE + 64 * j);
;                     v[j] = v[j] * rstd * g + b; am = fmaxf(am, fmaxf(fmaxf(fabsf(v[j][0]), fabsf(v[j][1])), fmaxf(fabsf(v[j][2]), fabsf(v[j][3])))); }
	s_nop 1
	v_add_f32_dpp v6, v6, v6 quad_perm:[1,0,3,2] row_mask:0xf bank_mask:0xf
	v_ashrrev_i32_e32 v79, 31, v78
	v_lshl_add_u64 v[78:79], v[78:79], 4, s[14:15]
	s_waitcnt lgkmcnt(0)
	s_nop 1
	v_add_f32_dpp v6, v6, v6 quad_perm:[2,3,0,1] row_mask:0xf bank_mask:0xf
	s_waitcnt lgkmcnt(0)
	s_nop 1
	v_add_f32_dpp v6, v6, v6 row_half_mirror row_mask:0xf bank_mask:0xf
	s_waitcnt lgkmcnt(0)
	s_nop 1
	v_add_f32_dpp v6, v6, v6 row_mirror row_mask:0xf bank_mask:0xf
	s_waitcnt lgkmcnt(0)
	v_mov_b32_e32 v32, v6
	s_nop 1
	v_permlane16_swap_b32_e32 v6, v32
	v_add_f32_e32 v6, v6, v32
	s_waitcnt lgkmcnt(0)
	v_mov_b32_e32 v32, v6
	s_nop 1
	v_permlane32_swap_b32_e32 v6, v32
	v_add_f32_e32 v6, v6, v32
	v_fmamk_f32 v6, v6, 0x3a000000, v166
	v_cmp_gt_f32_e32 vcc, s22, v6
	v_mul_f32_e32 v32, 0x4f800000, v6
	s_nop 0
	v_cndmask_b32_e32 v6, v6, v32, vcc
	v_sqrt_f32_e32 v32, v6
	s_nop 0
	v_add_u32_e32 v46, -1, v32
	v_fma_f32 v66, -v46, v32, v6
	v_cmp_ge_f32_e64 s[4:5], 0, v66
	v_add_u32_e32 v66, 1, v32
	s_nop 0
	v_cndmask_b32_e64 v46, v32, v46, s[4:5]
	v_fma_f32 v32, -v66, v32, v6
	v_cmp_lt_f32_e64 s[4:5], 0, v32
	s_nop 1
	v_cndmask_b32_e64 v32, v46, v66, s[4:5]
	v_mul_f32_e32 v46, 0x37800000, v32
	v_cndmask_b32_e32 v32, v32, v46, vcc
	v_cmp_class_f32_e32 vcc, v6, v167
	s_nop 1
	v_cndmask_b32_e32 v6, v32, v6, vcc
	v_div_scale_f32 v32, s[4:5], v6, v6, 1.0
	v_rcp_f32_e32 v46, v32
	s_add_i32 s4, s42, s75
	s_ashr_i32 s5, s4, 31
	v_fma_f32 v66, -v32, v46, 1.0
	v_fmac_f32_e32 v46, v66, v46
	v_div_scale_f32 v66, vcc, 1.0, v6, 1.0
	v_mul_f32_e32 v68, v66, v46
	v_fma_f32 v70, -v32, v68, v66
	v_fmac_f32_e32 v68, v70, v46
	v_fma_f32 v32, -v32, v68, v66
	v_div_fmas_f32 v32, v32, v46, v68
	v_div_fixup_f32 v32, v32, v6, 1.0
	v_pk_mul_f32 v[82:83], v[44:45], v[32:33] op_sel_hi:[1,0]
	v_pk_mul_f32 v[44:45], v[52:53], v[32:33] op_sel_hi:[1,0]
	v_mov_b32_e32 v70, v7
	v_pk_mul_f32 v[4:5], v[4:5], v[32:33] op_sel_hi:[1,0]
	v_pk_mul_f32 v[2:3], v[2:3], v[32:33] op_sel_hi:[1,0]
	v_pk_mul_f32 v[0:1], v[0:1], v[32:33] op_sel_hi:[1,0]
	v_pk_mul_f32 v[50:51], v[50:51], v[32:33] op_sel_hi:[1,0]
	s_waitcnt vmcnt(0)
	v_pk_fma_f32 v[52:53], v[196:197], v[82:83], v[228:229]
	v_mbcnt_lo_u32_b32 v74, -1, 0
	v_mbcnt_hi_u32_b32 v74, -1, v74
	v_pk_fma_f32 v[44:45], v[198:199], v[44:45], v[230:231]
	v_ashrrev_i32_e32 v75, 31, v74
	v_lshl_add_u64 v[74:75], v[74:75], 4, s[12:13]
	v_mbcnt_lo_u32_b32 v78, -1, 0
	v_mbcnt_hi_u32_b32 v78, -1, v78
	v_pk_mul_f32 v[82:83], v[54:55], v[32:33] op_sel_hi:[1,0]
	v_ashrrev_i32_e32 v79, 31, v78
	v_lshl_add_u64 v[78:79], v[78:79], 4, s[14:15]
	v_pk_mul_f32 v[54:55], v[56:57], v[32:33] op_sel_hi:[1,0]
	v_max_f32_e64 v6, |v44|, |v45|
	v_max3_f32 v6, |v52|, |v53|, v6
	s_waitcnt vmcnt(0)
	v_pk_fma_f32 v[56:57], v[200:201], v[82:83], v[232:233]
	v_mbcnt_lo_u32_b32 v74, -1, 0
	v_mbcnt_hi_u32_b32 v74, -1, v74
	v_pk_fma_f32 v[54:55], v[202:203], v[54:55], v[234:235]
	v_ashrrev_i32_e32 v75, 31, v74
	v_lshl_add_u64 v[74:75], v[74:75], 4, s[12:13]
	v_mbcnt_lo_u32_b32 v78, -1, 0
	v_mbcnt_hi_u32_b32 v78, -1, v78
	v_pk_mul_f32 v[82:83], v[58:59], v[32:33] op_sel_hi:[1,0]
	v_ashrrev_i32_e32 v79, 31, v78
	v_lshl_add_u64 v[78:79], v[78:79], 4, s[14:15]
	v_pk_mul_f32 v[58:59], v[60:61], v[32:33] op_sel_hi:[1,0]
	v_max_f32_e64 v46, |v54|, |v55|
	v_max3_f32 v46, |v56|, |v57|, v46
	v_max3_f32 v6, v6, 0, v46
	s_waitcnt vmcnt(0)
	v_pk_fma_f32 v[60:61], v[204:205], v[82:83], v[236:237]
	v_mbcnt_lo_u32_b32 v74, -1, 0
	v_mbcnt_hi_u32_b32 v74, -1, v74
	v_pk_fma_f32 v[58:59], v[206:207], v[58:59], v[238:239]
	v_ashrrev_i32_e32 v75, 31, v74
	v_lshl_add_u64 v[74:75], v[74:75], 4, s[12:13]
	v_mbcnt_lo_u32_b32 v78, -1, 0
	v_mbcnt_hi_u32_b32 v78, -1, v78
	v_pk_mul_f32 v[82:83], v[62:63], v[32:33] op_sel_hi:[1,0]
	v_ashrrev_i32_e32 v79, 31, v78
	v_lshl_add_u64 v[78:79], v[78:79], 4, s[14:15]
	v_pk_mul_f32 v[62:63], v[64:65], v[32:33] op_sel_hi:[1,0]
	v_max_f32_e64 v46, |v58|, |v59|
	v_max3_f32 v46, |v60|, |v61|, v46
	s_waitcnt vmcnt(0)
	v_pk_fma_f32 v[64:65], v[208:209], v[82:83], v[240:241]
	v_mbcnt_lo_u32_b32 v74, -1, 0
	v_mbcnt_hi_u32_b32 v74, -1, v74
	v_pk_fma_f32 v[62:63], v[210:211], v[62:63], v[242:243]
	v_ashrrev_i32_e32 v75, 31, v74
	v_lshl_add_u64 v[74:75], v[74:75], 4, s[12:13]
	v_add_co_u32_e32 v74, vcc, s23, v74
	v_max_f32_e64 v66, |v62|, |v63|
	s_nop 0
	v_addc_co_u32_e32 v75, vcc, 0, v75, vcc
	v_mbcnt_lo_u32_b32 v78, -1, 0
	v_mbcnt_hi_u32_b32 v78, -1, v78
	v_max3_f32 v66, |v64|, |v65|, v66
	v_ashrrev_i32_e32 v79, 31, v78
	v_lshl_add_u64 v[78:79], v[78:79], 4, s[14:15]
	v_add_co_u32_e32 v78, vcc, s23, v78
	v_max3_f32 v46, v6, v46, v66
	s_nop 0
	v_addc_co_u32_e32 v79, vcc, 0, v79, vcc
	v_mov_b32_e32 v66, v69
	v_pk_mul_f32 v[66:67], v[66:67], v[32:33] op_sel_hi:[1,0]
	v_pk_mul_f32 v[6:7], v[70:71], v[32:33] op_sel_hi:[1,0]
	s_waitcnt vmcnt(0)
	v_pk_fma_f32 v[66:67], v[214:215], v[66:67], v[246:247]
	v_pk_fma_f32 v[68:69], v[212:213], v[6:7], v[244:245]
	v_max_f32_e64 v6, |v66|, |v67|
	v_max3_f32 v82, |v68|, |v69|, v6
	v_mbcnt_lo_u32_b32 v6, -1, 0
	v_mbcnt_hi_u32_b32 v6, -1, v6
	s_nop 0
	v_ashrrev_i32_e32 v7, 31, v6
	v_lshl_add_u64 v[6:7], v[6:7], 4, s[12:13]
	v_add_co_u32_e32 v6, vcc, s23, v6
	s_nop 1
	v_addc_co_u32_e32 v7, vcc, 0, v7, vcc
	v_mbcnt_lo_u32_b32 v6, -1, 0
	v_mbcnt_hi_u32_b32 v6, -1, v6
	s_nop 0
	v_ashrrev_i32_e32 v7, 31, v6
	v_lshl_add_u64 v[6:7], v[6:7], 4, s[14:15]
	v_add_co_u32_e32 v6, vcc, s23, v6
	s_nop 1
	v_addc_co_u32_e32 v7, vcc, 0, v7, vcc
	v_pk_mul_f32 v[6:7], v[72:73], v[32:33] op_sel_hi:[1,0]
	s_waitcnt vmcnt(0)
; #define GAS __attribute__((address_space(1)))
; #define FLANE lane_id()
; __device__ __forceinline__ void p6_router(Frame& F) {
;     ...
;                 for (int j = 0; j < 8; ++j) { const f32x4 g = *((const GAS f32x4*)F.ln1_g + FLANE + 64 * j), b = *((const GAS f32x4*)F.ln1_b + FLANE + 64 * j);
;                     v[j] = v[j] * rstd * g + b; am = fmaxf(am, fmaxf(fmaxf(fabsf(v[j][0]), fabsf(v[j][1])), fmaxf(fabsf(v[j][2]), fabsf(v[j][3])))); }
; #pragma unroll
;                 for (int o = 1; o < 64; o <<= 1) am = fmaxf(am, __shfl_xor(am, o));
;                 const float sc = am > 0.f ? am * (1.f / 127.f) : 1.f, inv = 1.f / sc;
; #pragma unroll
;                 for (int j = 0; j < 8; ++j) { const int q0 = (int)__builtin_rintf(v[j][0] * inv), q1 = (int)__builtin_rintf(v[j][1] * inv), q2 = (int)__builtin_rintf(v[j][2] * inv), q3 = (int)__builtin_rintf(v[j][3] * inv);
;                     h1q[(size_t)m * (D / 4) + FLANE + 64 * j] = (unsigned)(q0 & 0xff) | ((unsigned)(q1 & 0xff) << 8) | ((unsigned)(q2 & 0xff) << 16) | ((unsigned)(q3 & 0xff) << 24); }
	v_pk_fma_f32 v[72:73], v[216:217], v[4:5], v[248:249]
	v_pk_fma_f32 v[70:71], v[218:219], v[6:7], v[250:251]
	s_nop 0
	v_max_f32_e64 v4, |v70|, |v71|
	v_max3_f32 v4, |v72|, |v73|, v4
	v_max3_f32 v80, v46, v82, v4
	v_mbcnt_lo_u32_b32 v4, -1, 0
	v_mbcnt_hi_u32_b32 v4, -1, v4
	v_mov_b32_e32 v46, v49
	v_ashrrev_i32_e32 v5, 31, v4
	v_lshl_add_u64 v[4:5], v[4:5], 4, s[12:13]
	v_add_co_u32_e32 v4, vcc, s23, v4
	v_pk_mul_f32 v[46:47], v[46:47], v[32:33] op_sel_hi:[1,0]
	s_nop 0
	v_addc_co_u32_e32 v5, vcc, 0, v5, vcc
	v_mbcnt_lo_u32_b32 v74, -1, 0
	v_mbcnt_hi_u32_b32 v74, -1, v74
	s_nop 0
	v_ashrrev_i32_e32 v75, 31, v74
	v_lshl_add_u64 v[74:75], v[74:75], 4, s[14:15]
	v_add_co_u32_e32 v74, vcc, s23, v74
	s_nop 1
	v_addc_co_u32_e32 v75, vcc, 0, v75, vcc
	s_waitcnt vmcnt(0)
	v_pk_fma_f32 v[74:75], v[2:3], v[222:223], v[184:185]
	v_pk_fma_f32 v[76:77], v[0:1], v[220:221], v[182:183]
	v_max_f32_e64 v0, |v74|, |v75|
	v_max3_f32 v78, |v76|, |v77|, v0
	v_mbcnt_lo_u32_b32 v0, -1, 0
	v_mbcnt_hi_u32_b32 v0, -1, v0
	s_nop 0
	v_ashrrev_i32_e32 v1, 31, v0
	v_lshl_add_u64 v[0:1], v[0:1], 4, s[12:13]
	v_add_co_u32_e32 v0, vcc, s23, v0
	s_nop 1
	v_addc_co_u32_e32 v1, vcc, 0, v1, vcc
	v_mbcnt_lo_u32_b32 v4, -1, 0
	v_mbcnt_hi_u32_b32 v4, -1, v4
	s_nop 0
	v_ashrrev_i32_e32 v5, 31, v4
	v_lshl_add_u64 v[4:5], v[4:5], 4, s[14:15]
	v_add_co_u32_e32 v4, vcc, s23, v4
	s_nop 1
	v_addc_co_u32_e32 v5, vcc, 0, v5, vcc
	s_waitcnt vmcnt(0)
	v_pk_fma_f32 v[2:3], v[46:47], v[226:227], v[188:189]
	v_pk_fma_f32 v[4:5], v[50:51], v[224:225], v[186:187]
	v_max_f32_e64 v0, |v2|, |v3|
	v_max3_f32 v0, |v4|, |v5|, v0
	v_max3_f32 v0, v80, v78, v0
	s_waitcnt lgkmcnt(0)
	s_nop 1
	v_max_f32_dpp v0, v0, v0 quad_perm:[1,0,3,2] row_mask:0xf bank_mask:0xf
	s_waitcnt lgkmcnt(0)
	s_nop 1
	v_max_f32_dpp v0, v0, v0 quad_perm:[2,3,0,1] row_mask:0xf bank_mask:0xf
	s_waitcnt lgkmcnt(0)
	s_nop 1
	v_max_f32_dpp v0, v0, v0 row_half_mirror row_mask:0xf bank_mask:0xf
	s_waitcnt lgkmcnt(0)
	s_nop 1
	v_max_f32_dpp v0, v0, v0 row_mirror row_mask:0xf bank_mask:0xf
	s_waitcnt lgkmcnt(0)
	v_mov_b32_e32 v1, v0
	s_nop 1
	v_permlane16_swap_b32_e32 v0, v1
	v_max_f32_e32 v0, v0, v1
	s_waitcnt lgkmcnt(0)
	v_mov_b32_e32 v1, v0
	s_nop 1
	v_permlane32_swap_b32_e32 v0, v1
	v_max_f32_e32 v0, v0, v1
	v_cmp_lt_f32_e32 vcc, 0, v0
	v_mul_f32_e32 v0, 0x3c010204, v0
	s_nop 0
	v_cndmask_b32_e32 v0, 1.0, v0, vcc
	v_div_scale_f32 v1, s[6:7], v0, v0, 1.0
	v_rcp_f32_e32 v6, v1
	s_lshl_b64 s[6:7], s[4:5], 11
	s_add_u32 s6, s3, s6
	s_addc_u32 s7, s24, s7
	v_fma_f32 v7, -v1, v6, 1.0
	v_fmac_f32_e32 v6, v7, v6
	v_div_scale_f32 v7, vcc, 1.0, v0, 1.0
	v_mul_f32_e32 v46, v7, v6
	v_fma_f32 v47, -v1, v46, v7
	v_fmac_f32_e32 v46, v47, v6
	v_fma_f32 v1, -v1, v46, v7
	v_div_fmas_f32 v1, v1, v6, v46
	v_div_fixup_f32 v1, v1, v0, 1.0
	v_mul_f32_e32 v7, v53, v1
	v_mul_f32_e32 v6, v52, v1
	v_rndne_f32_e32 v7, v7
	v_mul_f32_e32 v44, v44, v1
	v_mul_f32_e32 v45, v45, v1
	v_rndne_f32_e32 v6, v6
	v_cvt_i32_f32_e32 v7, v7
	v_rndne_f32_e32 v44, v44
	v_rndne_f32_e32 v45, v45
	v_cvt_i32_f32_e32 v6, v6
	v_cvt_i32_f32_sdwa v44, v44 dst_sel:WORD_1 dst_unused:UNUSED_PAD src0_sel:DWORD
	v_cvt_i32_f32_e32 v45, v45
	v_lshlrev_b32_e32 v7, 8, v7
	v_and_b32_e32 v7, 0xff00, v7
	v_and_b32_e32 v44, 0xff0000, v44
	v_perm_b32 v6, v45, v6, s1
	v_or3_b32 v44, v6, v7, v44
	v_mbcnt_lo_u32_b32 v6, -1, 0
	v_mbcnt_hi_u32_b32 v6, -1, v6
	v_mul_f32_e32 v45, v55, v1
	v_ashrrev_i32_e32 v7, 31, v6
	v_lshl_add_u64 v[6:7], v[6:7], 2, s[6:7]
	global_store_dword v[6:7], v44, off
	v_mul_f32_e32 v7, v57, v1
	v_mul_f32_e32 v6, v56, v1
	v_rndne_f32_e32 v7, v7
	v_mul_f32_e32 v44, v54, v1
	v_rndne_f32_e32 v6, v6
	v_cvt_i32_f32_e32 v7, v7
	v_rndne_f32_e32 v44, v44
	v_rndne_f32_e32 v45, v45
	v_cvt_i32_f32_e32 v6, v6
	v_cvt_i32_f32_sdwa v44, v44 dst_sel:WORD_1 dst_unused:UNUSED_PAD src0_sel:DWORD
	v_cvt_i32_f32_e32 v45, v45
	v_lshlrev_b32_e32 v7, 8, v7
	v_and_b32_e32 v7, 0xff00, v7
	v_and_b32_e32 v44, 0xff0000, v44
	v_perm_b32 v6, v45, v6, s1
	v_or3_b32 v44, v6, v7, v44
	v_mbcnt_lo_u32_b32 v6, -1, 0
	v_mbcnt_hi_u32_b32 v6, -1, v6
	v_mul_f32_e32 v45, v59, v1
	v_ashrrev_i32_e32 v7, 31, v6
	v_lshl_add_u64 v[6:7], v[6:7], 2, s[6:7]
	global_store_dword v[6:7], v44, off offset:256
	v_mul_f32_e32 v7, v61, v1
	v_mul_f32_e32 v6, v60, v1
	v_rndne_f32_e32 v7, v7
	v_mul_f32_e32 v44, v58, v1
	v_rndne_f32_e32 v6, v6
	v_cvt_i32_f32_e32 v7, v7
	v_rndne_f32_e32 v44, v44
	v_rndne_f32_e32 v45, v45
	v_cvt_i32_f32_e32 v6, v6
	v_cvt_i32_f32_sdwa v44, v44 dst_sel:WORD_1 dst_unused:UNUSED_PAD src0_sel:DWORD
	v_cvt_i32_f32_e32 v45, v45
	v_lshlrev_b32_e32 v7, 8, v7
	v_and_b32_e32 v7, 0xff00, v7
	v_and_b32_e32 v44, 0xff0000, v44
	v_perm_b32 v6, v45, v6, s1
	v_or3_b32 v44, v6, v7, v44
	v_mbcnt_lo_u32_b32 v6, -1, 0
	v_mbcnt_hi_u32_b32 v6, -1, v6
	v_mul_f32_e32 v45, v63, v1
	v_ashrrev_i32_e32 v7, 31, v6
	v_lshl_add_u64 v[6:7], v[6:7], 2, s[6:7]
	global_store_dword v[6:7], v44, off offset:512
	v_mul_f32_e32 v7, v65, v1
	v_mul_f32_e32 v6, v64, v1
	v_rndne_f32_e32 v7, v7
	v_mul_f32_e32 v44, v62, v1
	v_rndne_f32_e32 v6, v6
	v_cvt_i32_f32_e32 v7, v7
	v_rndne_f32_e32 v44, v44
	v_rndne_f32_e32 v45, v45
	v_cvt_i32_f32_e32 v6, v6
	v_cvt_i32_f32_sdwa v44, v44 dst_sel:WORD_1 dst_unused:UNUSED_PAD src0_sel:DWORD
	v_cvt_i32_f32_e32 v45, v45
	v_lshlrev_b32_e32 v7, 8, v7
	v_and_b32_e32 v7, 0xff00, v7
	v_and_b32_e32 v44, 0xff0000, v44
	v_perm_b32 v6, v45, v6, s1
	v_or3_b32 v44, v6, v7, v44
	v_mbcnt_lo_u32_b32 v6, -1, 0
	v_mbcnt_hi_u32_b32 v6, -1, v6
	v_mul_f32_e32 v45, v67, v1
	v_ashrrev_i32_e32 v7, 31, v6
	v_lshl_add_u64 v[6:7], v[6:7], 2, s[6:7]
	global_store_dword v[6:7], v44, off offset:768
	v_mul_f32_e32 v7, v69, v1
	v_mul_f32_e32 v6, v68, v1
; #define FLANE lane_id()
; __device__ __forceinline__ void p6_router(Frame& F) {
;     ...
;                 f32x4 v[8]; float s = 0.f;
; #pragma unroll
;                 for (int j = 0; j < 8; ++j) { const v2u w = raw[rr][j]; v[j] = (f32x4){bf_lo(w.x), bf_hi(w.x), bf_lo(w.y), bf_hi(w.y)}; s += (v[j][0] + v[j][1]) + (v[j][2] + v[j][3]); }
;                 const float mean = wave_sum(s) * (1.f / D); float s2 = 0.f;
;     ...
;                 for (int j = 0; j < 8; ++j) { const int q0 = (int)__builtin_rintf(v[j][0] * inv), q1 = (int)__builtin_rintf(v[j][1] * inv), q2 = (int)__builtin_rintf(v[j][2] * inv), q3 = (int)__builtin_rintf(v[j][3] * inv);
;                     h1q[(size_t)m * (D / 4) + FLANE + 64 * j] = (unsigned)(q0 & 0xff) | ((unsigned)(q1 & 0xff) << 8) | ((unsigned)(q2 & 0xff) << 16) | ((unsigned)(q3 & 0xff) << 24); }
;                 if (FLANE == 0) { st1[2 * m] = mean; st1[2 * m + 1] = rstd; stl[2 * row] = mean; stl[2 * row + 1] = rstd; sxg[m] = sc; sxl[row] = sc; }
	v_rndne_f32_e32 v7, v7
	v_mul_f32_e32 v44, v66, v1
	v_rndne_f32_e32 v6, v6
	v_cvt_i32_f32_e32 v7, v7
	v_rndne_f32_e32 v44, v44
	v_rndne_f32_e32 v45, v45
	v_cvt_i32_f32_e32 v6, v6
	v_cvt_i32_f32_sdwa v44, v44 dst_sel:WORD_1 dst_unused:UNUSED_PAD src0_sel:DWORD
	v_cvt_i32_f32_e32 v45, v45
	v_lshlrev_b32_e32 v7, 8, v7
	v_and_b32_e32 v7, 0xff00, v7
	v_and_b32_e32 v44, 0xff0000, v44
	v_perm_b32 v6, v45, v6, s1
	v_or3_b32 v44, v6, v7, v44
	v_mbcnt_lo_u32_b32 v6, -1, 0
	v_mbcnt_hi_u32_b32 v6, -1, v6
	v_mul_f32_e32 v45, v71, v1
	v_ashrrev_i32_e32 v7, 31, v6
	v_lshl_add_u64 v[6:7], v[6:7], 2, s[6:7]
	global_store_dword v[6:7], v44, off offset:1024
	v_mul_f32_e32 v7, v73, v1
	v_mul_f32_e32 v6, v72, v1
	v_rndne_f32_e32 v7, v7
	v_mul_f32_e32 v44, v70, v1
	v_rndne_f32_e32 v6, v6
	v_cvt_i32_f32_e32 v7, v7
	v_rndne_f32_e32 v44, v44
	v_rndne_f32_e32 v45, v45
	v_cvt_i32_f32_e32 v6, v6
	v_cvt_i32_f32_sdwa v44, v44 dst_sel:WORD_1 dst_unused:UNUSED_PAD src0_sel:DWORD
	v_cvt_i32_f32_e32 v45, v45
	v_lshlrev_b32_e32 v7, 8, v7
	v_and_b32_e32 v7, 0xff00, v7
	v_and_b32_e32 v44, 0xff0000, v44
	v_perm_b32 v6, v45, v6, s1
	v_or3_b32 v44, v6, v7, v44
	v_mbcnt_lo_u32_b32 v6, -1, 0
	v_mbcnt_hi_u32_b32 v6, -1, v6
	v_mul_f32_e32 v45, v75, v1
	v_ashrrev_i32_e32 v7, 31, v6
	v_lshl_add_u64 v[6:7], v[6:7], 2, s[6:7]
	global_store_dword v[6:7], v44, off offset:1280
	v_mul_f32_e32 v7, v77, v1
	v_mul_f32_e32 v6, v76, v1
	v_rndne_f32_e32 v7, v7
	v_mul_f32_e32 v44, v74, v1
	v_rndne_f32_e32 v6, v6
	v_cvt_i32_f32_e32 v7, v7
	v_rndne_f32_e32 v44, v44
	v_rndne_f32_e32 v45, v45
	v_mul_f32_e32 v5, v5, v1
	v_cvt_i32_f32_e32 v6, v6
	v_cvt_i32_f32_sdwa v44, v44 dst_sel:WORD_1 dst_unused:UNUSED_PAD src0_sel:DWORD
	v_cvt_i32_f32_e32 v45, v45
	v_mul_f32_e32 v4, v4, v1
	v_rndne_f32_e32 v5, v5
	v_mul_f32_e32 v2, v2, v1
	v_mul_f32_e32 v1, v3, v1
	v_rndne_f32_e32 v4, v4
	v_cvt_i32_f32_e32 v5, v5
	v_rndne_f32_e32 v2, v2
	v_rndne_f32_e32 v1, v1
	v_cvt_i32_f32_e32 v4, v4
	v_cvt_i32_f32_sdwa v2, v2 dst_sel:WORD_1 dst_unused:UNUSED_PAD src0_sel:DWORD
	v_cvt_i32_f32_e32 v1, v1
	v_lshlrev_b32_e32 v7, 8, v7
	v_and_b32_e32 v7, 0xff00, v7
	v_and_b32_e32 v44, 0xff0000, v44
	v_perm_b32 v6, v45, v6, s1
	v_or3_b32 v44, v6, v7, v44
	v_mbcnt_lo_u32_b32 v6, -1, 0
	v_mbcnt_hi_u32_b32 v6, -1, v6
	v_lshlrev_b32_e32 v3, 8, v5
	v_ashrrev_i32_e32 v7, 31, v6
	v_lshl_add_u64 v[6:7], v[6:7], 2, s[6:7]
	v_and_b32_e32 v3, 0xff00, v3
	v_and_b32_e32 v2, 0xff0000, v2
	v_perm_b32 v1, v1, v4, s1
	global_store_dword v[6:7], v44, off offset:1536
	v_or3_b32 v1, v1, v3, v2
	v_mbcnt_lo_u32_b32 v2, -1, 0
	v_mbcnt_hi_u32_b32 v2, -1, v2
	s_nop 0
	v_ashrrev_i32_e32 v3, 31, v2
	v_lshl_add_u64 v[2:3], v[2:3], 2, s[6:7]
	global_store_dword v[2:3], v1, off offset:1792
	v_mbcnt_lo_u32_b32 v1, -1, 0
	v_mbcnt_hi_u32_b32 v1, -1, v1
	s_nop 0
	v_cmp_eq_u32_e32 vcc, 0, v1
	s_and_saveexec_b64 s[6:7], vcc
	s_cbranch_execz .LBB0_1493
	s_lshl_b32 s8, s4, 1
	s_ashr_i32 s9, s8, 31
	s_lshl_b64 s[8:9], s[8:9], 2
	s_add_u32 s8, s27, s8
	s_addc_u32 s9, s64, s9
	v_readlane_b32 s0, v255, 46
	s_lshl_b64 s[4:5], s[4:5], 2
	v_mul_f32_e32 v2, 0x3a000000, v48
	v_mov_b32_e32 v3, v32
	v_mov_b32_e32 v1, s0
	s_add_u32 s4, s25, s4
	v_readlane_b32 s0, v255, 34
	ds_write_b64 v1, v[2:3]
	s_addc_u32 s5, s26, s5
	v_mov_b32_e32 v1, s0
	global_store_dwordx2 v33, v[2:3], s[8:9]
	global_store_dword v33, v0, s[4:5]
	ds_write_b32 v1, v0
.LBB0_1493:
	s_or_b64 exec, exec, s[6:7]
	v_lshlrev_b32_e32 v47, 16, v42
	v_lshlrev_b32_e32 v46, 16, v40
	v_and_b32_e32 v59, 0xffff0000, v42
	v_and_b32_e32 v58, 0xffff0000, v40
	v_lshlrev_b32_e32 v61, 16, v43
	v_lshlrev_b32_e32 v60, 16, v41
	v_and_b32_e32 v63, 0xffff0000, v43
	v_and_b32_e32 v62, 0xffff0000, v41
	v_pk_add_f32 v[0:1], v[46:47], v[58:59]
	v_pk_add_f32 v[2:3], v[60:61], v[62:63]
	v_lshlrev_b32_e32 v45, 16, v39
	v_pk_add_f32 v[0:1], v[0:1], v[2:3]
	v_lshlrev_b32_e32 v44, 16, v38
	v_add_f32_e32 v0, 0, v0
	v_and_b32_e32 v65, 0xffff0000, v39
	v_and_b32_e32 v64, 0xffff0000, v38
	v_add_f32_e32 v6, v0, v1
	v_pk_add_f32 v[0:1], v[44:45], v[64:65]
	v_lshlrev_b32_e32 v48, 16, v36
	v_and_b32_e32 v49, 0xffff0000, v36
	v_lshlrev_b32_e32 v50, 16, v37
	v_and_b32_e32 v51, 0xffff0000, v37
	v_and_b32_e32 v57, 0xffff0000, v30
	v_pk_add_f32 v[0:1], v[0:1], v[0:1] op_sel:[0,1] op_sel_hi:[1,0]
	v_add_f32_e32 v54, v48, v49
	v_add_f32_e32 v52, v50, v51
	v_lshlrev_b32_e32 v7, 16, v30
	v_lshlrev_b32_e32 v55, 16, v31
	v_and_b32_e32 v53, 0xffff0000, v31
	v_mov_b32_e32 v1, v57
	v_pk_add_f32 v[0:1], v[6:7], v[0:1]
	v_pk_add_f32 v[2:3], v[54:55], v[52:53]
	v_lshlrev_b32_e32 v5, 16, v29
	v_lshlrev_b32_e32 v4, 16, v28
	v_and_b32_e32 v67, 0xffff0000, v29
	v_and_b32_e32 v66, 0xffff0000, v28
	v_pk_add_f32 v[36:37], v[0:1], v[2:3]
	v_pk_add_f32 v[38:39], v[4:5], v[66:67]
	v_lshlrev_b32_e32 v0, 16, v26
	v_and_b32_e32 v1, 0xffff0000, v26
	v_lshlrev_b32_e32 v2, 16, v27
	v_and_b32_e32 v3, 0xffff0000, v27
	v_lshlrev_b32_e32 v30, 16, v24
	v_and_b32_e32 v31, 0xffff0000, v24
	v_lshlrev_b32_e32 v29, 16, v25
	v_and_b32_e32 v27, 0xffff0000, v25
	v_pk_add_f32 v[24:25], v[36:37], v[36:37] op_sel:[0,1] op_sel_hi:[1,0]
	v_pk_add_f32 v[36:37], v[38:39], v[38:39] op_sel:[0,1] op_sel_hi:[1,0]
	v_add_f32_e32 v28, v0, v1
	v_add_f32_e32 v26, v2, v3
	v_mov_b32_e32 v25, v30
	v_mov_b32_e32 v37, v31
	v_pk_add_f32 v[24:25], v[24:25], v[36:37]
	v_pk_add_f32 v[36:37], v[28:29], v[26:27]
	s_nop 0
	v_pk_add_f32 v[24:25], v[24:25], v[36:37]
	s_nop 0
	v_add_f32_e32 v6, v24, v25
	s_waitcnt lgkmcnt(0)
	s_nop 1
	v_add_f32_dpp v6, v6, v6 quad_perm:[1,0,3,2] row_mask:0xf bank_mask:0xf
	s_waitcnt lgkmcnt(0)
	s_nop 1
	v_add_f32_dpp v6, v6, v6 quad_perm:[2,3,0,1] row_mask:0xf bank_mask:0xf
	s_waitcnt lgkmcnt(0)
; __device__ __forceinline__ void p6_router(Frame& F) {
;     ...
;                 const float mean = wave_sum(s) * (1.f / D); float s2 = 0.f;
; #pragma unroll
;                 for (int j = 0; j < 8; ++j) { v[j] = v[j] - mean; s2 += (v[j][0] * v[j][0] + v[j][1] * v[j][1]) + (v[j][2] * v[j][2] + v[j][3] * v[j][3]); }
;                 const float rstd = 1.f / sqrtf(wave_sum(s2) * (1.f / D) + LN_EPS);
	s_nop 1
	v_add_f32_dpp v6, v6, v6 row_half_mirror row_mask:0xf bank_mask:0xf
	s_waitcnt lgkmcnt(0)
	s_nop 1
	v_add_f32_dpp v6, v6, v6 row_mirror row_mask:0xf bank_mask:0xf
	s_waitcnt lgkmcnt(0)
	v_mov_b32_e32 v24, v6
	s_nop 1
	v_permlane16_swap_b32_e32 v6, v24
	v_add_f32_e32 v6, v6, v24
	s_waitcnt lgkmcnt(0)
	v_mov_b32_e32 v24, v6
	s_nop 1
	v_permlane32_swap_b32_e32 v6, v24
	v_add_f32_e32 v25, v6, v24
	v_fmac_f32_e32 v62, 0xba000000, v25
	v_fmac_f32_e32 v58, 0xba000000, v25
	v_fmac_f32_e32 v63, 0xba000000, v25
	v_fmac_f32_e32 v59, 0xba000000, v25
	v_fmac_f32_e32 v60, 0xba000000, v25
	v_fmac_f32_e32 v46, 0xba000000, v25
	v_fmac_f32_e32 v61, 0xba000000, v25
	v_fmac_f32_e32 v47, 0xba000000, v25
	v_mov_b32_e32 v41, v59
	v_mov_b32_e32 v37, v58
	v_pk_mul_f32 v[38:39], v[58:59], v[58:59]
	v_pk_mul_f32 v[58:59], v[62:63], v[62:63]
	v_mov_b32_e32 v40, v47
	v_mov_b32_e32 v36, v46
	v_pk_fma_f32 v[46:47], v[46:47], v[46:47], v[38:39]
	v_pk_fma_f32 v[58:59], v[60:61], v[60:61], v[58:59]
	v_fmac_f32_e32 v64, 0xba000000, v25
	v_pk_add_f32 v[46:47], v[46:47], v[58:59]
	v_fmac_f32_e32 v65, 0xba000000, v25
	v_fmac_f32_e32 v45, 0xba000000, v25
	v_pk_add_f32 v[58:59], v[46:47], v[46:47] op_sel_hi:[0,1]
	v_fmac_f32_e32 v44, 0xba000000, v25
	v_mov_b32_e32 v46, v45
	v_mov_b32_e32 v47, v65
	v_mov_b32_e32 v45, v64
	v_mov_b32_e32 v42, v61
	v_mov_b32_e32 v43, v63
	v_mov_b32_e32 v38, v60
	v_mov_b32_e32 v39, v62
	v_pk_mul_f32 v[60:61], v[46:47], v[46:47]
	v_pk_mul_f32 v[62:63], v[44:45], v[44:45]
	v_fmac_f32_e32 v48, 0xba000000, v25
	v_pk_mov_b32 v[64:65], v[62:63], v[60:61] op_sel:[1,0]
	v_mov_b32_e32 v63, v61
	v_fmac_f32_e32 v49, 0xba000000, v25
	v_fmac_f32_e32 v50, 0xba000000, v25
	v_mul_f32_e32 v6, v48, v48
	v_pk_add_f32 v[60:61], v[64:65], v[62:63]
	v_fmac_f32_e32 v51, 0xba000000, v25
	v_pk_fma_f32 v[62:63], v[48:49], v[48:49], v[6:7] op_sel_hi:[1,1,0]
	v_mul_f32_e32 v6, v50, v50
	v_pk_add_f32 v[60:61], v[60:61], v[60:61] op_sel_hi:[0,1]
	v_pk_fma_f32 v[64:65], v[50:51], v[50:51], v[6:7] op_sel_hi:[1,1,0]
	v_fmac_f32_e32 v53, 0xba000000, v25
	v_fmac_f32_e32 v55, 0xba000000, v25
	v_fmac_f32_e32 v57, 0xba000000, v25
	v_fmac_f32_e32 v7, 0xba000000, v25
	v_mul_f32_e32 v62, v7, v7
	v_mul_f32_e32 v64, v57, v57
	v_mul_f32_e32 v60, v55, v55
	v_mul_f32_e32 v58, v53, v53
	v_pk_add_f32 v[62:63], v[62:63], v[64:65]
	v_pk_add_f32 v[58:59], v[60:61], v[58:59]
	v_fmac_f32_e32 v66, 0xba000000, v25
	v_pk_add_f32 v[58:59], v[62:63], v[58:59]
	v_fmac_f32_e32 v67, 0xba000000, v25
	v_fmac_f32_e32 v5, 0xba000000, v25
	v_pk_add_f32 v[60:61], v[58:59], v[58:59] op_sel_hi:[0,1]
	v_fmac_f32_e32 v4, 0xba000000, v25
	v_mov_b32_e32 v58, v5
	v_mov_b32_e32 v59, v67
	v_mov_b32_e32 v5, v66
	v_pk_mul_f32 v[62:63], v[58:59], v[58:59]
	v_pk_mul_f32 v[64:65], v[4:5], v[4:5]
	v_fmac_f32_e32 v0, 0xba000000, v25
	v_pk_mov_b32 v[66:67], v[64:65], v[62:63] op_sel:[1,0]
	v_mov_b32_e32 v65, v63
	v_fmac_f32_e32 v1, 0xba000000, v25
	v_fmac_f32_e32 v2, 0xba000000, v25
	v_mul_f32_e32 v6, v0, v0
	v_pk_add_f32 v[62:63], v[66:67], v[64:65]
	v_fmac_f32_e32 v3, 0xba000000, v25
	v_pk_fma_f32 v[64:65], v[0:1], v[0:1], v[6:7] op_sel_hi:[1,1,0]
	v_mul_f32_e32 v6, v2, v2
	v_pk_add_f32 v[62:63], v[62:63], v[62:63] op_sel_hi:[0,1]
	v_pk_fma_f32 v[66:67], v[2:3], v[2:3], v[6:7] op_sel_hi:[1,1,0]
	v_fmac_f32_e32 v27, 0xba000000, v25
	v_fmac_f32_e32 v29, 0xba000000, v25
	v_fmac_f32_e32 v31, 0xba000000, v25
	v_fmac_f32_e32 v30, 0xba000000, v25
	v_mul_f32_e32 v64, v30, v30
	v_mul_f32_e32 v66, v31, v31
	v_mul_f32_e32 v62, v29, v29
	v_mul_f32_e32 v60, v27, v27
	v_pk_add_f32 v[64:65], v[64:65], v[66:67]
	v_pk_add_f32 v[60:61], v[62:63], v[60:61]
	v_mov_b32_e32 v56, v7
	v_pk_add_f32 v[60:61], v[64:65], v[60:61]
	s_nop 0
	v_add_f32_e32 v6, v60, v61
	v_mbcnt_lo_u32_b32 v60, -1, 0
	v_mbcnt_hi_u32_b32 v60, -1, v60
	v_ashrrev_i32_e32 v61, 31, v60
	v_lshl_add_u64 v[60:61], v[60:61], 4, s[12:13]
	v_mbcnt_lo_u32_b32 v64, -1, 0
	v_mbcnt_hi_u32_b32 v64, -1, v64
	s_waitcnt lgkmcnt(0)
	s_nop 1
	v_add_f32_dpp v6, v6, v6 quad_perm:[1,0,3,2] row_mask:0xf bank_mask:0xf
	v_ashrrev_i32_e32 v65, 31, v64
	v_lshl_add_u64 v[64:65], v[64:65], 4, s[14:15]
	s_waitcnt lgkmcnt(0)
	s_nop 1
	v_add_f32_dpp v6, v6, v6 quad_perm:[2,3,0,1] row_mask:0xf bank_mask:0xf
	s_waitcnt lgkmcnt(0)
	s_nop 1
	v_add_f32_dpp v6, v6, v6 row_half_mirror row_mask:0xf bank_mask:0xf
	s_waitcnt lgkmcnt(0)
	s_nop 1
	v_add_f32_dpp v6, v6, v6 row_mirror row_mask:0xf bank_mask:0xf
	s_waitcnt lgkmcnt(0)
	v_mov_b32_e32 v24, v6
	s_nop 1
	v_permlane16_swap_b32_e32 v6, v24
	v_add_f32_e32 v6, v6, v24
	s_waitcnt lgkmcnt(0)
	v_mov_b32_e32 v24, v6
	s_nop 1
	v_permlane32_swap_b32_e32 v6, v24
	v_add_f32_e32 v6, v6, v24
	v_fmamk_f32 v6, v6, 0x3a000000, v166
	v_cmp_gt_f32_e32 vcc, s22, v6
	v_mul_f32_e32 v24, 0x4f800000, v6
	s_nop 0
	v_cndmask_b32_e32 v6, v6, v24, vcc
	v_sqrt_f32_e32 v24, v6
	s_nop 0
	v_add_u32_e32 v26, -1, v24
	v_fma_f32 v28, -v26, v24, v6
	v_cmp_ge_f32_e64 s[4:5], 0, v28
	v_add_u32_e32 v28, 1, v24
	s_nop 0
	v_cndmask_b32_e64 v26, v24, v26, s[4:5]
	v_fma_f32 v24, -v28, v24, v6
	v_cmp_lt_f32_e64 s[4:5], 0, v24
	s_nop 1
	v_cndmask_b32_e64 v24, v26, v28, s[4:5]
	v_mul_f32_e32 v26, 0x37800000, v24
	v_cndmask_b32_e32 v24, v24, v26, vcc
	v_cmp_class_f32_e32 vcc, v6, v167
	s_nop 1
	v_cndmask_b32_e32 v6, v24, v6, vcc
	v_div_scale_f32 v24, s[4:5], v6, v6, 1.0
	v_rcp_f32_e32 v26, v24
	s_add_i32 s4, s42, s77
	s_ashr_i32 s5, s4, 31
	v_fma_f32 v28, -v24, v26, 1.0
	v_fmac_f32_e32 v26, v28, v26
	v_div_scale_f32 v28, vcc, 1.0, v6, 1.0
	v_mul_f32_e32 v32, v28, v26
	v_fma_f32 v52, -v24, v32, v28
	v_fmac_f32_e32 v32, v52, v26
	v_fma_f32 v24, -v24, v32, v28
	v_div_fmas_f32 v24, v24, v26, v32
	v_div_fixup_f32 v24, v24, v6, 1.0
	v_pk_mul_f32 v[68:69], v[36:37], v[24:25] op_sel_hi:[1,0]
	v_pk_mul_f32 v[36:37], v[38:39], v[24:25] op_sel_hi:[1,0]
	v_mov_b32_e32 v52, v55
	v_pk_mul_f32 v[52:53], v[52:53], v[24:25] op_sel_hi:[1,0]
	v_pk_mul_f32 v[4:5], v[4:5], v[24:25] op_sel_hi:[1,0]
	v_pk_mul_f32 v[2:3], v[2:3], v[24:25] op_sel_hi:[1,0]
	v_pk_mul_f32 v[0:1], v[0:1], v[24:25] op_sel_hi:[1,0]
	s_waitcnt vmcnt(0)
; #define GAS __attribute__((address_space(1)))
; #define FLANE lane_id()
; __device__ __forceinline__ void p6_router(Frame& F) {
;     ...
;                 for (int j = 0; j < 8; ++j) { const f32x4 g = *((const GAS f32x4*)F.ln1_g + FLANE + 64 * j), b = *((const GAS f32x4*)F.ln1_b + FLANE + 64 * j);
;                     v[j] = v[j] * rstd * g + b; am = fmaxf(am, fmaxf(fmaxf(fabsf(v[j][0]), fabsf(v[j][1])), fmaxf(fabsf(v[j][2]), fabsf(v[j][3])))); }
	v_pk_fma_f32 v[38:39], v[196:197], v[68:69], v[228:229]
	v_mbcnt_lo_u32_b32 v60, -1, 0
	v_mbcnt_hi_u32_b32 v60, -1, v60
	v_pk_fma_f32 v[36:37], v[198:199], v[36:37], v[230:231]
	v_ashrrev_i32_e32 v61, 31, v60
	v_lshl_add_u64 v[60:61], v[60:61], 4, s[12:13]
	v_mbcnt_lo_u32_b32 v64, -1, 0
	v_mbcnt_hi_u32_b32 v64, -1, v64
	v_pk_mul_f32 v[68:69], v[40:41], v[24:25] op_sel_hi:[1,0]
	v_ashrrev_i32_e32 v65, 31, v64
	v_lshl_add_u64 v[64:65], v[64:65], 4, s[14:15]
	v_pk_mul_f32 v[40:41], v[42:43], v[24:25] op_sel_hi:[1,0]
	v_max_f32_e64 v6, |v36|, |v37|
	v_max3_f32 v6, |v38|, |v39|, v6
	v_pk_mul_f32 v[30:31], v[30:31], v[24:25] op_sel_hi:[1,0]
	s_waitcnt vmcnt(0)
	v_pk_fma_f32 v[42:43], v[200:201], v[68:69], v[232:233]
	v_mbcnt_lo_u32_b32 v60, -1, 0
	v_mbcnt_hi_u32_b32 v60, -1, v60
	v_pk_fma_f32 v[40:41], v[202:203], v[40:41], v[234:235]
	v_ashrrev_i32_e32 v61, 31, v60
	v_lshl_add_u64 v[60:61], v[60:61], 4, s[12:13]
	v_mbcnt_lo_u32_b32 v64, -1, 0
	v_mbcnt_hi_u32_b32 v64, -1, v64
	v_pk_mul_f32 v[68:69], v[44:45], v[24:25] op_sel_hi:[1,0]
	v_ashrrev_i32_e32 v65, 31, v64
	v_lshl_add_u64 v[64:65], v[64:65], 4, s[14:15]
	v_pk_mul_f32 v[44:45], v[46:47], v[24:25] op_sel_hi:[1,0]
	v_max_f32_e64 v26, |v40|, |v41|
	v_max3_f32 v26, |v42|, |v43|, v26
	v_max3_f32 v6, v6, 0, v26
	s_waitcnt vmcnt(0)
	v_pk_fma_f32 v[46:47], v[204:205], v[68:69], v[236:237]
	v_mbcnt_lo_u32_b32 v60, -1, 0
	v_mbcnt_hi_u32_b32 v60, -1, v60
	v_pk_fma_f32 v[44:45], v[206:207], v[44:45], v[238:239]
	v_ashrrev_i32_e32 v61, 31, v60
	v_lshl_add_u64 v[60:61], v[60:61], 4, s[12:13]
	v_mbcnt_lo_u32_b32 v64, -1, 0
	v_mbcnt_hi_u32_b32 v64, -1, v64
	v_pk_mul_f32 v[68:69], v[48:49], v[24:25] op_sel_hi:[1,0]
	v_ashrrev_i32_e32 v65, 31, v64
	v_lshl_add_u64 v[64:65], v[64:65], 4, s[14:15]
	v_pk_mul_f32 v[48:49], v[50:51], v[24:25] op_sel_hi:[1,0]
	v_max_f32_e64 v26, |v44|, |v45|
	v_max3_f32 v26, |v46|, |v47|, v26
	s_waitcnt vmcnt(0)
	v_pk_fma_f32 v[50:51], v[208:209], v[68:69], v[240:241]
	v_mbcnt_lo_u32_b32 v60, -1, 0
	v_mbcnt_hi_u32_b32 v60, -1, v60
	v_pk_fma_f32 v[48:49], v[210:211], v[48:49], v[242:243]
	v_ashrrev_i32_e32 v61, 31, v60
	v_lshl_add_u64 v[60:61], v[60:61], 4, s[12:13]
	v_add_co_u32_e32 v60, vcc, s23, v60
	v_max_f32_e64 v28, |v48|, |v49|
	s_nop 0
	v_addc_co_u32_e32 v61, vcc, 0, v61, vcc
	v_mbcnt_lo_u32_b32 v64, -1, 0
	v_mbcnt_hi_u32_b32 v64, -1, v64
	v_max3_f32 v28, |v50|, |v51|, v28
	v_ashrrev_i32_e32 v65, 31, v64
	v_lshl_add_u64 v[64:65], v[64:65], 4, s[14:15]
	v_add_co_u32_e32 v64, vcc, s23, v64
	v_max3_f32 v26, v6, v26, v28
	s_nop 0
	v_addc_co_u32_e32 v65, vcc, 0, v65, vcc
	v_pk_mul_f32 v[6:7], v[56:57], v[24:25] op_sel_hi:[1,0]
	s_waitcnt vmcnt(0)
	v_pk_fma_f32 v[52:53], v[214:215], v[52:53], v[246:247]
	v_pk_fma_f32 v[54:55], v[212:213], v[6:7], v[244:245]
	v_max_f32_e64 v6, |v52|, |v53|
	v_max3_f32 v28, |v54|, |v55|, v6
	v_mbcnt_lo_u32_b32 v6, -1, 0
	v_mbcnt_hi_u32_b32 v6, -1, v6
	s_nop 0
	v_ashrrev_i32_e32 v7, 31, v6
	v_lshl_add_u64 v[6:7], v[6:7], 4, s[12:13]
	v_add_co_u32_e32 v6, vcc, s23, v6
	s_nop 1
	v_addc_co_u32_e32 v7, vcc, 0, v7, vcc
	v_mbcnt_lo_u32_b32 v6, -1, 0
	v_mbcnt_hi_u32_b32 v6, -1, v6
	s_nop 0
	v_ashrrev_i32_e32 v7, 31, v6
	v_lshl_add_u64 v[6:7], v[6:7], 4, s[14:15]
	v_add_co_u32_e32 v6, vcc, s23, v6
	s_nop 1
	v_addc_co_u32_e32 v7, vcc, 0, v7, vcc
	v_pk_mul_f32 v[6:7], v[58:59], v[24:25] op_sel_hi:[1,0]
	s_waitcnt vmcnt(0)
	v_pk_fma_f32 v[58:59], v[216:217], v[4:5], v[248:249]
	v_pk_fma_f32 v[56:57], v[218:219], v[6:7], v[250:251]
	s_nop 0
	v_max_f32_e64 v4, |v56|, |v57|
	v_max3_f32 v4, |v58|, |v59|, v4
	v_max3_f32 v28, v26, v28, v4
	v_mbcnt_lo_u32_b32 v4, -1, 0
	v_mbcnt_hi_u32_b32 v4, -1, v4
	v_mov_b32_e32 v26, v29
	v_ashrrev_i32_e32 v5, 31, v4
	v_lshl_add_u64 v[4:5], v[4:5], 4, s[12:13]
	v_add_co_u32_e32 v4, vcc, s23, v4
	v_pk_mul_f32 v[26:27], v[26:27], v[24:25] op_sel_hi:[1,0]
	s_nop 0
	v_addc_co_u32_e32 v5, vcc, 0, v5, vcc
	v_mbcnt_lo_u32_b32 v60, -1, 0
	v_mbcnt_hi_u32_b32 v60, -1, v60
	s_nop 0
	v_ashrrev_i32_e32 v61, 31, v60
	v_lshl_add_u64 v[60:61], v[60:61], 4, s[14:15]
	v_add_co_u32_e32 v60, vcc, s23, v60
	s_nop 1
	v_addc_co_u32_e32 v61, vcc, 0, v61, vcc
	s_waitcnt vmcnt(0)
	v_pk_fma_f32 v[60:61], v[2:3], v[222:223], v[184:185]
	v_pk_fma_f32 v[62:63], v[0:1], v[220:221], v[182:183]
	v_max_f32_e64 v0, |v60|, |v61|
	v_max3_f32 v32, |v62|, |v63|, v0
	v_mbcnt_lo_u32_b32 v0, -1, 0
	v_mbcnt_hi_u32_b32 v0, -1, v0
	s_nop 0
	v_ashrrev_i32_e32 v1, 31, v0
	v_lshl_add_u64 v[0:1], v[0:1], 4, s[12:13]
	v_add_co_u32_e32 v0, vcc, s23, v0
	s_nop 1
	v_addc_co_u32_e32 v1, vcc, 0, v1, vcc
	v_mbcnt_lo_u32_b32 v4, -1, 0
	v_mbcnt_hi_u32_b32 v4, -1, v4
	s_nop 0
	v_ashrrev_i32_e32 v5, 31, v4
	v_lshl_add_u64 v[4:5], v[4:5], 4, s[14:15]
	v_add_co_u32_e32 v4, vcc, s23, v4
	s_nop 1
	v_addc_co_u32_e32 v5, vcc, 0, v5, vcc
	s_waitcnt vmcnt(0)
	v_pk_fma_f32 v[2:3], v[26:27], v[226:227], v[188:189]
	v_pk_fma_f32 v[4:5], v[30:31], v[224:225], v[186:187]
	v_max_f32_e64 v0, |v2|, |v3|
	v_max3_f32 v0, |v4|, |v5|, v0
	v_max3_f32 v0, v28, v32, v0
	s_waitcnt lgkmcnt(0)
	s_nop 1
	v_max_f32_dpp v0, v0, v0 quad_perm:[1,0,3,2] row_mask:0xf bank_mask:0xf
	s_waitcnt lgkmcnt(0)
	s_nop 1
	v_max_f32_dpp v0, v0, v0 quad_perm:[2,3,0,1] row_mask:0xf bank_mask:0xf
	s_waitcnt lgkmcnt(0)
	s_nop 1
	v_max_f32_dpp v0, v0, v0 row_half_mirror row_mask:0xf bank_mask:0xf
	s_waitcnt lgkmcnt(0)
	s_nop 1
	v_max_f32_dpp v0, v0, v0 row_mirror row_mask:0xf bank_mask:0xf
	s_waitcnt lgkmcnt(0)
	v_mov_b32_e32 v1, v0
	s_nop 1
	v_permlane16_swap_b32_e32 v0, v1
	v_max_f32_e32 v0, v0, v1
	s_waitcnt lgkmcnt(0)
; #define FLANE lane_id()
; __device__ __forceinline__ void p6_router(Frame& F) {
;     ...
; #pragma unroll
;                 for (int o = 1; o < 64; o <<= 1) am = fmaxf(am, __shfl_xor(am, o));
;                 const float sc = am > 0.f ? am * (1.f / 127.f) : 1.f, inv = 1.f / sc;
; #pragma unroll
;                 for (int j = 0; j < 8; ++j) { const int q0 = (int)__builtin_rintf(v[j][0] * inv), q1 = (int)__builtin_rintf(v[j][1] * inv), q2 = (int)__builtin_rintf(v[j][2] * inv), q3 = (int)__builtin_rintf(v[j][3] * inv);
;                     h1q[(size_t)m * (D / 4) + FLANE + 64 * j] = (unsigned)(q0 & 0xff) | ((unsigned)(q1 & 0xff) << 8) | ((unsigned)(q2 & 0xff) << 16) | ((unsigned)(q3 & 0xff) << 24); }
;                 if (FLANE == 0) { st1[2 * m] = mean; st1[2 * m + 1] = rstd; stl[2 * row] = mean; stl[2 * row + 1] = rstd; sxg[m] = sc; sxl[row] = sc; }
	v_mov_b32_e32 v1, v0
	s_nop 1
	v_permlane32_swap_b32_e32 v0, v1
	v_max_f32_e32 v0, v0, v1
	v_cmp_lt_f32_e32 vcc, 0, v0
	v_mul_f32_e32 v0, 0x3c010204, v0
	s_nop 0
	v_cndmask_b32_e32 v0, 1.0, v0, vcc
	v_div_scale_f32 v1, s[6:7], v0, v0, 1.0
	v_rcp_f32_e32 v6, v1
	s_lshl_b64 s[6:7], s[4:5], 11
	s_add_u32 s6, s3, s6
	s_addc_u32 s7, s24, s7
	v_fma_f32 v7, -v1, v6, 1.0
	v_fmac_f32_e32 v6, v7, v6
	v_div_scale_f32 v7, vcc, 1.0, v0, 1.0
	v_mul_f32_e32 v26, v7, v6
	v_fma_f32 v27, -v1, v26, v7
	v_fmac_f32_e32 v26, v27, v6
	v_fma_f32 v1, -v1, v26, v7
	v_div_fmas_f32 v1, v1, v6, v26
	v_div_fixup_f32 v1, v1, v0, 1.0
	v_mul_f32_e32 v7, v39, v1
	v_mul_f32_e32 v6, v38, v1
	v_rndne_f32_e32 v7, v7
	v_mul_f32_e32 v26, v36, v1
	v_mul_f32_e32 v27, v37, v1
	v_rndne_f32_e32 v6, v6
	v_cvt_i32_f32_e32 v7, v7
	v_rndne_f32_e32 v26, v26
	v_rndne_f32_e32 v27, v27
	v_cvt_i32_f32_e32 v6, v6
	v_cvt_i32_f32_sdwa v26, v26 dst_sel:WORD_1 dst_unused:UNUSED_PAD src0_sel:DWORD
	v_cvt_i32_f32_e32 v27, v27
	v_lshlrev_b32_e32 v7, 8, v7
	v_and_b32_e32 v7, 0xff00, v7
	v_and_b32_e32 v26, 0xff0000, v26
	v_perm_b32 v6, v27, v6, s1
	v_or3_b32 v26, v6, v7, v26
	v_mbcnt_lo_u32_b32 v6, -1, 0
	v_mbcnt_hi_u32_b32 v6, -1, v6
	v_mul_f32_e32 v27, v41, v1
	v_ashrrev_i32_e32 v7, 31, v6
	v_lshl_add_u64 v[6:7], v[6:7], 2, s[6:7]
	global_store_dword v[6:7], v26, off
	v_mul_f32_e32 v7, v43, v1
	v_mul_f32_e32 v6, v42, v1
	v_rndne_f32_e32 v7, v7
	v_mul_f32_e32 v26, v40, v1
	v_rndne_f32_e32 v6, v6
	v_cvt_i32_f32_e32 v7, v7
	v_rndne_f32_e32 v26, v26
	v_rndne_f32_e32 v27, v27
	v_cvt_i32_f32_e32 v6, v6
	v_cvt_i32_f32_sdwa v26, v26 dst_sel:WORD_1 dst_unused:UNUSED_PAD src0_sel:DWORD
	v_cvt_i32_f32_e32 v27, v27
	v_lshlrev_b32_e32 v7, 8, v7
	v_and_b32_e32 v7, 0xff00, v7
	v_and_b32_e32 v26, 0xff0000, v26
	v_perm_b32 v6, v27, v6, s1
	v_or3_b32 v26, v6, v7, v26
	v_mbcnt_lo_u32_b32 v6, -1, 0
	v_mbcnt_hi_u32_b32 v6, -1, v6
	v_mul_f32_e32 v27, v45, v1
	v_ashrrev_i32_e32 v7, 31, v6
	v_lshl_add_u64 v[6:7], v[6:7], 2, s[6:7]
	global_store_dword v[6:7], v26, off offset:256
	v_mul_f32_e32 v7, v47, v1
	v_mul_f32_e32 v6, v46, v1
	v_rndne_f32_e32 v7, v7
	v_mul_f32_e32 v26, v44, v1
	v_rndne_f32_e32 v6, v6
	v_cvt_i32_f32_e32 v7, v7
	v_rndne_f32_e32 v26, v26
	v_rndne_f32_e32 v27, v27
	v_cvt_i32_f32_e32 v6, v6
	v_cvt_i32_f32_sdwa v26, v26 dst_sel:WORD_1 dst_unused:UNUSED_PAD src0_sel:DWORD
	v_cvt_i32_f32_e32 v27, v27
	v_lshlrev_b32_e32 v7, 8, v7
	v_and_b32_e32 v7, 0xff00, v7
	v_and_b32_e32 v26, 0xff0000, v26
	v_perm_b32 v6, v27, v6, s1
	v_or3_b32 v26, v6, v7, v26
	v_mbcnt_lo_u32_b32 v6, -1, 0
	v_mbcnt_hi_u32_b32 v6, -1, v6
	v_mul_f32_e32 v27, v49, v1
	v_ashrrev_i32_e32 v7, 31, v6
	v_lshl_add_u64 v[6:7], v[6:7], 2, s[6:7]
	global_store_dword v[6:7], v26, off offset:512
	v_mul_f32_e32 v7, v51, v1
	v_mul_f32_e32 v6, v50, v1
	v_rndne_f32_e32 v7, v7
	v_mul_f32_e32 v26, v48, v1
	v_rndne_f32_e32 v6, v6
	v_cvt_i32_f32_e32 v7, v7
	v_rndne_f32_e32 v26, v26
	v_rndne_f32_e32 v27, v27
	v_cvt_i32_f32_e32 v6, v6
	v_cvt_i32_f32_sdwa v26, v26 dst_sel:WORD_1 dst_unused:UNUSED_PAD src0_sel:DWORD
	v_cvt_i32_f32_e32 v27, v27
	v_lshlrev_b32_e32 v7, 8, v7
	v_and_b32_e32 v7, 0xff00, v7
	v_and_b32_e32 v26, 0xff0000, v26
	v_perm_b32 v6, v27, v6, s1
	v_or3_b32 v26, v6, v7, v26
	v_mbcnt_lo_u32_b32 v6, -1, 0
	v_mbcnt_hi_u32_b32 v6, -1, v6
	v_mul_f32_e32 v27, v53, v1
	v_ashrrev_i32_e32 v7, 31, v6
	v_lshl_add_u64 v[6:7], v[6:7], 2, s[6:7]
	global_store_dword v[6:7], v26, off offset:768
	v_mul_f32_e32 v7, v55, v1
	v_mul_f32_e32 v6, v54, v1
	v_rndne_f32_e32 v7, v7
	v_mul_f32_e32 v26, v52, v1
	v_rndne_f32_e32 v6, v6
	v_cvt_i32_f32_e32 v7, v7
	v_rndne_f32_e32 v26, v26
	v_rndne_f32_e32 v27, v27
	v_cvt_i32_f32_e32 v6, v6
	v_cvt_i32_f32_sdwa v26, v26 dst_sel:WORD_1 dst_unused:UNUSED_PAD src0_sel:DWORD
	v_cvt_i32_f32_e32 v27, v27
	v_lshlrev_b32_e32 v7, 8, v7
	v_and_b32_e32 v7, 0xff00, v7
	v_and_b32_e32 v26, 0xff0000, v26
	v_perm_b32 v6, v27, v6, s1
	v_or3_b32 v26, v6, v7, v26
	v_mbcnt_lo_u32_b32 v6, -1, 0
	v_mbcnt_hi_u32_b32 v6, -1, v6
	v_mul_f32_e32 v27, v57, v1
	v_ashrrev_i32_e32 v7, 31, v6
	v_lshl_add_u64 v[6:7], v[6:7], 2, s[6:7]
	global_store_dword v[6:7], v26, off offset:1024
	v_mul_f32_e32 v7, v59, v1
	v_mul_f32_e32 v6, v58, v1
	v_rndne_f32_e32 v7, v7
	v_mul_f32_e32 v26, v56, v1
	v_rndne_f32_e32 v6, v6
	v_cvt_i32_f32_e32 v7, v7
	v_rndne_f32_e32 v26, v26
	v_rndne_f32_e32 v27, v27
	v_cvt_i32_f32_e32 v6, v6
	v_cvt_i32_f32_sdwa v26, v26 dst_sel:WORD_1 dst_unused:UNUSED_PAD src0_sel:DWORD
	v_cvt_i32_f32_e32 v27, v27
	v_lshlrev_b32_e32 v7, 8, v7
	v_and_b32_e32 v7, 0xff00, v7
	v_and_b32_e32 v26, 0xff0000, v26
	v_perm_b32 v6, v27, v6, s1
	v_or3_b32 v26, v6, v7, v26
	v_mbcnt_lo_u32_b32 v6, -1, 0
	v_mbcnt_hi_u32_b32 v6, -1, v6
	v_mul_f32_e32 v27, v61, v1
	v_ashrrev_i32_e32 v7, 31, v6
	v_lshl_add_u64 v[6:7], v[6:7], 2, s[6:7]
	global_store_dword v[6:7], v26, off offset:1280
	v_mul_f32_e32 v7, v63, v1
	v_mul_f32_e32 v6, v62, v1
	v_rndne_f32_e32 v7, v7
	v_mul_f32_e32 v26, v60, v1
	v_rndne_f32_e32 v6, v6
	v_cvt_i32_f32_e32 v7, v7
	v_rndne_f32_e32 v26, v26
	v_rndne_f32_e32 v27, v27
	v_mul_f32_e32 v5, v5, v1
	v_cvt_i32_f32_e32 v6, v6
	v_cvt_i32_f32_sdwa v26, v26 dst_sel:WORD_1 dst_unused:UNUSED_PAD src0_sel:DWORD
	v_cvt_i32_f32_e32 v27, v27
	v_mul_f32_e32 v4, v4, v1
	v_rndne_f32_e32 v5, v5
	v_mul_f32_e32 v2, v2, v1
	v_mul_f32_e32 v1, v3, v1
	v_rndne_f32_e32 v4, v4
	v_cvt_i32_f32_e32 v5, v5
	v_rndne_f32_e32 v2, v2
	v_rndne_f32_e32 v1, v1
	v_cvt_i32_f32_e32 v4, v4
	v_cvt_i32_f32_sdwa v2, v2 dst_sel:WORD_1 dst_unused:UNUSED_PAD src0_sel:DWORD
	v_cvt_i32_f32_e32 v1, v1
	v_lshlrev_b32_e32 v7, 8, v7
	v_and_b32_e32 v7, 0xff00, v7
	v_and_b32_e32 v26, 0xff0000, v26
	v_perm_b32 v6, v27, v6, s1
	v_or3_b32 v26, v6, v7, v26
	v_mbcnt_lo_u32_b32 v6, -1, 0
	v_mbcnt_hi_u32_b32 v6, -1, v6
	v_lshlrev_b32_e32 v3, 8, v5
	v_ashrrev_i32_e32 v7, 31, v6
	v_lshl_add_u64 v[6:7], v[6:7], 2, s[6:7]
	v_and_b32_e32 v3, 0xff00, v3
	v_and_b32_e32 v2, 0xff0000, v2
	v_perm_b32 v1, v1, v4, s1
	global_store_dword v[6:7], v26, off offset:1536
	v_or3_b32 v1, v1, v3, v2
	v_mbcnt_lo_u32_b32 v2, -1, 0
	v_mbcnt_hi_u32_b32 v2, -1, v2
	s_nop 0
	v_ashrrev_i32_e32 v3, 31, v2
	v_lshl_add_u64 v[2:3], v[2:3], 2, s[6:7]
	global_store_dword v[2:3], v1, off offset:1792
	v_mbcnt_lo_u32_b32 v1, -1, 0
	v_mbcnt_hi_u32_b32 v1, -1, v1
	s_nop 0
	v_cmp_eq_u32_e32 vcc, 0, v1
	s_and_saveexec_b64 s[6:7], vcc
	s_cbranch_execz .LBB0_1495
	s_lshl_b32 s8, s4, 1
	s_ashr_i32 s9, s8, 31
	s_lshl_b64 s[8:9], s[8:9], 2
	s_add_u32 s8, s27, s8
	s_addc_u32 s9, s64, s9
	v_readlane_b32 s0, v255, 47
	s_lshl_b64 s[4:5], s[4:5], 2
	v_mul_f32_e32 v2, 0x3a000000, v25
	v_mov_b32_e32 v3, v24
	v_mov_b32_e32 v1, s0
	s_add_u32 s4, s25, s4
	v_readlane_b32 s0, v255, 36
	ds_write_b64 v1, v[2:3]
	s_addc_u32 s5, s26, s5
	v_mov_b32_e32 v1, s0
	global_store_dwordx2 v33, v[2:3], s[8:9]
	global_store_dword v33, v0, s[4:5]
	ds_write_b32 v1, v0
; __device__ __forceinline__ void p6_router(Frame& F) {
;     ...
;                 f32x4 v[8]; float s = 0.f;
; #pragma unroll
;                 for (int j = 0; j < 8; ++j) { const v2u w = raw[rr][j]; v[j] = (f32x4){bf_lo(w.x), bf_hi(w.x), bf_lo(w.y), bf_hi(w.y)}; s += (v[j][0] + v[j][1]) + (v[j][2] + v[j][3]); }
;                 const float mean = wave_sum(s) * (1.f / D); float s2 = 0.f;
; #pragma unroll
;                 for (int j = 0; j < 8; ++j) { v[j] = v[j] - mean; s2 += (v[j][0] * v[j][0] + v[j][1] * v[j][1]) + (v[j][2] * v[j][2] + v[j][3] * v[j][3]); }
.LBB0_1495:
	s_or_b64 exec, exec, s[6:7]
	v_lshlrev_b32_e32 v27, 16, v22
	v_lshlrev_b32_e32 v26, 16, v20
	v_and_b32_e32 v43, 0xffff0000, v22
	v_and_b32_e32 v42, 0xffff0000, v20
	v_lshlrev_b32_e32 v45, 16, v23
	v_lshlrev_b32_e32 v44, 16, v21
	v_and_b32_e32 v47, 0xffff0000, v23
	v_and_b32_e32 v46, 0xffff0000, v21
	v_pk_add_f32 v[0:1], v[26:27], v[42:43]
	v_pk_add_f32 v[2:3], v[44:45], v[46:47]
	v_lshlrev_b32_e32 v25, 16, v19
	v_pk_add_f32 v[0:1], v[0:1], v[2:3]
	v_lshlrev_b32_e32 v24, 16, v18
	v_add_f32_e32 v0, 0, v0
	v_and_b32_e32 v49, 0xffff0000, v19
	v_and_b32_e32 v48, 0xffff0000, v18
	v_add_f32_e32 v6, v0, v1
	v_pk_add_f32 v[0:1], v[24:25], v[48:49]
	v_lshlrev_b32_e32 v28, 16, v16
	v_and_b32_e32 v29, 0xffff0000, v16
	v_lshlrev_b32_e32 v30, 16, v17
	v_and_b32_e32 v31, 0xffff0000, v17
	v_and_b32_e32 v41, 0xffff0000, v14
	v_pk_add_f32 v[0:1], v[0:1], v[0:1] op_sel:[0,1] op_sel_hi:[1,0]
	v_add_f32_e32 v38, v28, v29
	v_add_f32_e32 v36, v30, v31
	v_lshlrev_b32_e32 v7, 16, v14
	v_lshlrev_b32_e32 v39, 16, v15
	v_and_b32_e32 v37, 0xffff0000, v15
	v_mov_b32_e32 v1, v41
	v_pk_add_f32 v[0:1], v[6:7], v[0:1]
	v_pk_add_f32 v[2:3], v[38:39], v[36:37]
	v_lshlrev_b32_e32 v5, 16, v13
	v_lshlrev_b32_e32 v4, 16, v12
	v_and_b32_e32 v51, 0xffff0000, v13
	v_and_b32_e32 v50, 0xffff0000, v12
	v_pk_add_f32 v[16:17], v[0:1], v[2:3]
	v_pk_add_f32 v[18:19], v[4:5], v[50:51]
	v_lshlrev_b32_e32 v0, 16, v10
	v_and_b32_e32 v1, 0xffff0000, v10
	v_lshlrev_b32_e32 v2, 16, v11
	v_and_b32_e32 v3, 0xffff0000, v11
	v_lshlrev_b32_e32 v14, 16, v8
	v_and_b32_e32 v15, 0xffff0000, v8
	v_lshlrev_b32_e32 v13, 16, v9
	v_and_b32_e32 v11, 0xffff0000, v9
	v_pk_add_f32 v[8:9], v[16:17], v[16:17] op_sel:[0,1] op_sel_hi:[1,0]
	v_pk_add_f32 v[16:17], v[18:19], v[18:19] op_sel:[0,1] op_sel_hi:[1,0]
	v_add_f32_e32 v12, v0, v1
	v_add_f32_e32 v10, v2, v3
	v_mov_b32_e32 v9, v14
	v_mov_b32_e32 v17, v15
	v_pk_add_f32 v[8:9], v[8:9], v[16:17]
	v_pk_add_f32 v[16:17], v[12:13], v[10:11]
	s_nop 0
	v_pk_add_f32 v[8:9], v[8:9], v[16:17]
	s_nop 0
	v_add_f32_e32 v6, v8, v9
	s_waitcnt lgkmcnt(0)
	s_nop 1
	v_add_f32_dpp v6, v6, v6 quad_perm:[1,0,3,2] row_mask:0xf bank_mask:0xf
	s_waitcnt lgkmcnt(0)
	s_nop 1
	v_add_f32_dpp v6, v6, v6 quad_perm:[2,3,0,1] row_mask:0xf bank_mask:0xf
	s_waitcnt lgkmcnt(0)
	s_nop 1
	v_add_f32_dpp v6, v6, v6 row_half_mirror row_mask:0xf bank_mask:0xf
	s_waitcnt lgkmcnt(0)
	s_nop 1
	v_add_f32_dpp v6, v6, v6 row_mirror row_mask:0xf bank_mask:0xf
	s_waitcnt lgkmcnt(0)
	v_mov_b32_e32 v8, v6
	s_nop 1
	v_permlane16_swap_b32_e32 v6, v8
	v_add_f32_e32 v6, v6, v8
	s_waitcnt lgkmcnt(0)
	v_mov_b32_e32 v8, v6
	s_nop 1
	v_permlane32_swap_b32_e32 v6, v8
	v_add_f32_e32 v9, v6, v8
	v_fmac_f32_e32 v46, 0xba000000, v9
	v_fmac_f32_e32 v42, 0xba000000, v9
	v_fmac_f32_e32 v47, 0xba000000, v9
	v_fmac_f32_e32 v43, 0xba000000, v9
	v_fmac_f32_e32 v44, 0xba000000, v9
	v_fmac_f32_e32 v26, 0xba000000, v9
	v_fmac_f32_e32 v45, 0xba000000, v9
	v_fmac_f32_e32 v27, 0xba000000, v9
	v_mov_b32_e32 v21, v43
	v_mov_b32_e32 v17, v42
	v_pk_mul_f32 v[18:19], v[42:43], v[42:43]
	v_pk_mul_f32 v[42:43], v[46:47], v[46:47]
	v_mov_b32_e32 v20, v27
	v_mov_b32_e32 v16, v26
	v_pk_fma_f32 v[26:27], v[26:27], v[26:27], v[18:19]
	v_pk_fma_f32 v[42:43], v[44:45], v[44:45], v[42:43]
	v_fmac_f32_e32 v48, 0xba000000, v9
	v_pk_add_f32 v[26:27], v[26:27], v[42:43]
	v_fmac_f32_e32 v49, 0xba000000, v9
	v_fmac_f32_e32 v25, 0xba000000, v9
	v_pk_add_f32 v[42:43], v[26:27], v[26:27] op_sel_hi:[0,1]
	v_fmac_f32_e32 v24, 0xba000000, v9
	v_mov_b32_e32 v26, v25
	v_mov_b32_e32 v27, v49
	v_mov_b32_e32 v25, v48
	v_mov_b32_e32 v22, v45
	v_mov_b32_e32 v23, v47
	v_mov_b32_e32 v18, v44
	v_mov_b32_e32 v19, v46
	v_pk_mul_f32 v[44:45], v[26:27], v[26:27]
	v_pk_mul_f32 v[46:47], v[24:25], v[24:25]
	v_fmac_f32_e32 v28, 0xba000000, v9
	v_pk_mov_b32 v[48:49], v[46:47], v[44:45] op_sel:[1,0]
	v_mov_b32_e32 v47, v45
	v_fmac_f32_e32 v29, 0xba000000, v9
	v_fmac_f32_e32 v30, 0xba000000, v9
	v_mul_f32_e32 v6, v28, v28
	v_pk_add_f32 v[44:45], v[48:49], v[46:47]
	v_fmac_f32_e32 v31, 0xba000000, v9
	v_pk_fma_f32 v[46:47], v[28:29], v[28:29], v[6:7] op_sel_hi:[1,1,0]
	v_mul_f32_e32 v6, v30, v30
	v_pk_add_f32 v[44:45], v[44:45], v[44:45] op_sel_hi:[0,1]
	v_pk_fma_f32 v[48:49], v[30:31], v[30:31], v[6:7] op_sel_hi:[1,1,0]
	v_fmac_f32_e32 v37, 0xba000000, v9
	v_fmac_f32_e32 v39, 0xba000000, v9
	v_fmac_f32_e32 v41, 0xba000000, v9
	v_fmac_f32_e32 v7, 0xba000000, v9
	v_mul_f32_e32 v46, v7, v7
	v_mul_f32_e32 v48, v41, v41
	v_mul_f32_e32 v44, v39, v39
	v_mul_f32_e32 v42, v37, v37
	v_pk_add_f32 v[46:47], v[46:47], v[48:49]
	v_pk_add_f32 v[42:43], v[44:45], v[42:43]
	v_fmac_f32_e32 v50, 0xba000000, v9
	v_pk_add_f32 v[42:43], v[46:47], v[42:43]
	v_fmac_f32_e32 v51, 0xba000000, v9
	v_fmac_f32_e32 v5, 0xba000000, v9
	v_pk_add_f32 v[44:45], v[42:43], v[42:43] op_sel_hi:[0,1]
	v_fmac_f32_e32 v4, 0xba000000, v9
	v_mov_b32_e32 v42, v5
	v_mov_b32_e32 v43, v51
	v_mov_b32_e32 v5, v50
	v_pk_mul_f32 v[46:47], v[42:43], v[42:43]
	v_pk_mul_f32 v[48:49], v[4:5], v[4:5]
	v_fmac_f32_e32 v0, 0xba000000, v9
	v_pk_mov_b32 v[50:51], v[48:49], v[46:47] op_sel:[1,0]
	v_mov_b32_e32 v49, v47
	v_fmac_f32_e32 v1, 0xba000000, v9
	v_fmac_f32_e32 v2, 0xba000000, v9
	v_mul_f32_e32 v6, v0, v0
	v_pk_add_f32 v[46:47], v[50:51], v[48:49]
	v_fmac_f32_e32 v3, 0xba000000, v9
	v_pk_fma_f32 v[48:49], v[0:1], v[0:1], v[6:7] op_sel_hi:[1,1,0]
	v_mul_f32_e32 v6, v2, v2
	v_pk_add_f32 v[46:47], v[46:47], v[46:47] op_sel_hi:[0,1]
	v_pk_fma_f32 v[50:51], v[2:3], v[2:3], v[6:7] op_sel_hi:[1,1,0]
	v_fmac_f32_e32 v11, 0xba000000, v9
	v_fmac_f32_e32 v13, 0xba000000, v9
	v_fmac_f32_e32 v15, 0xba000000, v9
	v_fmac_f32_e32 v14, 0xba000000, v9
	v_mul_f32_e32 v48, v14, v14
	v_mul_f32_e32 v50, v15, v15
	v_mul_f32_e32 v46, v13, v13
	v_mul_f32_e32 v44, v11, v11
	v_pk_add_f32 v[48:49], v[48:49], v[50:51]
	v_pk_add_f32 v[44:45], v[46:47], v[44:45]
	v_mov_b32_e32 v40, v7
	v_pk_add_f32 v[44:45], v[48:49], v[44:45]
	s_nop 0
	v_add_f32_e32 v6, v44, v45
	v_mbcnt_lo_u32_b32 v44, -1, 0
	v_mbcnt_hi_u32_b32 v44, -1, v44
	v_ashrrev_i32_e32 v45, 31, v44
	v_lshl_add_u64 v[44:45], v[44:45], 4, s[12:13]
	v_mbcnt_lo_u32_b32 v48, -1, 0
	v_mbcnt_hi_u32_b32 v48, -1, v48
	s_waitcnt lgkmcnt(0)
; #define GAS __attribute__((address_space(1)))
; #define FLANE lane_id()
; __device__ __forceinline__ void p6_router(Frame& F) {
;     ...
;                 for (int j = 0; j < 8; ++j) { v[j] = v[j] - mean; s2 += (v[j][0] * v[j][0] + v[j][1] * v[j][1]) + (v[j][2] * v[j][2] + v[j][3] * v[j][3]); }
;                 const float rstd = 1.f / sqrtf(wave_sum(s2) * (1.f / D) + LN_EPS);
;                 float am = 0.f;
; #pragma unroll
;                 for (int j = 0; j < 8; ++j) { const f32x4 g = *((const GAS f32x4*)F.ln1_g + FLANE + 64 * j), b = *((const GAS f32x4*)F.ln1_b + FLANE + 64 * j);
;                     v[j] = v[j] * rstd * g + b; am = fmaxf(am, fmaxf(fmaxf(fabsf(v[j][0]), fabsf(v[j][1])), fmaxf(fabsf(v[j][2]), fabsf(v[j][3])))); }
	s_nop 1
	v_add_f32_dpp v6, v6, v6 quad_perm:[1,0,3,2] row_mask:0xf bank_mask:0xf
	v_ashrrev_i32_e32 v49, 31, v48
	v_lshl_add_u64 v[48:49], v[48:49], 4, s[14:15]
	s_waitcnt lgkmcnt(0)
	s_nop 1
	v_add_f32_dpp v6, v6, v6 quad_perm:[2,3,0,1] row_mask:0xf bank_mask:0xf
	s_waitcnt lgkmcnt(0)
	s_nop 1
	v_add_f32_dpp v6, v6, v6 row_half_mirror row_mask:0xf bank_mask:0xf
	s_waitcnt lgkmcnt(0)
	s_nop 1
	v_add_f32_dpp v6, v6, v6 row_mirror row_mask:0xf bank_mask:0xf
	s_waitcnt lgkmcnt(0)
	v_mov_b32_e32 v8, v6
	s_nop 1
	v_permlane16_swap_b32_e32 v6, v8
	v_add_f32_e32 v6, v6, v8
	s_waitcnt lgkmcnt(0)
	v_mov_b32_e32 v8, v6
	s_nop 1
	v_permlane32_swap_b32_e32 v6, v8
	v_add_f32_e32 v6, v6, v8
	v_fmamk_f32 v6, v6, 0x3a000000, v166
	v_cmp_gt_f32_e32 vcc, s22, v6
	v_mul_f32_e32 v8, 0x4f800000, v6
	s_nop 0
	v_cndmask_b32_e32 v6, v6, v8, vcc
	v_sqrt_f32_e32 v8, v6
	s_nop 0
	v_add_u32_e32 v10, -1, v8
	v_fma_f32 v12, -v10, v8, v6
	v_cmp_ge_f32_e64 s[4:5], 0, v12
	v_add_u32_e32 v12, 1, v8
	s_nop 0
	v_cndmask_b32_e64 v10, v8, v10, s[4:5]
	v_fma_f32 v8, -v12, v8, v6
	v_cmp_lt_f32_e64 s[4:5], 0, v8
	s_nop 1
	v_cndmask_b32_e64 v8, v10, v12, s[4:5]
	v_mul_f32_e32 v10, 0x37800000, v8
	v_cndmask_b32_e32 v8, v8, v10, vcc
	v_cmp_class_f32_e32 vcc, v6, v167
	s_nop 1
	v_cndmask_b32_e32 v6, v8, v6, vcc
	v_div_scale_f32 v8, s[4:5], v6, v6, 1.0
	v_rcp_f32_e32 v10, v8
	s_add_i32 s4, s42, s79
	s_ashr_i32 s5, s4, 31
	v_fma_f32 v12, -v8, v10, 1.0
	v_fmac_f32_e32 v10, v12, v10
	v_div_scale_f32 v12, vcc, 1.0, v6, 1.0
	v_mul_f32_e32 v32, v12, v10
	v_fma_f32 v36, -v8, v32, v12
	v_fmac_f32_e32 v32, v36, v10
	v_fma_f32 v8, -v8, v32, v12
	v_div_fmas_f32 v8, v8, v10, v32
	v_div_fixup_f32 v8, v8, v6, 1.0
	v_pk_mul_f32 v[52:53], v[16:17], v[8:9] op_sel_hi:[1,0]
	v_pk_mul_f32 v[16:17], v[18:19], v[8:9] op_sel_hi:[1,0]
	v_mov_b32_e32 v36, v39
	v_pk_mul_f32 v[36:37], v[36:37], v[8:9] op_sel_hi:[1,0]
	v_pk_mul_f32 v[4:5], v[4:5], v[8:9] op_sel_hi:[1,0]
	v_pk_mul_f32 v[2:3], v[2:3], v[8:9] op_sel_hi:[1,0]
	v_pk_mul_f32 v[0:1], v[0:1], v[8:9] op_sel_hi:[1,0]
	s_waitcnt vmcnt(0)
	v_pk_fma_f32 v[18:19], v[196:197], v[52:53], v[228:229]
	v_mbcnt_lo_u32_b32 v44, -1, 0
	v_mbcnt_hi_u32_b32 v44, -1, v44
	v_pk_fma_f32 v[16:17], v[198:199], v[16:17], v[230:231]
	v_ashrrev_i32_e32 v45, 31, v44
	v_lshl_add_u64 v[44:45], v[44:45], 4, s[12:13]
	v_mbcnt_lo_u32_b32 v48, -1, 0
	v_mbcnt_hi_u32_b32 v48, -1, v48
	v_pk_mul_f32 v[52:53], v[20:21], v[8:9] op_sel_hi:[1,0]
	v_ashrrev_i32_e32 v49, 31, v48
	v_lshl_add_u64 v[48:49], v[48:49], 4, s[14:15]
	v_pk_mul_f32 v[20:21], v[22:23], v[8:9] op_sel_hi:[1,0]
	v_max_f32_e64 v6, |v16|, |v17|
	v_max3_f32 v6, |v18|, |v19|, v6
	v_pk_mul_f32 v[14:15], v[14:15], v[8:9] op_sel_hi:[1,0]
	s_waitcnt vmcnt(0)
	v_pk_fma_f32 v[22:23], v[200:201], v[52:53], v[232:233]
	v_mbcnt_lo_u32_b32 v44, -1, 0
	v_mbcnt_hi_u32_b32 v44, -1, v44
	v_pk_fma_f32 v[20:21], v[202:203], v[20:21], v[234:235]
	v_ashrrev_i32_e32 v45, 31, v44
	v_lshl_add_u64 v[44:45], v[44:45], 4, s[12:13]
	v_mbcnt_lo_u32_b32 v48, -1, 0
	v_mbcnt_hi_u32_b32 v48, -1, v48
	v_pk_mul_f32 v[52:53], v[24:25], v[8:9] op_sel_hi:[1,0]
	v_ashrrev_i32_e32 v49, 31, v48
	v_lshl_add_u64 v[48:49], v[48:49], 4, s[14:15]
	v_pk_mul_f32 v[24:25], v[26:27], v[8:9] op_sel_hi:[1,0]
	v_max_f32_e64 v10, |v20|, |v21|
	v_max3_f32 v10, |v22|, |v23|, v10
	v_max3_f32 v6, v6, 0, v10
	s_waitcnt vmcnt(0)
	v_pk_fma_f32 v[26:27], v[204:205], v[52:53], v[236:237]
	v_mbcnt_lo_u32_b32 v44, -1, 0
	v_mbcnt_hi_u32_b32 v44, -1, v44
	v_pk_fma_f32 v[24:25], v[206:207], v[24:25], v[238:239]
	v_ashrrev_i32_e32 v45, 31, v44
	v_lshl_add_u64 v[44:45], v[44:45], 4, s[12:13]
	v_mbcnt_lo_u32_b32 v48, -1, 0
	v_mbcnt_hi_u32_b32 v48, -1, v48
	v_pk_mul_f32 v[52:53], v[28:29], v[8:9] op_sel_hi:[1,0]
	v_ashrrev_i32_e32 v49, 31, v48
	v_lshl_add_u64 v[48:49], v[48:49], 4, s[14:15]
	v_pk_mul_f32 v[28:29], v[30:31], v[8:9] op_sel_hi:[1,0]
	v_max_f32_e64 v10, |v24|, |v25|
	v_max3_f32 v10, |v26|, |v27|, v10
	s_waitcnt vmcnt(0)
	v_pk_fma_f32 v[30:31], v[208:209], v[52:53], v[240:241]
	v_mbcnt_lo_u32_b32 v44, -1, 0
	v_mbcnt_hi_u32_b32 v44, -1, v44
	v_pk_fma_f32 v[28:29], v[210:211], v[28:29], v[242:243]
	v_ashrrev_i32_e32 v45, 31, v44
	v_lshl_add_u64 v[44:45], v[44:45], 4, s[12:13]
	v_add_co_u32_e32 v44, vcc, s23, v44
	v_max_f32_e64 v12, |v28|, |v29|
	s_nop 0
	v_addc_co_u32_e32 v45, vcc, 0, v45, vcc
	v_mbcnt_lo_u32_b32 v48, -1, 0
	v_mbcnt_hi_u32_b32 v48, -1, v48
	v_max3_f32 v12, |v30|, |v31|, v12
	v_ashrrev_i32_e32 v49, 31, v48
	v_lshl_add_u64 v[48:49], v[48:49], 4, s[14:15]
	v_add_co_u32_e32 v48, vcc, s23, v48
	v_max3_f32 v10, v6, v10, v12
	s_nop 0
	v_addc_co_u32_e32 v49, vcc, 0, v49, vcc
	v_pk_mul_f32 v[6:7], v[40:41], v[8:9] op_sel_hi:[1,0]
	s_waitcnt vmcnt(0)
	v_pk_fma_f32 v[36:37], v[214:215], v[36:37], v[246:247]
	v_pk_fma_f32 v[38:39], v[212:213], v[6:7], v[244:245]
	v_max_f32_e64 v6, |v36|, |v37|
	v_max3_f32 v12, |v38|, |v39|, v6
	v_mbcnt_lo_u32_b32 v6, -1, 0
	v_mbcnt_hi_u32_b32 v6, -1, v6
	s_nop 0
	v_ashrrev_i32_e32 v7, 31, v6
	v_lshl_add_u64 v[6:7], v[6:7], 4, s[12:13]
	v_add_co_u32_e32 v6, vcc, s23, v6
	s_nop 1
	v_addc_co_u32_e32 v7, vcc, 0, v7, vcc
	v_mbcnt_lo_u32_b32 v6, -1, 0
	v_mbcnt_hi_u32_b32 v6, -1, v6
	s_nop 0
	v_ashrrev_i32_e32 v7, 31, v6
	v_lshl_add_u64 v[6:7], v[6:7], 4, s[14:15]
	v_add_co_u32_e32 v6, vcc, s23, v6
	s_nop 1
	v_addc_co_u32_e32 v7, vcc, 0, v7, vcc
	v_pk_mul_f32 v[6:7], v[42:43], v[8:9] op_sel_hi:[1,0]
	s_waitcnt vmcnt(0)
; #define GAS __attribute__((address_space(1)))
; #define FLANE lane_id()
; __device__ __forceinline__ void p6_router(Frame& F) {
;     ...
;                 for (int j = 0; j < 8; ++j) { const f32x4 g = *((const GAS f32x4*)F.ln1_g + FLANE + 64 * j), b = *((const GAS f32x4*)F.ln1_b + FLANE + 64 * j);
;                     v[j] = v[j] * rstd * g + b; am = fmaxf(am, fmaxf(fmaxf(fabsf(v[j][0]), fabsf(v[j][1])), fmaxf(fabsf(v[j][2]), fabsf(v[j][3])))); }
; #pragma unroll
;                 for (int o = 1; o < 64; o <<= 1) am = fmaxf(am, __shfl_xor(am, o));
	v_pk_fma_f32 v[42:43], v[216:217], v[4:5], v[248:249]
	v_pk_fma_f32 v[40:41], v[218:219], v[6:7], v[250:251]
	s_nop 0
	v_max_f32_e64 v4, |v40|, |v41|
	v_max3_f32 v4, |v42|, |v43|, v4
	v_max3_f32 v12, v10, v12, v4
	v_mbcnt_lo_u32_b32 v4, -1, 0
	v_mbcnt_hi_u32_b32 v4, -1, v4
	v_mov_b32_e32 v10, v13
	v_ashrrev_i32_e32 v5, 31, v4
	v_lshl_add_u64 v[4:5], v[4:5], 4, s[12:13]
	v_add_co_u32_e32 v4, vcc, s23, v4
	v_pk_mul_f32 v[10:11], v[10:11], v[8:9] op_sel_hi:[1,0]
	s_nop 0
	v_addc_co_u32_e32 v5, vcc, 0, v5, vcc
	v_mbcnt_lo_u32_b32 v44, -1, 0
	v_mbcnt_hi_u32_b32 v44, -1, v44
	s_nop 0
	v_ashrrev_i32_e32 v45, 31, v44
	v_lshl_add_u64 v[44:45], v[44:45], 4, s[14:15]
	v_add_co_u32_e32 v44, vcc, s23, v44
	s_nop 1
	v_addc_co_u32_e32 v45, vcc, 0, v45, vcc
	s_waitcnt vmcnt(0)
	v_pk_fma_f32 v[44:45], v[2:3], v[222:223], v[184:185]
	v_pk_fma_f32 v[46:47], v[0:1], v[220:221], v[182:183]
	v_max_f32_e64 v0, |v44|, |v45|
	v_max3_f32 v32, |v46|, |v47|, v0
	v_mbcnt_lo_u32_b32 v0, -1, 0
	v_mbcnt_hi_u32_b32 v0, -1, v0
	s_nop 0
	v_ashrrev_i32_e32 v1, 31, v0
	v_lshl_add_u64 v[0:1], v[0:1], 4, s[12:13]
	v_add_co_u32_e32 v0, vcc, s23, v0
	s_nop 1
	v_addc_co_u32_e32 v1, vcc, 0, v1, vcc
	v_mbcnt_lo_u32_b32 v4, -1, 0
	v_mbcnt_hi_u32_b32 v4, -1, v4
	s_nop 0
	v_ashrrev_i32_e32 v5, 31, v4
	v_lshl_add_u64 v[4:5], v[4:5], 4, s[14:15]
	v_add_co_u32_e32 v4, vcc, s23, v4
	s_nop 1
	v_addc_co_u32_e32 v5, vcc, 0, v5, vcc
	s_waitcnt vmcnt(0)
	v_pk_fma_f32 v[2:3], v[10:11], v[226:227], v[188:189]
	v_pk_fma_f32 v[4:5], v[14:15], v[224:225], v[186:187]
	v_max_f32_e64 v0, |v2|, |v3|
	v_max3_f32 v0, |v4|, |v5|, v0
	v_max3_f32 v0, v12, v32, v0
	s_waitcnt lgkmcnt(0)
	s_nop 1
	v_max_f32_dpp v0, v0, v0 quad_perm:[1,0,3,2] row_mask:0xf bank_mask:0xf
	s_waitcnt lgkmcnt(0)
	s_nop 1
	v_max_f32_dpp v0, v0, v0 quad_perm:[2,3,0,1] row_mask:0xf bank_mask:0xf
	s_waitcnt lgkmcnt(0)
	s_nop 1
	v_max_f32_dpp v0, v0, v0 row_half_mirror row_mask:0xf bank_mask:0xf
	s_waitcnt lgkmcnt(0)
	s_nop 1
	v_max_f32_dpp v0, v0, v0 row_mirror row_mask:0xf bank_mask:0xf
	s_waitcnt lgkmcnt(0)
	v_mov_b32_e32 v1, v0
	s_nop 1
	v_permlane16_swap_b32_e32 v0, v1
	v_max_f32_e32 v0, v0, v1
	s_waitcnt lgkmcnt(0)
; #define FLANE lane_id()
; __device__ __forceinline__ void p6_router(Frame& F) {
;     ...
;                 for (int o = 1; o < 64; o <<= 1) am = fmaxf(am, __shfl_xor(am, o));
;                 const float sc = am > 0.f ? am * (1.f / 127.f) : 1.f, inv = 1.f / sc;
; #pragma unroll
;                 for (int j = 0; j < 8; ++j) { const int q0 = (int)__builtin_rintf(v[j][0] * inv), q1 = (int)__builtin_rintf(v[j][1] * inv), q2 = (int)__builtin_rintf(v[j][2] * inv), q3 = (int)__builtin_rintf(v[j][3] * inv);
;                     h1q[(size_t)m * (D / 4) + FLANE + 64 * j] = (unsigned)(q0 & 0xff) | ((unsigned)(q1 & 0xff) << 8) | ((unsigned)(q2 & 0xff) << 16) | ((unsigned)(q3 & 0xff) << 24); }
;                 if (FLANE == 0) { st1[2 * m] = mean; st1[2 * m + 1] = rstd; stl[2 * row] = mean; stl[2 * row + 1] = rstd; sxg[m] = sc; sxl[row] = sc; }
	v_mov_b32_e32 v1, v0
	s_nop 1
	v_permlane32_swap_b32_e32 v0, v1
	v_max_f32_e32 v0, v0, v1
	v_cmp_lt_f32_e32 vcc, 0, v0
	v_mul_f32_e32 v0, 0x3c010204, v0
	s_nop 0
	v_cndmask_b32_e32 v0, 1.0, v0, vcc
	v_div_scale_f32 v1, s[6:7], v0, v0, 1.0
	v_rcp_f32_e32 v6, v1
	s_lshl_b64 s[6:7], s[4:5], 11
	s_add_u32 s6, s3, s6
	s_addc_u32 s7, s24, s7
	v_fma_f32 v7, -v1, v6, 1.0
	v_fmac_f32_e32 v6, v7, v6
	v_div_scale_f32 v7, vcc, 1.0, v0, 1.0
	v_mul_f32_e32 v10, v7, v6
	v_fma_f32 v11, -v1, v10, v7
	v_fmac_f32_e32 v10, v11, v6
	v_fma_f32 v1, -v1, v10, v7
	v_div_fmas_f32 v1, v1, v6, v10
	v_div_fixup_f32 v1, v1, v0, 1.0
	v_mul_f32_e32 v7, v19, v1
	v_mul_f32_e32 v6, v18, v1
	v_rndne_f32_e32 v7, v7
	v_mul_f32_e32 v10, v16, v1
	v_mul_f32_e32 v11, v17, v1
	v_rndne_f32_e32 v6, v6
	v_cvt_i32_f32_e32 v7, v7
	v_rndne_f32_e32 v10, v10
	v_rndne_f32_e32 v11, v11
	v_cvt_i32_f32_e32 v6, v6
	v_cvt_i32_f32_sdwa v10, v10 dst_sel:WORD_1 dst_unused:UNUSED_PAD src0_sel:DWORD
	v_cvt_i32_f32_e32 v11, v11
	v_lshlrev_b32_e32 v7, 8, v7
	v_and_b32_e32 v7, 0xff00, v7
	v_and_b32_e32 v10, 0xff0000, v10
	v_perm_b32 v6, v11, v6, s1
	v_or3_b32 v10, v6, v7, v10
	v_mbcnt_lo_u32_b32 v6, -1, 0
	v_mbcnt_hi_u32_b32 v6, -1, v6
	v_mul_f32_e32 v11, v21, v1
	v_ashrrev_i32_e32 v7, 31, v6
	v_lshl_add_u64 v[6:7], v[6:7], 2, s[6:7]
	global_store_dword v[6:7], v10, off
	v_mul_f32_e32 v7, v23, v1
	v_mul_f32_e32 v6, v22, v1
	v_rndne_f32_e32 v7, v7
	v_mul_f32_e32 v10, v20, v1
	v_rndne_f32_e32 v6, v6
	v_cvt_i32_f32_e32 v7, v7
	v_rndne_f32_e32 v10, v10
	v_rndne_f32_e32 v11, v11
	v_cvt_i32_f32_e32 v6, v6
	v_cvt_i32_f32_sdwa v10, v10 dst_sel:WORD_1 dst_unused:UNUSED_PAD src0_sel:DWORD
	v_cvt_i32_f32_e32 v11, v11
	v_lshlrev_b32_e32 v7, 8, v7
	v_and_b32_e32 v7, 0xff00, v7
	v_and_b32_e32 v10, 0xff0000, v10
	v_perm_b32 v6, v11, v6, s1
	v_or3_b32 v10, v6, v7, v10
	v_mbcnt_lo_u32_b32 v6, -1, 0
	v_mbcnt_hi_u32_b32 v6, -1, v6
	v_mul_f32_e32 v11, v25, v1
	v_ashrrev_i32_e32 v7, 31, v6
	v_lshl_add_u64 v[6:7], v[6:7], 2, s[6:7]
	global_store_dword v[6:7], v10, off offset:256
	v_mul_f32_e32 v7, v27, v1
	v_mul_f32_e32 v6, v26, v1
	v_rndne_f32_e32 v7, v7
	v_mul_f32_e32 v10, v24, v1
	v_rndne_f32_e32 v6, v6
	v_cvt_i32_f32_e32 v7, v7
	v_rndne_f32_e32 v10, v10
	v_rndne_f32_e32 v11, v11
	v_cvt_i32_f32_e32 v6, v6
	v_cvt_i32_f32_sdwa v10, v10 dst_sel:WORD_1 dst_unused:UNUSED_PAD src0_sel:DWORD
	v_cvt_i32_f32_e32 v11, v11
	v_lshlrev_b32_e32 v7, 8, v7
	v_and_b32_e32 v7, 0xff00, v7
	v_and_b32_e32 v10, 0xff0000, v10
	v_perm_b32 v6, v11, v6, s1
	v_or3_b32 v10, v6, v7, v10
	v_mbcnt_lo_u32_b32 v6, -1, 0
	v_mbcnt_hi_u32_b32 v6, -1, v6
	v_mul_f32_e32 v11, v29, v1
	v_ashrrev_i32_e32 v7, 31, v6
	v_lshl_add_u64 v[6:7], v[6:7], 2, s[6:7]
	global_store_dword v[6:7], v10, off offset:512
	v_mul_f32_e32 v7, v31, v1
	v_mul_f32_e32 v6, v30, v1
	v_rndne_f32_e32 v7, v7
	v_mul_f32_e32 v10, v28, v1
	v_rndne_f32_e32 v6, v6
	v_cvt_i32_f32_e32 v7, v7
	v_rndne_f32_e32 v10, v10
	v_rndne_f32_e32 v11, v11
	v_cvt_i32_f32_e32 v6, v6
	v_cvt_i32_f32_sdwa v10, v10 dst_sel:WORD_1 dst_unused:UNUSED_PAD src0_sel:DWORD
	v_cvt_i32_f32_e32 v11, v11
	v_lshlrev_b32_e32 v7, 8, v7
	v_and_b32_e32 v7, 0xff00, v7
	v_and_b32_e32 v10, 0xff0000, v10
	v_perm_b32 v6, v11, v6, s1
	v_or3_b32 v10, v6, v7, v10
	v_mbcnt_lo_u32_b32 v6, -1, 0
	v_mbcnt_hi_u32_b32 v6, -1, v6
	v_mul_f32_e32 v11, v37, v1
	v_ashrrev_i32_e32 v7, 31, v6
	v_lshl_add_u64 v[6:7], v[6:7], 2, s[6:7]
	global_store_dword v[6:7], v10, off offset:768
	v_mul_f32_e32 v7, v39, v1
	v_mul_f32_e32 v6, v38, v1
	v_rndne_f32_e32 v7, v7
	v_mul_f32_e32 v10, v36, v1
	v_rndne_f32_e32 v6, v6
	v_cvt_i32_f32_e32 v7, v7
	v_rndne_f32_e32 v10, v10
	v_rndne_f32_e32 v11, v11
	v_cvt_i32_f32_e32 v6, v6
	v_cvt_i32_f32_sdwa v10, v10 dst_sel:WORD_1 dst_unused:UNUSED_PAD src0_sel:DWORD
	v_cvt_i32_f32_e32 v11, v11
	v_lshlrev_b32_e32 v7, 8, v7
	v_and_b32_e32 v7, 0xff00, v7
	v_and_b32_e32 v10, 0xff0000, v10
	v_perm_b32 v6, v11, v6, s1
	v_or3_b32 v10, v6, v7, v10
	v_mbcnt_lo_u32_b32 v6, -1, 0
	v_mbcnt_hi_u32_b32 v6, -1, v6
	v_mul_f32_e32 v11, v41, v1
	v_ashrrev_i32_e32 v7, 31, v6
	v_lshl_add_u64 v[6:7], v[6:7], 2, s[6:7]
	global_store_dword v[6:7], v10, off offset:1024
	v_mul_f32_e32 v7, v43, v1
	v_mul_f32_e32 v6, v42, v1
	v_rndne_f32_e32 v7, v7
	v_mul_f32_e32 v10, v40, v1
	v_rndne_f32_e32 v6, v6
	v_cvt_i32_f32_e32 v7, v7
	v_rndne_f32_e32 v10, v10
	v_rndne_f32_e32 v11, v11
	v_cvt_i32_f32_e32 v6, v6
	v_cvt_i32_f32_sdwa v10, v10 dst_sel:WORD_1 dst_unused:UNUSED_PAD src0_sel:DWORD
	v_cvt_i32_f32_e32 v11, v11
	v_lshlrev_b32_e32 v7, 8, v7
	v_and_b32_e32 v7, 0xff00, v7
	v_and_b32_e32 v10, 0xff0000, v10
	v_perm_b32 v6, v11, v6, s1
	v_or3_b32 v10, v6, v7, v10
	v_mbcnt_lo_u32_b32 v6, -1, 0
	v_mbcnt_hi_u32_b32 v6, -1, v6
	v_mul_f32_e32 v11, v45, v1
	v_ashrrev_i32_e32 v7, 31, v6
	v_lshl_add_u64 v[6:7], v[6:7], 2, s[6:7]
	global_store_dword v[6:7], v10, off offset:1280
	v_mul_f32_e32 v7, v47, v1
	v_mul_f32_e32 v6, v46, v1
	v_rndne_f32_e32 v7, v7
	v_mul_f32_e32 v10, v44, v1
	v_rndne_f32_e32 v6, v6
	v_cvt_i32_f32_e32 v7, v7
	v_rndne_f32_e32 v10, v10
	v_rndne_f32_e32 v11, v11
	v_mul_f32_e32 v5, v5, v1
	v_cvt_i32_f32_e32 v6, v6
	v_cvt_i32_f32_sdwa v10, v10 dst_sel:WORD_1 dst_unused:UNUSED_PAD src0_sel:DWORD
	v_cvt_i32_f32_e32 v11, v11
	v_mul_f32_e32 v4, v4, v1
	v_rndne_f32_e32 v5, v5
	v_mul_f32_e32 v2, v2, v1
	v_mul_f32_e32 v1, v3, v1
	v_rndne_f32_e32 v4, v4
	v_cvt_i32_f32_e32 v5, v5
	v_rndne_f32_e32 v2, v2
	v_rndne_f32_e32 v1, v1
	v_cvt_i32_f32_e32 v4, v4
	v_cvt_i32_f32_sdwa v2, v2 dst_sel:WORD_1 dst_unused:UNUSED_PAD src0_sel:DWORD
	v_cvt_i32_f32_e32 v1, v1
	v_lshlrev_b32_e32 v7, 8, v7
	v_and_b32_e32 v7, 0xff00, v7
	v_and_b32_e32 v10, 0xff0000, v10
	v_perm_b32 v6, v11, v6, s1
	v_or3_b32 v10, v6, v7, v10
	v_mbcnt_lo_u32_b32 v6, -1, 0
	v_mbcnt_hi_u32_b32 v6, -1, v6
	v_lshlrev_b32_e32 v3, 8, v5
	v_ashrrev_i32_e32 v7, 31, v6
	v_lshl_add_u64 v[6:7], v[6:7], 2, s[6:7]
	v_and_b32_e32 v3, 0xff00, v3
	v_and_b32_e32 v2, 0xff0000, v2
	v_perm_b32 v1, v1, v4, s1
	global_store_dword v[6:7], v10, off offset:1536
	v_or3_b32 v1, v1, v3, v2
	v_mbcnt_lo_u32_b32 v2, -1, 0
	v_mbcnt_hi_u32_b32 v2, -1, v2
	s_nop 0
	v_ashrrev_i32_e32 v3, 31, v2
	v_lshl_add_u64 v[2:3], v[2:3], 2, s[6:7]
	global_store_dword v[2:3], v1, off offset:1792
	v_mbcnt_lo_u32_b32 v1, -1, 0
	v_mbcnt_hi_u32_b32 v1, -1, v1
	s_nop 0
	v_cmp_eq_u32_e32 vcc, 0, v1
	s_and_saveexec_b64 s[6:7], vcc
	s_cbranch_execz .LBB0_1497
	s_lshl_b32 s8, s4, 1
	s_ashr_i32 s9, s8, 31
	s_lshl_b64 s[8:9], s[8:9], 2
	s_add_u32 s8, s27, s8
	s_addc_u32 s9, s64, s9
	v_readlane_b32 s0, v255, 49
	s_lshl_b64 s[4:5], s[4:5], 2
	v_mul_f32_e32 v2, 0x3a000000, v9
	v_mov_b32_e32 v3, v8
	v_mov_b32_e32 v1, s0
	s_add_u32 s4, s25, s4
	v_readlane_b32 s0, v255, 38
	ds_write_b64 v1, v[2:3]
	s_addc_u32 s5, s26, s5
	v_mov_b32_e32 v1, s0
	global_store_dwordx2 v33, v[2:3], s[8:9]
	global_store_dword v33, v0, s[4:5]
	ds_write_b32 v1, v0
